# every back-to-back v_mfma_f32_16x16x32_bf16 cluster of the GEMM K-loops put on an 8-byte boundary (one s_nop 0 in front of a cluster where needed)
# baseline (speedup 1.0000x reference)
.LBB0_188:
	s_ashr_i32 s21, s20, 31
	s_lshl_b64 s[22:23], s[20:21], 20
	s_add_u32 s22, s31, s22
	s_addc_u32 s23, s34, s23
	s_and_b64 s[24:25], s[2:3], exec
	s_cselect_b32 s5, s23, s29
	s_cselect_b32 s7, s22, s28
	s_ashr_i32 s19, s18, 31
	s_lshl_b64 s[24:25], s[18:19], 20
	s_add_u32 s24, s35, s24
	s_addc_u32 s25, s36, s25
	s_and_b64 s[26:27], s[2:3], exec
	s_cselect_b32 s19, s25, s9
	s_cselect_b32 s21, s24, s8
	s_add_u32 s59, s8, 0x100
	s_addc_u32 s60, s9, 0
	s_add_u32 s8, s28, 0x80080
	v_mov_b32_e32 v0, 0
	s_addc_u32 s9, s29, 0
	s_mov_b32 s61, -2
	s_cmp_eq_u32 s56, 1
	s_cbranch_scc1 .Lpeel_zero_P1
	v_add_u32_e32 v140, s37, v193
	v_add_u32_e32 v160, s40, v193
	ds_read_b128 v[128:131], v140
	ds_read_b128 v[132:135], v140 offset:1024
	ds_read_b128 v[136:139], v140 offset:2048
	ds_read_b128 v[140:143], v140 offset:3072
	ds_read_b128 v[144:147], v160
	ds_read_b128 v[148:151], v160 offset:1024
	ds_read_b128 v[176:179], v160 offset:2048
	ds_read_b128 v[180:183], v160 offset:3072
	s_add_u32 s26, s8, 0xfff80080
	s_addc_u32 s27, s9, -1
	s_cmp_eq_u32 s61, 28
	s_cselect_b32 s29, s5, s27
	s_cselect_b32 s28, s7, s26
	s_cselect_b32 s27, s19, s60
	s_cselect_b32 s26, s21, s59
	v_lshl_add_u64 v[162:163], s[8:9], 0, v[174:175]
	s_add_i32 m0, s43, 0xc000
	ds_read_b128 v[184:187], v199
	ds_read_b128 v[188:191], v199 offset:1024
	ds_read_b128 v[200:203], v199 offset:2048
	ds_read_b128 v[204:207], v199 offset:3072
	ds_read_b128 v[208:211], v199 offset:4096
	ds_read_b128 v[212:215], v199 offset:5120
	ds_read_b128 v[216:219], v199 offset:6144
	ds_read_b128 v[230:233], v199 offset:7168
	global_load_lds_dwordx4 v[162:163], off
	v_lshl_add_u64 v[162:163], s[8:9], 0, v[172:173]
	s_add_i32 m0, s43, 0xe000
	s_nop 0
	global_load_lds_dwordx4 v[162:163], off
	s_waitcnt vmcnt(16)
	s_waitcnt lgkmcnt(0)
	s_barrier
	s_setprio 1
	s_waitcnt lgkmcnt(0)
	s_nop 0
	v_mfma_f32_16x16x32_bf16 v[124:127], v[128:131], v[184:187], 0
	v_mfma_f32_16x16x32_bf16 v[120:123], v[136:139], v[184:187], 0
	v_mfma_f32_16x16x32_bf16 v[108:111], v[128:131], v[200:203], 0
	v_mfma_f32_16x16x32_bf16 v[104:107], v[136:139], v[200:203], 0
	v_mfma_f32_16x16x32_bf16 v[92:95], v[128:131], v[208:211], 0
	v_mfma_f32_16x16x32_bf16 v[88:91], v[136:139], v[208:211], 0
	v_mfma_f32_16x16x32_bf16 v[76:79], v[128:131], v[216:219], 0
	v_mfma_f32_16x16x32_bf16 v[72:75], v[136:139], v[216:219], 0
	v_mfma_f32_16x16x32_bf16 v[124:127], v[132:135], v[188:191], v[124:127]
	v_mfma_f32_16x16x32_bf16 v[120:123], v[140:143], v[188:191], v[120:123]
	v_mfma_f32_16x16x32_bf16 v[108:111], v[132:135], v[204:207], v[108:111]
	v_mfma_f32_16x16x32_bf16 v[104:107], v[140:143], v[204:207], v[104:107]
	v_mfma_f32_16x16x32_bf16 v[92:95], v[132:135], v[212:215], v[92:95]
	v_mfma_f32_16x16x32_bf16 v[88:91], v[140:143], v[212:215], v[88:91]
	v_mfma_f32_16x16x32_bf16 v[76:79], v[132:135], v[230:233], v[76:79]
	v_mfma_f32_16x16x32_bf16 v[72:75], v[140:143], v[230:233], v[72:75]
	s_setprio 0
	s_setprio 1
	v_mfma_f32_16x16x32_bf16 v[116:119], v[144:147], v[184:187], 0
	v_mfma_f32_16x16x32_bf16 v[112:115], v[176:179], v[184:187], 0
	v_mfma_f32_16x16x32_bf16 v[100:103], v[144:147], v[200:203], 0
	v_mfma_f32_16x16x32_bf16 v[96:99], v[176:179], v[200:203], 0
	v_mfma_f32_16x16x32_bf16 v[84:87], v[144:147], v[208:211], 0
	v_mfma_f32_16x16x32_bf16 v[80:83], v[176:179], v[208:211], 0
	v_mfma_f32_16x16x32_bf16 v[68:71], v[144:147], v[216:219], 0
	v_mfma_f32_16x16x32_bf16 v[64:67], v[176:179], v[216:219], 0
	v_mfma_f32_16x16x32_bf16 v[116:119], v[148:151], v[188:191], v[116:119]
	v_mfma_f32_16x16x32_bf16 v[112:115], v[180:183], v[188:191], v[112:115]
	v_mfma_f32_16x16x32_bf16 v[100:103], v[148:151], v[204:207], v[100:103]
	v_mfma_f32_16x16x32_bf16 v[96:99], v[180:183], v[204:207], v[96:99]
	v_mfma_f32_16x16x32_bf16 v[84:87], v[148:151], v[212:215], v[84:87]
	v_mfma_f32_16x16x32_bf16 v[80:83], v[180:183], v[212:215], v[80:83]
	v_mfma_f32_16x16x32_bf16 v[68:71], v[148:151], v[230:233], v[68:71]
	v_mfma_f32_16x16x32_bf16 v[64:67], v[180:183], v[230:233], v[64:67]
	s_setprio 0
	s_barrier
	s_mov_b32 m0, s38
	v_lshl_add_u64 v[162:163], s[26:27], 0, v[154:155]
	s_add_u32 s62, s26, 0x80000
	ds_read_b128 v[184:187], v199 offset:16384
	ds_read_b128 v[188:191], v199 offset:17408
	ds_read_b128 v[200:203], v199 offset:18432
	ds_read_b128 v[204:207], v199 offset:19456
	ds_read_b128 v[208:211], v199 offset:20480
	ds_read_b128 v[212:215], v199 offset:21504
	ds_read_b128 v[216:219], v199 offset:22528
	ds_read_b128 v[230:233], v199 offset:23552
	global_load_lds_dwordx4 v[162:163], off
	v_lshl_add_u64 v[166:167], s[26:27], 0, v[158:159]
	s_mov_b32 m0, s39
	s_addc_u32 s63, s27, 0
	global_load_lds_dwordx4 v[166:167], off
	v_lshl_add_u64 v[194:195], s[62:63], 0, v[154:155]
	s_mov_b32 m0, s41
	v_lshl_add_u64 v[196:197], s[28:29], 0, v[156:157]
	global_load_lds_dwordx4 v[194:195], off
	v_lshl_add_u64 v[194:195], s[62:63], 0, v[158:159]
	s_mov_b32 m0, s42
	s_nop 0
	global_load_lds_dwordx4 v[194:195], off
	v_lshl_add_u64 v[194:195], s[28:29], 0, v[152:153]
	s_mov_b32 m0, s43
	s_nop 0
	global_load_lds_dwordx4 v[194:195], off
	s_mov_b32 m0, s44
	s_nop 0
	global_load_lds_dwordx4 v[196:197], off
	s_waitcnt vmcnt(16)
	s_waitcnt lgkmcnt(0)
	s_barrier
	s_setprio 1
	s_waitcnt lgkmcnt(0)
	s_nop 0
	v_mfma_f32_16x16x32_bf16 v[60:63], v[128:131], v[184:187], 0
	v_mfma_f32_16x16x32_bf16 v[56:59], v[136:139], v[184:187], 0
	v_mfma_f32_16x16x32_bf16 v[44:47], v[128:131], v[200:203], 0
	v_mfma_f32_16x16x32_bf16 v[40:43], v[136:139], v[200:203], 0
	v_mfma_f32_16x16x32_bf16 v[28:31], v[128:131], v[208:211], 0
	v_mfma_f32_16x16x32_bf16 v[24:27], v[136:139], v[208:211], 0
	v_mfma_f32_16x16x32_bf16 v[12:15], v[128:131], v[216:219], 0
	v_mfma_f32_16x16x32_bf16 v[8:11], v[136:139], v[216:219], 0
	v_mfma_f32_16x16x32_bf16 v[60:63], v[132:135], v[188:191], v[60:63]
	v_mfma_f32_16x16x32_bf16 v[56:59], v[140:143], v[188:191], v[56:59]
	v_mfma_f32_16x16x32_bf16 v[44:47], v[132:135], v[204:207], v[44:47]
	v_mfma_f32_16x16x32_bf16 v[40:43], v[140:143], v[204:207], v[40:43]
	v_mfma_f32_16x16x32_bf16 v[28:31], v[132:135], v[212:215], v[28:31]
	v_mfma_f32_16x16x32_bf16 v[24:27], v[140:143], v[212:215], v[24:27]
	v_mfma_f32_16x16x32_bf16 v[12:15], v[132:135], v[230:233], v[12:15]
	v_mfma_f32_16x16x32_bf16 v[8:11], v[140:143], v[230:233], v[8:11]
	s_setprio 0
	s_setprio 1
	v_mfma_f32_16x16x32_bf16 v[52:55], v[144:147], v[184:187], 0
	v_mfma_f32_16x16x32_bf16 v[48:51], v[176:179], v[184:187], 0
	v_mfma_f32_16x16x32_bf16 v[36:39], v[144:147], v[200:203], 0
	v_mfma_f32_16x16x32_bf16 v[32:35], v[176:179], v[200:203], 0
	v_mfma_f32_16x16x32_bf16 v[20:23], v[144:147], v[208:211], 0
	v_mfma_f32_16x16x32_bf16 v[16:19], v[176:179], v[208:211], 0
	v_mfma_f32_16x16x32_bf16 v[4:7], v[144:147], v[216:219], 0
	v_mfma_f32_16x16x32_bf16 v[0:3], v[176:179], v[216:219], 0
	v_mfma_f32_16x16x32_bf16 v[52:55], v[148:151], v[188:191], v[52:55]
	v_mfma_f32_16x16x32_bf16 v[48:51], v[180:183], v[188:191], v[48:51]
	v_mfma_f32_16x16x32_bf16 v[36:39], v[148:151], v[204:207], v[36:39]
	v_mfma_f32_16x16x32_bf16 v[32:35], v[180:183], v[204:207], v[32:35]
	v_mfma_f32_16x16x32_bf16 v[20:23], v[148:151], v[212:215], v[20:23]
	v_mfma_f32_16x16x32_bf16 v[16:19], v[180:183], v[212:215], v[16:19]
	v_mfma_f32_16x16x32_bf16 v[4:7], v[148:151], v[230:233], v[4:7]
	v_mfma_f32_16x16x32_bf16 v[0:3], v[180:183], v[230:233], v[0:3]
	s_setprio 0
	s_barrier
	v_add_u32_e32 v140, s48, v193
	v_add_u32_e32 v160, s53, v193
	ds_read_b128 v[128:131], v140
	ds_read_b128 v[132:135], v140 offset:1024
	ds_read_b128 v[136:139], v140 offset:2048
	ds_read_b128 v[140:143], v140 offset:3072
	ds_read_b128 v[144:147], v160
	ds_read_b128 v[148:151], v160 offset:1024
	ds_read_b128 v[176:179], v160 offset:2048
	ds_read_b128 v[180:183], v160 offset:3072
	s_add_u32 s28, s28, 0x80000
	s_addc_u32 s29, s29, 0
	s_mov_b32 m0, s45
	v_lshl_add_u64 v[220:221], s[28:29], 0, v[152:153]
	ds_read_b128 v[184:187], v199 offset:32768
	ds_read_b128 v[188:191], v199 offset:33792
	ds_read_b128 v[200:203], v199 offset:34816
	ds_read_b128 v[204:207], v199 offset:35840
	ds_read_b128 v[208:211], v199 offset:36864
	ds_read_b128 v[212:215], v199 offset:37888
	ds_read_b128 v[216:219], v199 offset:38912
	ds_read_b128 v[230:233], v199 offset:39936
	global_load_lds_dwordx4 v[220:221], off
	v_lshl_add_u64 v[220:221], s[28:29], 0, v[156:157]
	s_mov_b32 m0, s47
	s_nop 0
	global_load_lds_dwordx4 v[220:221], off
	s_waitcnt vmcnt(8)
	s_waitcnt lgkmcnt(0)
	s_barrier
	s_setprio 1
	s_waitcnt lgkmcnt(0)
	s_nop 0
	v_mfma_f32_16x16x32_bf16 v[124:127], v[128:131], v[184:187], v[124:127]
	v_mfma_f32_16x16x32_bf16 v[120:123], v[136:139], v[184:187], v[120:123]
	v_mfma_f32_16x16x32_bf16 v[108:111], v[128:131], v[200:203], v[108:111]
	v_mfma_f32_16x16x32_bf16 v[104:107], v[136:139], v[200:203], v[104:107]
	v_mfma_f32_16x16x32_bf16 v[92:95], v[128:131], v[208:211], v[92:95]
	v_mfma_f32_16x16x32_bf16 v[88:91], v[136:139], v[208:211], v[88:91]
	v_mfma_f32_16x16x32_bf16 v[76:79], v[128:131], v[216:219], v[76:79]
	v_mfma_f32_16x16x32_bf16 v[72:75], v[136:139], v[216:219], v[72:75]
	v_mfma_f32_16x16x32_bf16 v[124:127], v[132:135], v[188:191], v[124:127]
	v_mfma_f32_16x16x32_bf16 v[120:123], v[140:143], v[188:191], v[120:123]
	v_mfma_f32_16x16x32_bf16 v[108:111], v[132:135], v[204:207], v[108:111]
	v_mfma_f32_16x16x32_bf16 v[104:107], v[140:143], v[204:207], v[104:107]
	v_mfma_f32_16x16x32_bf16 v[92:95], v[132:135], v[212:215], v[92:95]
	v_mfma_f32_16x16x32_bf16 v[88:91], v[140:143], v[212:215], v[88:91]
	v_mfma_f32_16x16x32_bf16 v[76:79], v[132:135], v[230:233], v[76:79]
	v_mfma_f32_16x16x32_bf16 v[72:75], v[140:143], v[230:233], v[72:75]
	s_setprio 0
	s_setprio 1
	v_mfma_f32_16x16x32_bf16 v[116:119], v[144:147], v[184:187], v[116:119]
	v_mfma_f32_16x16x32_bf16 v[112:115], v[176:179], v[184:187], v[112:115]
	v_mfma_f32_16x16x32_bf16 v[100:103], v[144:147], v[200:203], v[100:103]
	v_mfma_f32_16x16x32_bf16 v[96:99], v[176:179], v[200:203], v[96:99]
	v_mfma_f32_16x16x32_bf16 v[84:87], v[144:147], v[208:211], v[84:87]
	v_mfma_f32_16x16x32_bf16 v[80:83], v[176:179], v[208:211], v[80:83]
	v_mfma_f32_16x16x32_bf16 v[68:71], v[144:147], v[216:219], v[68:71]
	v_mfma_f32_16x16x32_bf16 v[64:67], v[176:179], v[216:219], v[64:67]
	v_mfma_f32_16x16x32_bf16 v[116:119], v[148:151], v[188:191], v[116:119]
	v_mfma_f32_16x16x32_bf16 v[112:115], v[180:183], v[188:191], v[112:115]
	v_mfma_f32_16x16x32_bf16 v[100:103], v[148:151], v[204:207], v[100:103]
	v_mfma_f32_16x16x32_bf16 v[96:99], v[180:183], v[204:207], v[96:99]
	v_mfma_f32_16x16x32_bf16 v[84:87], v[148:151], v[212:215], v[84:87]
	v_mfma_f32_16x16x32_bf16 v[80:83], v[180:183], v[212:215], v[80:83]
	v_mfma_f32_16x16x32_bf16 v[68:71], v[148:151], v[230:233], v[68:71]
	v_mfma_f32_16x16x32_bf16 v[64:67], v[180:183], v[230:233], v[64:67]
	s_setprio 0
	s_barrier
	s_mov_b32 m0, s49
	v_lshl_add_u64 v[162:163], v[162:163], 0, s[86:87]
	s_add_u32 s26, s26, 0x80080
	ds_read_b128 v[184:187], v199 offset:49152
	ds_read_b128 v[188:191], v199 offset:50176
	ds_read_b128 v[200:203], v199 offset:51200
	ds_read_b128 v[204:207], v199 offset:52224
	ds_read_b128 v[208:211], v199 offset:53248
	ds_read_b128 v[212:215], v199 offset:54272
	ds_read_b128 v[216:219], v199 offset:55296
	ds_read_b128 v[230:233], v199 offset:56320
	global_load_lds_dwordx4 v[162:163], off
	v_lshl_add_u64 v[162:163], v[166:167], 0, s[86:87]
	s_mov_b32 m0, s50
	s_addc_u32 s27, s27, 0
	global_load_lds_dwordx4 v[162:163], off
	v_lshl_add_u64 v[162:163], s[26:27], 0, v[154:155]
	s_mov_b32 m0, s54
	s_nop 0
	global_load_lds_dwordx4 v[162:163], off
	v_lshl_add_u64 v[162:163], s[26:27], 0, v[158:159]
	s_mov_b32 m0, s55
	s_nop 0
	global_load_lds_dwordx4 v[162:163], off
	v_lshl_add_u64 v[162:163], v[194:195], 0, s[86:87]
	s_mov_b32 m0, s51
	s_nop 0
	global_load_lds_dwordx4 v[162:163], off
	v_lshl_add_u64 v[162:163], v[196:197], 0, s[86:87]
	s_mov_b32 m0, s52
	s_nop 0
	global_load_lds_dwordx4 v[162:163], off
	s_waitcnt vmcnt(8)
	s_waitcnt lgkmcnt(0)
	s_barrier
	s_setprio 1
	s_waitcnt lgkmcnt(0)
	v_mfma_f32_16x16x32_bf16 v[60:63], v[128:131], v[184:187], v[60:63]
	v_mfma_f32_16x16x32_bf16 v[56:59], v[136:139], v[184:187], v[56:59]
	v_mfma_f32_16x16x32_bf16 v[44:47], v[128:131], v[200:203], v[44:47]
	v_mfma_f32_16x16x32_bf16 v[40:43], v[136:139], v[200:203], v[40:43]
	v_mfma_f32_16x16x32_bf16 v[28:31], v[128:131], v[208:211], v[28:31]
	v_mfma_f32_16x16x32_bf16 v[24:27], v[136:139], v[208:211], v[24:27]
	v_mfma_f32_16x16x32_bf16 v[12:15], v[128:131], v[216:219], v[12:15]
	v_mfma_f32_16x16x32_bf16 v[8:11], v[136:139], v[216:219], v[8:11]
	v_mfma_f32_16x16x32_bf16 v[60:63], v[132:135], v[188:191], v[60:63]
	v_mfma_f32_16x16x32_bf16 v[56:59], v[140:143], v[188:191], v[56:59]
	v_mfma_f32_16x16x32_bf16 v[44:47], v[132:135], v[204:207], v[44:47]
	v_mfma_f32_16x16x32_bf16 v[40:43], v[140:143], v[204:207], v[40:43]
	v_mfma_f32_16x16x32_bf16 v[28:31], v[132:135], v[212:215], v[28:31]
	v_mfma_f32_16x16x32_bf16 v[24:27], v[140:143], v[212:215], v[24:27]
	v_mfma_f32_16x16x32_bf16 v[12:15], v[132:135], v[230:233], v[12:15]
	v_mfma_f32_16x16x32_bf16 v[8:11], v[140:143], v[230:233], v[8:11]
	s_setprio 0
	s_setprio 1
	v_mfma_f32_16x16x32_bf16 v[52:55], v[144:147], v[184:187], v[52:55]
	v_mfma_f32_16x16x32_bf16 v[48:51], v[176:179], v[184:187], v[48:51]
	v_mfma_f32_16x16x32_bf16 v[36:39], v[144:147], v[200:203], v[36:39]
	v_mfma_f32_16x16x32_bf16 v[32:35], v[176:179], v[200:203], v[32:35]
	v_mfma_f32_16x16x32_bf16 v[20:23], v[144:147], v[208:211], v[20:23]
	v_mfma_f32_16x16x32_bf16 v[16:19], v[176:179], v[208:211], v[16:19]
	v_mfma_f32_16x16x32_bf16 v[4:7], v[144:147], v[216:219], v[4:7]
	v_mfma_f32_16x16x32_bf16 v[0:3], v[176:179], v[216:219], v[0:3]
	v_mfma_f32_16x16x32_bf16 v[52:55], v[148:151], v[188:191], v[52:55]
	v_mfma_f32_16x16x32_bf16 v[48:51], v[180:183], v[188:191], v[48:51]
	v_mfma_f32_16x16x32_bf16 v[36:39], v[148:151], v[204:207], v[36:39]
	v_mfma_f32_16x16x32_bf16 v[32:35], v[180:183], v[204:207], v[32:35]
	v_mfma_f32_16x16x32_bf16 v[20:23], v[148:151], v[212:215], v[20:23]
	v_mfma_f32_16x16x32_bf16 v[16:19], v[180:183], v[212:215], v[16:19]
	v_mfma_f32_16x16x32_bf16 v[4:7], v[148:151], v[230:233], v[4:7]
	v_mfma_f32_16x16x32_bf16 v[0:3], v[180:183], v[230:233], v[0:3]
	s_setprio 0
	s_barrier
	s_add_i32 s61, s61, 2
	s_add_u32 s59, s59, 0x100
	s_addc_u32 s60, s60, 0
	s_add_u32 s8, s8, 0x100
	s_addc_u32 s9, s9, 0
	s_branch .LBB0_189

.LBB0_189:
	v_add_u32_e32 v140, s37, v193
	v_add_u32_e32 v160, s40, v193
	ds_read_b128 v[128:131], v140
	ds_read_b128 v[132:135], v140 offset:1024
	ds_read_b128 v[136:139], v140 offset:2048
	ds_read_b128 v[140:143], v140 offset:3072
	ds_read_b128 v[144:147], v160
	ds_read_b128 v[148:151], v160 offset:1024
	ds_read_b128 v[176:179], v160 offset:2048
	ds_read_b128 v[180:183], v160 offset:3072
	s_add_u32 s26, s8, 0xfff80080
	s_addc_u32 s27, s9, -1
	s_cmp_eq_u32 s61, 28
	s_cselect_b32 s29, s5, s27
	s_cselect_b32 s28, s7, s26
	s_cselect_b32 s27, s19, s60
	s_cselect_b32 s26, s21, s59
	v_lshl_add_u64 v[162:163], s[8:9], 0, v[174:175]
	s_add_i32 m0, s43, 0xc000
	ds_read_b128 v[184:187], v199
	ds_read_b128 v[188:191], v199 offset:1024
	ds_read_b128 v[200:203], v199 offset:2048
	ds_read_b128 v[204:207], v199 offset:3072
	ds_read_b128 v[208:211], v199 offset:4096
	ds_read_b128 v[212:215], v199 offset:5120
	ds_read_b128 v[216:219], v199 offset:6144
	ds_read_b128 v[230:233], v199 offset:7168
	global_load_lds_dwordx4 v[162:163], off
	v_lshl_add_u64 v[162:163], s[8:9], 0, v[172:173]
	s_add_i32 m0, s43, 0xe000
	s_nop 0
	global_load_lds_dwordx4 v[162:163], off
	s_waitcnt vmcnt(8)
	s_waitcnt lgkmcnt(0)
	s_barrier
	s_setprio 1
	s_waitcnt lgkmcnt(0)
	s_nop 0
	v_mfma_f32_16x16x32_bf16 v[124:127], v[128:131], v[184:187], v[124:127]
	v_mfma_f32_16x16x32_bf16 v[120:123], v[136:139], v[184:187], v[120:123]
	v_mfma_f32_16x16x32_bf16 v[108:111], v[128:131], v[200:203], v[108:111]
	v_mfma_f32_16x16x32_bf16 v[104:107], v[136:139], v[200:203], v[104:107]
	v_mfma_f32_16x16x32_bf16 v[92:95], v[128:131], v[208:211], v[92:95]
	v_mfma_f32_16x16x32_bf16 v[88:91], v[136:139], v[208:211], v[88:91]
	v_mfma_f32_16x16x32_bf16 v[76:79], v[128:131], v[216:219], v[76:79]
	v_mfma_f32_16x16x32_bf16 v[72:75], v[136:139], v[216:219], v[72:75]
	v_mfma_f32_16x16x32_bf16 v[124:127], v[132:135], v[188:191], v[124:127]
	v_mfma_f32_16x16x32_bf16 v[120:123], v[140:143], v[188:191], v[120:123]
	v_mfma_f32_16x16x32_bf16 v[108:111], v[132:135], v[204:207], v[108:111]
	v_mfma_f32_16x16x32_bf16 v[104:107], v[140:143], v[204:207], v[104:107]
	v_mfma_f32_16x16x32_bf16 v[92:95], v[132:135], v[212:215], v[92:95]
	v_mfma_f32_16x16x32_bf16 v[88:91], v[140:143], v[212:215], v[88:91]
	v_mfma_f32_16x16x32_bf16 v[76:79], v[132:135], v[230:233], v[76:79]
	v_mfma_f32_16x16x32_bf16 v[72:75], v[140:143], v[230:233], v[72:75]
	s_setprio 0
	s_setprio 1
	v_mfma_f32_16x16x32_bf16 v[116:119], v[144:147], v[184:187], v[116:119]
	v_mfma_f32_16x16x32_bf16 v[112:115], v[176:179], v[184:187], v[112:115]
	v_mfma_f32_16x16x32_bf16 v[100:103], v[144:147], v[200:203], v[100:103]
	v_mfma_f32_16x16x32_bf16 v[96:99], v[176:179], v[200:203], v[96:99]
	v_mfma_f32_16x16x32_bf16 v[84:87], v[144:147], v[208:211], v[84:87]
	v_mfma_f32_16x16x32_bf16 v[80:83], v[176:179], v[208:211], v[80:83]
	v_mfma_f32_16x16x32_bf16 v[68:71], v[144:147], v[216:219], v[68:71]
	v_mfma_f32_16x16x32_bf16 v[64:67], v[176:179], v[216:219], v[64:67]
	v_mfma_f32_16x16x32_bf16 v[116:119], v[148:151], v[188:191], v[116:119]
	v_mfma_f32_16x16x32_bf16 v[112:115], v[180:183], v[188:191], v[112:115]
	v_mfma_f32_16x16x32_bf16 v[100:103], v[148:151], v[204:207], v[100:103]
	v_mfma_f32_16x16x32_bf16 v[96:99], v[180:183], v[204:207], v[96:99]
	v_mfma_f32_16x16x32_bf16 v[84:87], v[148:151], v[212:215], v[84:87]
	v_mfma_f32_16x16x32_bf16 v[80:83], v[180:183], v[212:215], v[80:83]
	v_mfma_f32_16x16x32_bf16 v[68:71], v[148:151], v[230:233], v[68:71]
	v_mfma_f32_16x16x32_bf16 v[64:67], v[180:183], v[230:233], v[64:67]
	s_setprio 0
	s_barrier
	s_mov_b32 m0, s38
	v_lshl_add_u64 v[162:163], s[26:27], 0, v[154:155]
	s_add_u32 s62, s26, 0x80000
	ds_read_b128 v[184:187], v199 offset:16384
	ds_read_b128 v[188:191], v199 offset:17408
	ds_read_b128 v[200:203], v199 offset:18432
	ds_read_b128 v[204:207], v199 offset:19456
	ds_read_b128 v[208:211], v199 offset:20480
	ds_read_b128 v[212:215], v199 offset:21504
	ds_read_b128 v[216:219], v199 offset:22528
	ds_read_b128 v[230:233], v199 offset:23552
	global_load_lds_dwordx4 v[162:163], off
	v_lshl_add_u64 v[166:167], s[26:27], 0, v[158:159]
	s_mov_b32 m0, s39
	s_addc_u32 s63, s27, 0
	global_load_lds_dwordx4 v[166:167], off
	v_lshl_add_u64 v[194:195], s[62:63], 0, v[154:155]
	s_mov_b32 m0, s41
	v_lshl_add_u64 v[196:197], s[28:29], 0, v[156:157]
	global_load_lds_dwordx4 v[194:195], off
	v_lshl_add_u64 v[194:195], s[62:63], 0, v[158:159]
	s_mov_b32 m0, s42
	s_nop 0
	global_load_lds_dwordx4 v[194:195], off
	v_lshl_add_u64 v[194:195], s[28:29], 0, v[152:153]
	s_mov_b32 m0, s43
	s_nop 0
	global_load_lds_dwordx4 v[194:195], off
	s_mov_b32 m0, s44
	s_nop 0
	global_load_lds_dwordx4 v[196:197], off
	s_waitcnt vmcnt(8)
	s_waitcnt lgkmcnt(0)
	s_barrier
	s_setprio 1
	s_waitcnt lgkmcnt(0)
	s_nop 0
	v_mfma_f32_16x16x32_bf16 v[60:63], v[128:131], v[184:187], v[60:63]
	v_mfma_f32_16x16x32_bf16 v[56:59], v[136:139], v[184:187], v[56:59]
	v_mfma_f32_16x16x32_bf16 v[44:47], v[128:131], v[200:203], v[44:47]
	v_mfma_f32_16x16x32_bf16 v[40:43], v[136:139], v[200:203], v[40:43]
	v_mfma_f32_16x16x32_bf16 v[28:31], v[128:131], v[208:211], v[28:31]
	v_mfma_f32_16x16x32_bf16 v[24:27], v[136:139], v[208:211], v[24:27]
	v_mfma_f32_16x16x32_bf16 v[12:15], v[128:131], v[216:219], v[12:15]
	v_mfma_f32_16x16x32_bf16 v[8:11], v[136:139], v[216:219], v[8:11]
	v_mfma_f32_16x16x32_bf16 v[60:63], v[132:135], v[188:191], v[60:63]
	v_mfma_f32_16x16x32_bf16 v[56:59], v[140:143], v[188:191], v[56:59]
	v_mfma_f32_16x16x32_bf16 v[44:47], v[132:135], v[204:207], v[44:47]
	v_mfma_f32_16x16x32_bf16 v[40:43], v[140:143], v[204:207], v[40:43]
	v_mfma_f32_16x16x32_bf16 v[28:31], v[132:135], v[212:215], v[28:31]
	v_mfma_f32_16x16x32_bf16 v[24:27], v[140:143], v[212:215], v[24:27]
	v_mfma_f32_16x16x32_bf16 v[12:15], v[132:135], v[230:233], v[12:15]
	v_mfma_f32_16x16x32_bf16 v[8:11], v[140:143], v[230:233], v[8:11]
	s_setprio 0
	s_setprio 1
	v_mfma_f32_16x16x32_bf16 v[52:55], v[144:147], v[184:187], v[52:55]
	v_mfma_f32_16x16x32_bf16 v[48:51], v[176:179], v[184:187], v[48:51]
	v_mfma_f32_16x16x32_bf16 v[36:39], v[144:147], v[200:203], v[36:39]
	v_mfma_f32_16x16x32_bf16 v[32:35], v[176:179], v[200:203], v[32:35]
	v_mfma_f32_16x16x32_bf16 v[20:23], v[144:147], v[208:211], v[20:23]
	v_mfma_f32_16x16x32_bf16 v[16:19], v[176:179], v[208:211], v[16:19]
	v_mfma_f32_16x16x32_bf16 v[4:7], v[144:147], v[216:219], v[4:7]
	v_mfma_f32_16x16x32_bf16 v[0:3], v[176:179], v[216:219], v[0:3]
	v_mfma_f32_16x16x32_bf16 v[52:55], v[148:151], v[188:191], v[52:55]
	v_mfma_f32_16x16x32_bf16 v[48:51], v[180:183], v[188:191], v[48:51]
	v_mfma_f32_16x16x32_bf16 v[36:39], v[148:151], v[204:207], v[36:39]
	v_mfma_f32_16x16x32_bf16 v[32:35], v[180:183], v[204:207], v[32:35]
	v_mfma_f32_16x16x32_bf16 v[20:23], v[148:151], v[212:215], v[20:23]
	v_mfma_f32_16x16x32_bf16 v[16:19], v[180:183], v[212:215], v[16:19]
	v_mfma_f32_16x16x32_bf16 v[4:7], v[148:151], v[230:233], v[4:7]
	v_mfma_f32_16x16x32_bf16 v[0:3], v[180:183], v[230:233], v[0:3]
	s_setprio 0
	s_barrier
	v_add_u32_e32 v140, s48, v193
	v_add_u32_e32 v160, s53, v193
	ds_read_b128 v[128:131], v140
	ds_read_b128 v[132:135], v140 offset:1024
	ds_read_b128 v[136:139], v140 offset:2048
	ds_read_b128 v[140:143], v140 offset:3072
	ds_read_b128 v[144:147], v160
	ds_read_b128 v[148:151], v160 offset:1024
	ds_read_b128 v[176:179], v160 offset:2048
	ds_read_b128 v[180:183], v160 offset:3072
	s_add_u32 s28, s28, 0x80000
	s_addc_u32 s29, s29, 0
	s_mov_b32 m0, s45
	v_lshl_add_u64 v[220:221], s[28:29], 0, v[152:153]
	ds_read_b128 v[184:187], v199 offset:32768
	ds_read_b128 v[188:191], v199 offset:33792
	ds_read_b128 v[200:203], v199 offset:34816
	ds_read_b128 v[204:207], v199 offset:35840
	ds_read_b128 v[208:211], v199 offset:36864
	ds_read_b128 v[212:215], v199 offset:37888
	ds_read_b128 v[216:219], v199 offset:38912
	ds_read_b128 v[230:233], v199 offset:39936
	global_load_lds_dwordx4 v[220:221], off
	v_lshl_add_u64 v[220:221], s[28:29], 0, v[156:157]
	s_mov_b32 m0, s47
	s_nop 0
	global_load_lds_dwordx4 v[220:221], off
	s_waitcnt vmcnt(8)
	s_waitcnt lgkmcnt(0)
	s_barrier
	s_setprio 1
	s_waitcnt lgkmcnt(0)
	s_nop 0
	v_mfma_f32_16x16x32_bf16 v[124:127], v[128:131], v[184:187], v[124:127]
	v_mfma_f32_16x16x32_bf16 v[120:123], v[136:139], v[184:187], v[120:123]
	v_mfma_f32_16x16x32_bf16 v[108:111], v[128:131], v[200:203], v[108:111]
	v_mfma_f32_16x16x32_bf16 v[104:107], v[136:139], v[200:203], v[104:107]
	v_mfma_f32_16x16x32_bf16 v[92:95], v[128:131], v[208:211], v[92:95]
	v_mfma_f32_16x16x32_bf16 v[88:91], v[136:139], v[208:211], v[88:91]
	v_mfma_f32_16x16x32_bf16 v[76:79], v[128:131], v[216:219], v[76:79]
	v_mfma_f32_16x16x32_bf16 v[72:75], v[136:139], v[216:219], v[72:75]
	v_mfma_f32_16x16x32_bf16 v[124:127], v[132:135], v[188:191], v[124:127]
	v_mfma_f32_16x16x32_bf16 v[120:123], v[140:143], v[188:191], v[120:123]
	v_mfma_f32_16x16x32_bf16 v[108:111], v[132:135], v[204:207], v[108:111]
	v_mfma_f32_16x16x32_bf16 v[104:107], v[140:143], v[204:207], v[104:107]
	v_mfma_f32_16x16x32_bf16 v[92:95], v[132:135], v[212:215], v[92:95]
	v_mfma_f32_16x16x32_bf16 v[88:91], v[140:143], v[212:215], v[88:91]
	v_mfma_f32_16x16x32_bf16 v[76:79], v[132:135], v[230:233], v[76:79]
	v_mfma_f32_16x16x32_bf16 v[72:75], v[140:143], v[230:233], v[72:75]
	s_setprio 0
	s_setprio 1
	v_mfma_f32_16x16x32_bf16 v[116:119], v[144:147], v[184:187], v[116:119]
	v_mfma_f32_16x16x32_bf16 v[112:115], v[176:179], v[184:187], v[112:115]
	v_mfma_f32_16x16x32_bf16 v[100:103], v[144:147], v[200:203], v[100:103]
	v_mfma_f32_16x16x32_bf16 v[96:99], v[176:179], v[200:203], v[96:99]
	v_mfma_f32_16x16x32_bf16 v[84:87], v[144:147], v[208:211], v[84:87]
	v_mfma_f32_16x16x32_bf16 v[80:83], v[176:179], v[208:211], v[80:83]
	v_mfma_f32_16x16x32_bf16 v[68:71], v[144:147], v[216:219], v[68:71]
	v_mfma_f32_16x16x32_bf16 v[64:67], v[176:179], v[216:219], v[64:67]
	v_mfma_f32_16x16x32_bf16 v[116:119], v[148:151], v[188:191], v[116:119]
	v_mfma_f32_16x16x32_bf16 v[112:115], v[180:183], v[188:191], v[112:115]
	v_mfma_f32_16x16x32_bf16 v[100:103], v[148:151], v[204:207], v[100:103]
	v_mfma_f32_16x16x32_bf16 v[96:99], v[180:183], v[204:207], v[96:99]
	v_mfma_f32_16x16x32_bf16 v[84:87], v[148:151], v[212:215], v[84:87]
	v_mfma_f32_16x16x32_bf16 v[80:83], v[180:183], v[212:215], v[80:83]
	v_mfma_f32_16x16x32_bf16 v[68:71], v[148:151], v[230:233], v[68:71]
	v_mfma_f32_16x16x32_bf16 v[64:67], v[180:183], v[230:233], v[64:67]
	s_setprio 0
	s_barrier
	s_mov_b32 m0, s49
	v_lshl_add_u64 v[162:163], v[162:163], 0, s[86:87]
	s_add_u32 s26, s26, 0x80080
	ds_read_b128 v[184:187], v199 offset:49152
	ds_read_b128 v[188:191], v199 offset:50176
	ds_read_b128 v[200:203], v199 offset:51200
	ds_read_b128 v[204:207], v199 offset:52224
	ds_read_b128 v[208:211], v199 offset:53248
	ds_read_b128 v[212:215], v199 offset:54272
	ds_read_b128 v[216:219], v199 offset:55296
	ds_read_b128 v[230:233], v199 offset:56320
	global_load_lds_dwordx4 v[162:163], off
	v_lshl_add_u64 v[162:163], v[166:167], 0, s[86:87]
	s_mov_b32 m0, s50
	s_addc_u32 s27, s27, 0
	global_load_lds_dwordx4 v[162:163], off
	v_lshl_add_u64 v[162:163], s[26:27], 0, v[154:155]
	s_mov_b32 m0, s54
	s_nop 0
	global_load_lds_dwordx4 v[162:163], off
	v_lshl_add_u64 v[162:163], s[26:27], 0, v[158:159]
	s_mov_b32 m0, s55
	s_nop 0
	global_load_lds_dwordx4 v[162:163], off
	v_lshl_add_u64 v[162:163], v[194:195], 0, s[86:87]
	s_mov_b32 m0, s51
	s_nop 0
	global_load_lds_dwordx4 v[162:163], off
	v_lshl_add_u64 v[162:163], v[196:197], 0, s[86:87]
	s_mov_b32 m0, s52
	s_nop 0
	global_load_lds_dwordx4 v[162:163], off
	s_waitcnt vmcnt(8)
	s_waitcnt lgkmcnt(0)
	s_barrier
	s_setprio 1
	s_waitcnt lgkmcnt(0)
	v_mfma_f32_16x16x32_bf16 v[60:63], v[128:131], v[184:187], v[60:63]
	v_mfma_f32_16x16x32_bf16 v[56:59], v[136:139], v[184:187], v[56:59]
	v_mfma_f32_16x16x32_bf16 v[44:47], v[128:131], v[200:203], v[44:47]
	v_mfma_f32_16x16x32_bf16 v[40:43], v[136:139], v[200:203], v[40:43]
	v_mfma_f32_16x16x32_bf16 v[28:31], v[128:131], v[208:211], v[28:31]
	v_mfma_f32_16x16x32_bf16 v[24:27], v[136:139], v[208:211], v[24:27]
	v_mfma_f32_16x16x32_bf16 v[12:15], v[128:131], v[216:219], v[12:15]
	v_mfma_f32_16x16x32_bf16 v[8:11], v[136:139], v[216:219], v[8:11]
	v_mfma_f32_16x16x32_bf16 v[60:63], v[132:135], v[188:191], v[60:63]
	v_mfma_f32_16x16x32_bf16 v[56:59], v[140:143], v[188:191], v[56:59]
	v_mfma_f32_16x16x32_bf16 v[44:47], v[132:135], v[204:207], v[44:47]
	v_mfma_f32_16x16x32_bf16 v[40:43], v[140:143], v[204:207], v[40:43]
	v_mfma_f32_16x16x32_bf16 v[28:31], v[132:135], v[212:215], v[28:31]
	v_mfma_f32_16x16x32_bf16 v[24:27], v[140:143], v[212:215], v[24:27]
	v_mfma_f32_16x16x32_bf16 v[12:15], v[132:135], v[230:233], v[12:15]
	v_mfma_f32_16x16x32_bf16 v[8:11], v[140:143], v[230:233], v[8:11]
	s_setprio 0
	s_setprio 1
	v_mfma_f32_16x16x32_bf16 v[52:55], v[144:147], v[184:187], v[52:55]
	v_mfma_f32_16x16x32_bf16 v[48:51], v[176:179], v[184:187], v[48:51]
	v_mfma_f32_16x16x32_bf16 v[36:39], v[144:147], v[200:203], v[36:39]
	v_mfma_f32_16x16x32_bf16 v[32:35], v[176:179], v[200:203], v[32:35]
	v_mfma_f32_16x16x32_bf16 v[20:23], v[144:147], v[208:211], v[20:23]
	v_mfma_f32_16x16x32_bf16 v[16:19], v[176:179], v[208:211], v[16:19]
	v_mfma_f32_16x16x32_bf16 v[4:7], v[144:147], v[216:219], v[4:7]
	v_mfma_f32_16x16x32_bf16 v[0:3], v[176:179], v[216:219], v[0:3]
	v_mfma_f32_16x16x32_bf16 v[52:55], v[148:151], v[188:191], v[52:55]
	v_mfma_f32_16x16x32_bf16 v[48:51], v[180:183], v[188:191], v[48:51]
	v_mfma_f32_16x16x32_bf16 v[36:39], v[148:151], v[204:207], v[36:39]
	v_mfma_f32_16x16x32_bf16 v[32:35], v[180:183], v[204:207], v[32:35]
	v_mfma_f32_16x16x32_bf16 v[20:23], v[148:151], v[212:215], v[20:23]
	v_mfma_f32_16x16x32_bf16 v[16:19], v[180:183], v[212:215], v[16:19]
	v_mfma_f32_16x16x32_bf16 v[4:7], v[148:151], v[230:233], v[4:7]
	v_mfma_f32_16x16x32_bf16 v[0:3], v[180:183], v[230:233], v[0:3]
	s_setprio 0
	s_barrier
	s_add_i32 s61, s61, 2
	s_add_u32 s59, s59, 0x100
	s_addc_u32 s60, s60, 0
	s_add_u32 s8, s8, 0x100
	s_addc_u32 s9, s9, 0
	s_cmp_gt_u32 s61, 29
	s_cbranch_scc0 .LBB0_189
	s_and_b64 vcc, exec, s[12:13]
	s_cbranch_vccz .LBB0_192
	s_barrier

.LBB0_682:
	v_add_u32_e32 v144, s28, v198
	v_add_u32_e32 v160, s31, v198
	s_add_u32 s18, s14, s16
	ds_read_b128 v[128:131], v144
	ds_read_b128 v[132:135], v144 offset:1024
	ds_read_b128 v[140:143], v144 offset:2048
	ds_read_b128 v[144:147], v144 offset:3072
	ds_read_b128 v[148:151], v160
	ds_read_b128 v[152:155], v160 offset:1024
	ds_read_b128 v[156:159], v160 offset:2048
	ds_read_b128 v[182:185], v160 offset:3072
	s_addc_u32 s19, s15, s17
	s_add_u32 s18, s18, 0x100
	s_addc_u32 s19, s19, 0
	s_add_u32 s33, s54, s16
	s_addc_u32 s57, s55, s17
	s_cmpk_eq_i32 s16, 0x1700
	s_cselect_b32 s21, s5, s19
	s_cselect_b32 s20, s4, s18
	s_cselect_b32 s19, s13, s57
	s_cselect_b32 s18, s12, s33
	v_lshl_add_u64 v[162:163], v[138:139], 0, s[16:17]
	s_add_i32 m0, s36, 0xc000
	ds_read_b128 v[186:189], v201
	ds_read_b128 v[190:193], v201 offset:1024
	ds_read_b128 v[194:197], v201 offset:2048
	ds_read_b128 v[202:205], v201 offset:3072
	ds_read_b128 v[206:209], v201 offset:4096
	ds_read_b128 v[210:213], v201 offset:5120
	ds_read_b128 v[214:217], v201 offset:6144
	ds_read_b128 v[218:221], v201 offset:7168
	global_load_lds_dwordx4 v[162:163], off
	v_lshl_add_u64 v[162:163], v[136:137], 0, s[16:17]
	s_add_i32 m0, s36, 0xe000
	s_nop 0
	global_load_lds_dwordx4 v[162:163], off
	s_waitcnt vmcnt(8)
	s_waitcnt lgkmcnt(0)
	s_barrier
	s_setprio 1
	s_waitcnt lgkmcnt(0)
	v_mfma_f32_16x16x32_bf16 v[124:127], v[128:131], v[186:189], v[124:127]
	v_mfma_f32_16x16x32_bf16 v[120:123], v[140:143], v[186:189], v[120:123]
	v_mfma_f32_16x16x32_bf16 v[108:111], v[128:131], v[194:197], v[108:111]
	v_mfma_f32_16x16x32_bf16 v[104:107], v[140:143], v[194:197], v[104:107]
	v_mfma_f32_16x16x32_bf16 v[92:95], v[128:131], v[206:209], v[92:95]
	v_mfma_f32_16x16x32_bf16 v[88:91], v[140:143], v[206:209], v[88:91]
	v_mfma_f32_16x16x32_bf16 v[76:79], v[128:131], v[214:217], v[76:79]
	v_mfma_f32_16x16x32_bf16 v[72:75], v[140:143], v[214:217], v[72:75]
	v_mfma_f32_16x16x32_bf16 v[124:127], v[132:135], v[190:193], v[124:127]
	v_mfma_f32_16x16x32_bf16 v[120:123], v[144:147], v[190:193], v[120:123]
	v_mfma_f32_16x16x32_bf16 v[108:111], v[132:135], v[202:205], v[108:111]
	v_mfma_f32_16x16x32_bf16 v[104:107], v[144:147], v[202:205], v[104:107]
	v_mfma_f32_16x16x32_bf16 v[92:95], v[132:135], v[210:213], v[92:95]
	v_mfma_f32_16x16x32_bf16 v[88:91], v[144:147], v[210:213], v[88:91]
	v_mfma_f32_16x16x32_bf16 v[76:79], v[132:135], v[218:221], v[76:79]
	v_mfma_f32_16x16x32_bf16 v[72:75], v[144:147], v[218:221], v[72:75]
	s_setprio 0
	s_setprio 1
	v_mfma_f32_16x16x32_bf16 v[116:119], v[148:151], v[186:189], v[116:119]
	v_mfma_f32_16x16x32_bf16 v[112:115], v[156:159], v[186:189], v[112:115]
	v_mfma_f32_16x16x32_bf16 v[100:103], v[148:151], v[194:197], v[100:103]
	v_mfma_f32_16x16x32_bf16 v[96:99], v[156:159], v[194:197], v[96:99]
	v_mfma_f32_16x16x32_bf16 v[84:87], v[148:151], v[206:209], v[84:87]
	v_mfma_f32_16x16x32_bf16 v[80:83], v[156:159], v[206:209], v[80:83]
	v_mfma_f32_16x16x32_bf16 v[68:71], v[148:151], v[214:217], v[68:71]
	v_mfma_f32_16x16x32_bf16 v[64:67], v[156:159], v[214:217], v[64:67]
	v_mfma_f32_16x16x32_bf16 v[116:119], v[152:155], v[190:193], v[116:119]
	v_mfma_f32_16x16x32_bf16 v[112:115], v[182:185], v[190:193], v[112:115]
	v_mfma_f32_16x16x32_bf16 v[100:103], v[152:155], v[202:205], v[100:103]
	v_mfma_f32_16x16x32_bf16 v[96:99], v[182:185], v[202:205], v[96:99]
	v_mfma_f32_16x16x32_bf16 v[84:87], v[152:155], v[210:213], v[84:87]
	v_mfma_f32_16x16x32_bf16 v[80:83], v[182:185], v[210:213], v[80:83]
	v_mfma_f32_16x16x32_bf16 v[68:71], v[152:155], v[218:221], v[68:71]
	v_mfma_f32_16x16x32_bf16 v[64:67], v[182:185], v[218:221], v[64:67]
	s_setprio 0
	s_barrier
	s_mov_b32 m0, s29
	v_lshl_add_u64 v[162:163], s[18:19], 0, v[168:169]
	s_add_u32 s58, s18, 0xc0000
	ds_read_b128 v[186:189], v201 offset:16384
	ds_read_b128 v[190:193], v201 offset:17408
	ds_read_b128 v[194:197], v201 offset:18432
	ds_read_b128 v[202:205], v201 offset:19456
	ds_read_b128 v[206:209], v201 offset:20480
	ds_read_b128 v[210:213], v201 offset:21504
	ds_read_b128 v[214:217], v201 offset:22528
	ds_read_b128 v[218:221], v201 offset:23552
	global_load_lds_dwordx4 v[162:163], off
	v_lshl_add_u64 v[222:223], s[18:19], 0, v[172:173]
	s_mov_b32 m0, s30
	s_addc_u32 s59, s19, 0
	global_load_lds_dwordx4 v[222:223], off
	v_lshl_add_u64 v[224:225], s[58:59], 0, v[168:169]
	s_mov_b32 m0, s34
	v_lshl_add_u64 v[230:231], s[20:21], 0, v[170:171]
	global_load_lds_dwordx4 v[224:225], off
	v_lshl_add_u64 v[224:225], s[58:59], 0, v[172:173]
	s_mov_b32 m0, s35
	s_nop 0
	global_load_lds_dwordx4 v[224:225], off
	v_lshl_add_u64 v[224:225], s[20:21], 0, v[166:167]
	s_mov_b32 m0, s36
	s_nop 0
	global_load_lds_dwordx4 v[224:225], off
	s_mov_b32 m0, s37
	s_nop 0
	global_load_lds_dwordx4 v[230:231], off
	s_waitcnt vmcnt(8)
	s_waitcnt lgkmcnt(0)
	s_barrier
	s_setprio 1
	s_waitcnt lgkmcnt(0)
	s_nop 0
	v_mfma_f32_16x16x32_bf16 v[60:63], v[128:131], v[186:189], v[60:63]
	v_mfma_f32_16x16x32_bf16 v[56:59], v[140:143], v[186:189], v[56:59]
	v_mfma_f32_16x16x32_bf16 v[44:47], v[128:131], v[194:197], v[44:47]
	v_mfma_f32_16x16x32_bf16 v[40:43], v[140:143], v[194:197], v[40:43]
	v_mfma_f32_16x16x32_bf16 v[28:31], v[128:131], v[206:209], v[28:31]
	v_mfma_f32_16x16x32_bf16 v[24:27], v[140:143], v[206:209], v[24:27]
	v_mfma_f32_16x16x32_bf16 v[12:15], v[128:131], v[214:217], v[12:15]
	v_mfma_f32_16x16x32_bf16 v[8:11], v[140:143], v[214:217], v[8:11]
	v_mfma_f32_16x16x32_bf16 v[60:63], v[132:135], v[190:193], v[60:63]
	v_mfma_f32_16x16x32_bf16 v[56:59], v[144:147], v[190:193], v[56:59]
	v_mfma_f32_16x16x32_bf16 v[44:47], v[132:135], v[202:205], v[44:47]
	v_mfma_f32_16x16x32_bf16 v[40:43], v[144:147], v[202:205], v[40:43]
	v_mfma_f32_16x16x32_bf16 v[28:31], v[132:135], v[210:213], v[28:31]
	v_mfma_f32_16x16x32_bf16 v[24:27], v[144:147], v[210:213], v[24:27]
	v_mfma_f32_16x16x32_bf16 v[12:15], v[132:135], v[218:221], v[12:15]
	v_mfma_f32_16x16x32_bf16 v[8:11], v[144:147], v[218:221], v[8:11]
	s_setprio 0
	s_setprio 1
	v_mfma_f32_16x16x32_bf16 v[52:55], v[148:151], v[186:189], v[52:55]
	v_mfma_f32_16x16x32_bf16 v[48:51], v[156:159], v[186:189], v[48:51]
	v_mfma_f32_16x16x32_bf16 v[36:39], v[148:151], v[194:197], v[36:39]
	v_mfma_f32_16x16x32_bf16 v[32:35], v[156:159], v[194:197], v[32:35]
	v_mfma_f32_16x16x32_bf16 v[20:23], v[148:151], v[206:209], v[20:23]
	v_mfma_f32_16x16x32_bf16 v[16:19], v[156:159], v[206:209], v[16:19]
	v_mfma_f32_16x16x32_bf16 v[4:7], v[148:151], v[214:217], v[4:7]
	v_mfma_f32_16x16x32_bf16 v[0:3], v[156:159], v[214:217], v[0:3]
	v_mfma_f32_16x16x32_bf16 v[52:55], v[152:155], v[190:193], v[52:55]
	v_mfma_f32_16x16x32_bf16 v[48:51], v[182:185], v[190:193], v[48:51]
	v_mfma_f32_16x16x32_bf16 v[36:39], v[152:155], v[202:205], v[36:39]
	v_mfma_f32_16x16x32_bf16 v[32:35], v[182:185], v[202:205], v[32:35]
	v_mfma_f32_16x16x32_bf16 v[20:23], v[152:155], v[210:213], v[20:23]
	v_mfma_f32_16x16x32_bf16 v[16:19], v[182:185], v[210:213], v[16:19]
	v_mfma_f32_16x16x32_bf16 v[4:7], v[152:155], v[218:221], v[4:7]
	v_mfma_f32_16x16x32_bf16 v[0:3], v[182:185], v[218:221], v[0:3]
	s_setprio 0
	s_barrier
	v_add_u32_e32 v144, s41, v198
	v_add_u32_e32 v160, s46, v198
	ds_read_b128 v[128:131], v144
	ds_read_b128 v[132:135], v144 offset:1024
	ds_read_b128 v[140:143], v144 offset:2048
	ds_read_b128 v[144:147], v144 offset:3072
	ds_read_b128 v[148:151], v160
	ds_read_b128 v[152:155], v160 offset:1024
	ds_read_b128 v[156:159], v160 offset:2048
	ds_read_b128 v[182:185], v160 offset:3072
	s_add_u32 s20, s20, 0x340000
	s_addc_u32 s21, s21, 0
	s_mov_b32 m0, s38
	v_lshl_add_u64 v[232:233], s[20:21], 0, v[166:167]
	ds_read_b128 v[186:189], v201 offset:32768
	ds_read_b128 v[190:193], v201 offset:33792
	ds_read_b128 v[194:197], v201 offset:34816
	ds_read_b128 v[202:205], v201 offset:35840
	ds_read_b128 v[206:209], v201 offset:36864
	ds_read_b128 v[210:213], v201 offset:37888
	ds_read_b128 v[214:217], v201 offset:38912
	ds_read_b128 v[218:221], v201 offset:39936
	global_load_lds_dwordx4 v[232:233], off
	v_lshl_add_u64 v[232:233], s[20:21], 0, v[170:171]
	s_mov_b32 m0, s39
	s_nop 0
	global_load_lds_dwordx4 v[232:233], off
	s_waitcnt vmcnt(8)
	s_waitcnt lgkmcnt(0)
	s_barrier
	s_setprio 1
	s_waitcnt lgkmcnt(0)
	s_nop 0
	v_mfma_f32_16x16x32_bf16 v[124:127], v[128:131], v[186:189], v[124:127]
	v_mfma_f32_16x16x32_bf16 v[120:123], v[140:143], v[186:189], v[120:123]
	v_mfma_f32_16x16x32_bf16 v[108:111], v[128:131], v[194:197], v[108:111]
	v_mfma_f32_16x16x32_bf16 v[104:107], v[140:143], v[194:197], v[104:107]
	v_mfma_f32_16x16x32_bf16 v[92:95], v[128:131], v[206:209], v[92:95]
	v_mfma_f32_16x16x32_bf16 v[88:91], v[140:143], v[206:209], v[88:91]
	v_mfma_f32_16x16x32_bf16 v[76:79], v[128:131], v[214:217], v[76:79]
	v_mfma_f32_16x16x32_bf16 v[72:75], v[140:143], v[214:217], v[72:75]
	v_mfma_f32_16x16x32_bf16 v[124:127], v[132:135], v[190:193], v[124:127]
	v_mfma_f32_16x16x32_bf16 v[120:123], v[144:147], v[190:193], v[120:123]
	v_mfma_f32_16x16x32_bf16 v[108:111], v[132:135], v[202:205], v[108:111]
	v_mfma_f32_16x16x32_bf16 v[104:107], v[144:147], v[202:205], v[104:107]
	v_mfma_f32_16x16x32_bf16 v[92:95], v[132:135], v[210:213], v[92:95]
	v_mfma_f32_16x16x32_bf16 v[88:91], v[144:147], v[210:213], v[88:91]
	v_mfma_f32_16x16x32_bf16 v[76:79], v[132:135], v[218:221], v[76:79]
	v_mfma_f32_16x16x32_bf16 v[72:75], v[144:147], v[218:221], v[72:75]
	s_setprio 0
	s_setprio 1
	v_mfma_f32_16x16x32_bf16 v[116:119], v[148:151], v[186:189], v[116:119]
	v_mfma_f32_16x16x32_bf16 v[112:115], v[156:159], v[186:189], v[112:115]
	v_mfma_f32_16x16x32_bf16 v[100:103], v[148:151], v[194:197], v[100:103]
	v_mfma_f32_16x16x32_bf16 v[96:99], v[156:159], v[194:197], v[96:99]
	v_mfma_f32_16x16x32_bf16 v[84:87], v[148:151], v[206:209], v[84:87]
	v_mfma_f32_16x16x32_bf16 v[80:83], v[156:159], v[206:209], v[80:83]
	v_mfma_f32_16x16x32_bf16 v[68:71], v[148:151], v[214:217], v[68:71]
	v_mfma_f32_16x16x32_bf16 v[64:67], v[156:159], v[214:217], v[64:67]
	v_mfma_f32_16x16x32_bf16 v[116:119], v[152:155], v[190:193], v[116:119]
	v_mfma_f32_16x16x32_bf16 v[112:115], v[182:185], v[190:193], v[112:115]
	v_mfma_f32_16x16x32_bf16 v[100:103], v[152:155], v[202:205], v[100:103]
	v_mfma_f32_16x16x32_bf16 v[96:99], v[182:185], v[202:205], v[96:99]
	v_mfma_f32_16x16x32_bf16 v[84:87], v[152:155], v[210:213], v[84:87]
	v_mfma_f32_16x16x32_bf16 v[80:83], v[182:185], v[210:213], v[80:83]
	v_mfma_f32_16x16x32_bf16 v[68:71], v[152:155], v[218:221], v[68:71]
	v_mfma_f32_16x16x32_bf16 v[64:67], v[182:185], v[218:221], v[64:67]
	s_setprio 0
	s_barrier
	s_mov_b32 m0, s42
	v_lshl_add_u64 v[162:163], v[162:163], 0, s[86:87]
	s_add_u32 s18, s18, 0xc0080
	ds_read_b128 v[186:189], v201 offset:49152
	ds_read_b128 v[190:193], v201 offset:50176
	ds_read_b128 v[194:197], v201 offset:51200
	ds_read_b128 v[202:205], v201 offset:52224
	ds_read_b128 v[206:209], v201 offset:53248
	ds_read_b128 v[210:213], v201 offset:54272
	ds_read_b128 v[214:217], v201 offset:55296
	ds_read_b128 v[218:221], v201 offset:56320
	global_load_lds_dwordx4 v[162:163], off
	v_lshl_add_u64 v[162:163], v[222:223], 0, s[86:87]
	s_mov_b32 m0, s43
	s_addc_u32 s19, s19, 0
	global_load_lds_dwordx4 v[162:163], off
	v_lshl_add_u64 v[162:163], s[18:19], 0, v[168:169]
	s_mov_b32 m0, s47
	s_nop 0
	global_load_lds_dwordx4 v[162:163], off
	v_lshl_add_u64 v[162:163], s[18:19], 0, v[172:173]
	s_mov_b32 m0, s48
	s_nop 0
	global_load_lds_dwordx4 v[162:163], off
	v_lshl_add_u64 v[162:163], v[224:225], 0, s[86:87]
	s_mov_b32 m0, s44
	s_nop 0
	global_load_lds_dwordx4 v[162:163], off
	v_lshl_add_u64 v[162:163], v[230:231], 0, s[86:87]
	s_mov_b32 m0, s45
	s_nop 0
	global_load_lds_dwordx4 v[162:163], off
	s_waitcnt vmcnt(8)
	s_waitcnt lgkmcnt(0)
	s_barrier
	s_setprio 1
	s_waitcnt lgkmcnt(0)
	v_mfma_f32_16x16x32_bf16 v[60:63], v[128:131], v[186:189], v[60:63]
	v_mfma_f32_16x16x32_bf16 v[56:59], v[140:143], v[186:189], v[56:59]
	v_mfma_f32_16x16x32_bf16 v[44:47], v[128:131], v[194:197], v[44:47]
	v_mfma_f32_16x16x32_bf16 v[40:43], v[140:143], v[194:197], v[40:43]
	v_mfma_f32_16x16x32_bf16 v[28:31], v[128:131], v[206:209], v[28:31]
	v_mfma_f32_16x16x32_bf16 v[24:27], v[140:143], v[206:209], v[24:27]
	v_mfma_f32_16x16x32_bf16 v[12:15], v[128:131], v[214:217], v[12:15]
	v_mfma_f32_16x16x32_bf16 v[8:11], v[140:143], v[214:217], v[8:11]
	v_mfma_f32_16x16x32_bf16 v[60:63], v[132:135], v[190:193], v[60:63]
	v_mfma_f32_16x16x32_bf16 v[56:59], v[144:147], v[190:193], v[56:59]
	v_mfma_f32_16x16x32_bf16 v[44:47], v[132:135], v[202:205], v[44:47]
	v_mfma_f32_16x16x32_bf16 v[40:43], v[144:147], v[202:205], v[40:43]
	v_mfma_f32_16x16x32_bf16 v[28:31], v[132:135], v[210:213], v[28:31]
	v_mfma_f32_16x16x32_bf16 v[24:27], v[144:147], v[210:213], v[24:27]
	v_mfma_f32_16x16x32_bf16 v[12:15], v[132:135], v[218:221], v[12:15]
	v_mfma_f32_16x16x32_bf16 v[8:11], v[144:147], v[218:221], v[8:11]
	s_setprio 0
	s_setprio 1
	v_mfma_f32_16x16x32_bf16 v[52:55], v[148:151], v[186:189], v[52:55]
	v_mfma_f32_16x16x32_bf16 v[48:51], v[156:159], v[186:189], v[48:51]
	v_mfma_f32_16x16x32_bf16 v[36:39], v[148:151], v[194:197], v[36:39]
	v_mfma_f32_16x16x32_bf16 v[32:35], v[156:159], v[194:197], v[32:35]
	v_mfma_f32_16x16x32_bf16 v[20:23], v[148:151], v[206:209], v[20:23]
	v_mfma_f32_16x16x32_bf16 v[16:19], v[156:159], v[206:209], v[16:19]
	v_mfma_f32_16x16x32_bf16 v[4:7], v[148:151], v[214:217], v[4:7]
	v_mfma_f32_16x16x32_bf16 v[0:3], v[156:159], v[214:217], v[0:3]
	v_mfma_f32_16x16x32_bf16 v[52:55], v[152:155], v[190:193], v[52:55]
	v_mfma_f32_16x16x32_bf16 v[48:51], v[182:185], v[190:193], v[48:51]
	v_mfma_f32_16x16x32_bf16 v[36:39], v[152:155], v[202:205], v[36:39]
	v_mfma_f32_16x16x32_bf16 v[32:35], v[182:185], v[202:205], v[32:35]
	v_mfma_f32_16x16x32_bf16 v[20:23], v[152:155], v[210:213], v[20:23]
	v_mfma_f32_16x16x32_bf16 v[16:19], v[182:185], v[210:213], v[16:19]
	v_mfma_f32_16x16x32_bf16 v[4:7], v[152:155], v[218:221], v[4:7]
	v_mfma_f32_16x16x32_bf16 v[0:3], v[182:185], v[218:221], v[0:3]
	s_setprio 0
	s_barrier
	s_add_i32 s56, s56, 2
	s_add_u32 s16, s16, 0x100
	s_addc_u32 s17, s17, 0
	s_cmp_gt_u32 s56, 45
	s_cbranch_scc1 .LBB0_685

.LBB0_750:
	v_mov_b64_e32 v[0:1], 0x400
	s_ashr_i32 s7, s6, 31
	v_cmp_lt_i64_e32 vcc, s[8:9], v[0:1]
	s_lshl_b64 s[8:9], s[6:7], 20
	s_add_u32 s8, s23, s8
	s_addc_u32 s9, s24, s9
	s_and_b64 s[10:11], vcc, exec
	s_cselect_b32 s7, s9, s17
	s_cselect_b32 s50, s8, s16
	s_ashr_i32 s5, s4, 31
	s_lshl_b64 s[10:11], s[4:5], 20
	s_add_u32 s10, s25, s10
	s_addc_u32 s11, s26, s11
	s_and_b64 s[18:19], vcc, exec
	s_cselect_b32 s5, s11, s15
	s_cselect_b32 s51, s10, s14
	s_add_u32 s52, s14, 0x100
	s_addc_u32 s53, s15, 0
	s_add_u32 s14, s16, 0x80080
	v_mov_b32_e32 v0, 0
	s_addc_u32 s15, s17, 0
	s_mov_b32 s54, -2
	s_cmp_eq_u32 s48, 1
	s_cbranch_scc1 .Lpeel_zero_P5
	v_add_u32_e32 v120, s13, v230
	v_add_u32_e32 v148, s29, v230
	ds_read_b128 v[88:91], v120
	ds_read_b128 v[100:103], v120 offset:1024
	ds_read_b128 v[112:115], v120 offset:2048
	ds_read_b128 v[120:123], v120 offset:3072
	ds_read_b128 v[124:127], v148
	ds_read_b128 v[140:143], v148 offset:1024
	ds_read_b128 v[144:147], v148 offset:2048
	ds_read_b128 v[148:151], v148 offset:3072
	s_add_u32 s16, s14, 0xfff80080
	s_addc_u32 s17, s15, -1
	s_cmp_eq_u32 s54, 28
	s_cselect_b32 s19, s7, s17
	s_cselect_b32 s18, s50, s16
	s_cselect_b32 s17, s5, s53
	s_cselect_b32 s16, s51, s52
	v_lshl_add_u64 v[206:207], s[14:15], 0, v[204:205]
	s_add_i32 m0, s34, 0xc000
	ds_read_b128 v[152:155], v232
	ds_read_b128 v[170:173], v232 offset:1024
	ds_read_b128 v[174:177], v232 offset:2048
	ds_read_b128 v[178:181], v232 offset:3072
	ds_read_b128 v[182:185], v232 offset:4096
	ds_read_b128 v[186:189], v232 offset:5120
	ds_read_b128 v[190:193], v232 offset:6144
	ds_read_b128 v[194:197], v232 offset:7168
	global_load_lds_dwordx4 v[206:207], off
	v_lshl_add_u64 v[206:207], s[14:15], 0, v[202:203]
	s_add_i32 m0, s34, 0xe000
	s_nop 0
	global_load_lds_dwordx4 v[206:207], off
	s_waitcnt vmcnt(40)
	s_waitcnt lgkmcnt(0)
	s_barrier
	s_setprio 1
	s_waitcnt lgkmcnt(0)
	v_mfma_f32_16x16x32_bf16 v[166:169], v[88:91], v[152:155], 0
	v_mfma_f32_16x16x32_bf16 v[156:159], v[112:115], v[152:155], 0
	v_mfma_f32_16x16x32_bf16 v[128:131], v[88:91], v[174:177], 0
	v_mfma_f32_16x16x32_bf16 v[116:119], v[112:115], v[174:177], 0
	v_mfma_f32_16x16x32_bf16 v[96:99], v[88:91], v[182:185], 0
	v_mfma_f32_16x16x32_bf16 v[92:95], v[112:115], v[182:185], 0
	v_mfma_f32_16x16x32_bf16 v[76:79], v[88:91], v[190:193], 0
	v_mfma_f32_16x16x32_bf16 v[72:75], v[112:115], v[190:193], 0
	v_mfma_f32_16x16x32_bf16 v[166:169], v[100:103], v[170:173], v[166:169]
	v_mfma_f32_16x16x32_bf16 v[156:159], v[120:123], v[170:173], v[156:159]
	v_mfma_f32_16x16x32_bf16 v[128:131], v[100:103], v[178:181], v[128:131]
	v_mfma_f32_16x16x32_bf16 v[116:119], v[120:123], v[178:181], v[116:119]
	v_mfma_f32_16x16x32_bf16 v[96:99], v[100:103], v[186:189], v[96:99]
	v_mfma_f32_16x16x32_bf16 v[92:95], v[120:123], v[186:189], v[92:95]
	v_mfma_f32_16x16x32_bf16 v[76:79], v[100:103], v[194:197], v[76:79]
	v_mfma_f32_16x16x32_bf16 v[72:75], v[120:123], v[194:197], v[72:75]
	s_setprio 0
	s_setprio 1
	v_mfma_f32_16x16x32_bf16 v[136:139], v[124:127], v[152:155], 0
	v_mfma_f32_16x16x32_bf16 v[132:135], v[144:147], v[152:155], 0
	v_mfma_f32_16x16x32_bf16 v[108:111], v[124:127], v[174:177], 0
	v_mfma_f32_16x16x32_bf16 v[104:107], v[144:147], v[174:177], 0
	v_mfma_f32_16x16x32_bf16 v[84:87], v[124:127], v[182:185], 0
	v_mfma_f32_16x16x32_bf16 v[80:83], v[144:147], v[182:185], 0
	v_mfma_f32_16x16x32_bf16 v[68:71], v[124:127], v[190:193], 0
	v_mfma_f32_16x16x32_bf16 v[64:67], v[144:147], v[190:193], 0
	v_mfma_f32_16x16x32_bf16 v[136:139], v[140:143], v[170:173], v[136:139]
	v_mfma_f32_16x16x32_bf16 v[132:135], v[148:151], v[170:173], v[132:135]
	v_mfma_f32_16x16x32_bf16 v[108:111], v[140:143], v[178:181], v[108:111]
	v_mfma_f32_16x16x32_bf16 v[104:107], v[148:151], v[178:181], v[104:107]
	v_mfma_f32_16x16x32_bf16 v[84:87], v[140:143], v[186:189], v[84:87]
	v_mfma_f32_16x16x32_bf16 v[80:83], v[148:151], v[186:189], v[80:83]
	v_mfma_f32_16x16x32_bf16 v[68:71], v[140:143], v[194:197], v[68:71]
	v_mfma_f32_16x16x32_bf16 v[64:67], v[148:151], v[194:197], v[64:67]
	s_setprio 0
	s_barrier
	s_mov_b32 m0, s27
	v_lshl_add_u64 v[206:207], s[16:17], 0, v[160:161]
	s_add_u32 s56, s16, 0x80000
	ds_read_b128 v[152:155], v232 offset:16384
	ds_read_b128 v[170:173], v232 offset:17408
	ds_read_b128 v[174:177], v232 offset:18432
	ds_read_b128 v[178:181], v232 offset:19456
	ds_read_b128 v[182:185], v232 offset:20480
	ds_read_b128 v[186:189], v232 offset:21504
	ds_read_b128 v[190:193], v232 offset:22528
	ds_read_b128 v[194:197], v232 offset:23552
	global_load_lds_dwordx4 v[206:207], off
	v_lshl_add_u64 v[208:209], s[16:17], 0, v[200:201]
	s_mov_b32 m0, s28
	s_addc_u32 s57, s17, 0
	global_load_lds_dwordx4 v[208:209], off
	v_lshl_add_u64 v[210:211], s[56:57], 0, v[160:161]
	s_mov_b32 m0, s30
	v_lshl_add_u64 v[212:213], s[18:19], 0, v[198:199]
	global_load_lds_dwordx4 v[210:211], off
	v_lshl_add_u64 v[210:211], s[56:57], 0, v[200:201]
	s_mov_b32 m0, s31
	s_nop 0
	global_load_lds_dwordx4 v[210:211], off
	v_lshl_add_u64 v[210:211], s[18:19], 0, v[162:163]
	s_mov_b32 m0, s34
	s_nop 0
	global_load_lds_dwordx4 v[210:211], off
	s_mov_b32 m0, s35
	s_nop 0
	global_load_lds_dwordx4 v[212:213], off
	s_waitcnt vmcnt(40)
	s_waitcnt lgkmcnt(0)
	s_barrier
	s_setprio 1
	s_waitcnt lgkmcnt(0)
	s_nop 0
	v_mfma_f32_16x16x32_bf16 v[60:63], v[88:91], v[152:155], 0
	v_mfma_f32_16x16x32_bf16 v[56:59], v[112:115], v[152:155], 0
	v_mfma_f32_16x16x32_bf16 v[44:47], v[88:91], v[174:177], 0
	v_mfma_f32_16x16x32_bf16 v[40:43], v[112:115], v[174:177], 0
	v_mfma_f32_16x16x32_bf16 v[28:31], v[88:91], v[182:185], 0
	v_mfma_f32_16x16x32_bf16 v[24:27], v[112:115], v[182:185], 0
	v_mfma_f32_16x16x32_bf16 v[12:15], v[88:91], v[190:193], 0
	v_mfma_f32_16x16x32_bf16 v[8:11], v[112:115], v[190:193], 0
	v_mfma_f32_16x16x32_bf16 v[60:63], v[100:103], v[170:173], v[60:63]
	v_mfma_f32_16x16x32_bf16 v[56:59], v[120:123], v[170:173], v[56:59]
	v_mfma_f32_16x16x32_bf16 v[44:47], v[100:103], v[178:181], v[44:47]
	v_mfma_f32_16x16x32_bf16 v[40:43], v[120:123], v[178:181], v[40:43]
	v_mfma_f32_16x16x32_bf16 v[28:31], v[100:103], v[186:189], v[28:31]
	v_mfma_f32_16x16x32_bf16 v[24:27], v[120:123], v[186:189], v[24:27]
	v_mfma_f32_16x16x32_bf16 v[12:15], v[100:103], v[194:197], v[12:15]
	v_mfma_f32_16x16x32_bf16 v[8:11], v[120:123], v[194:197], v[8:11]
	s_setprio 0
	s_setprio 1
	v_mfma_f32_16x16x32_bf16 v[52:55], v[124:127], v[152:155], 0
	v_mfma_f32_16x16x32_bf16 v[48:51], v[144:147], v[152:155], 0
	v_mfma_f32_16x16x32_bf16 v[36:39], v[124:127], v[174:177], 0
	v_mfma_f32_16x16x32_bf16 v[32:35], v[144:147], v[174:177], 0
	v_mfma_f32_16x16x32_bf16 v[20:23], v[124:127], v[182:185], 0
	v_mfma_f32_16x16x32_bf16 v[16:19], v[144:147], v[182:185], 0
	v_mfma_f32_16x16x32_bf16 v[4:7], v[124:127], v[190:193], 0
	v_mfma_f32_16x16x32_bf16 v[0:3], v[144:147], v[190:193], 0
	v_mfma_f32_16x16x32_bf16 v[52:55], v[140:143], v[170:173], v[52:55]
	v_mfma_f32_16x16x32_bf16 v[48:51], v[148:151], v[170:173], v[48:51]
	v_mfma_f32_16x16x32_bf16 v[36:39], v[140:143], v[178:181], v[36:39]
	v_mfma_f32_16x16x32_bf16 v[32:35], v[148:151], v[178:181], v[32:35]
	v_mfma_f32_16x16x32_bf16 v[20:23], v[140:143], v[186:189], v[20:23]
	v_mfma_f32_16x16x32_bf16 v[16:19], v[148:151], v[186:189], v[16:19]
	v_mfma_f32_16x16x32_bf16 v[4:7], v[140:143], v[194:197], v[4:7]
	v_mfma_f32_16x16x32_bf16 v[0:3], v[148:151], v[194:197], v[0:3]
	s_setprio 0
	s_barrier
	v_add_u32_e32 v120, s39, v230
	v_add_u32_e32 v148, s44, v230
	ds_read_b128 v[88:91], v120
	ds_read_b128 v[100:103], v120 offset:1024
	ds_read_b128 v[112:115], v120 offset:2048
	ds_read_b128 v[120:123], v120 offset:3072
	ds_read_b128 v[124:127], v148
	ds_read_b128 v[140:143], v148 offset:1024
	ds_read_b128 v[144:147], v148 offset:2048
	ds_read_b128 v[148:151], v148 offset:3072
	s_add_u32 s18, s18, 0x80000
	s_addc_u32 s19, s19, 0
	s_mov_b32 m0, s36
	v_lshl_add_u64 v[214:215], s[18:19], 0, v[162:163]
	ds_read_b128 v[152:155], v232 offset:32768
	ds_read_b128 v[170:173], v232 offset:33792
	ds_read_b128 v[174:177], v232 offset:34816
	ds_read_b128 v[178:181], v232 offset:35840
	ds_read_b128 v[182:185], v232 offset:36864
	ds_read_b128 v[186:189], v232 offset:37888
	ds_read_b128 v[190:193], v232 offset:38912
	ds_read_b128 v[194:197], v232 offset:39936
	global_load_lds_dwordx4 v[214:215], off
	v_lshl_add_u64 v[214:215], s[18:19], 0, v[198:199]
	s_mov_b32 m0, s37
	s_nop 0
	global_load_lds_dwordx4 v[214:215], off
	s_waitcnt vmcnt(8)
	s_waitcnt lgkmcnt(0)
	s_barrier
	s_setprio 1
	s_waitcnt lgkmcnt(0)
	s_nop 0
	v_mfma_f32_16x16x32_bf16 v[166:169], v[88:91], v[152:155], v[166:169]
	v_mfma_f32_16x16x32_bf16 v[156:159], v[112:115], v[152:155], v[156:159]
	v_mfma_f32_16x16x32_bf16 v[128:131], v[88:91], v[174:177], v[128:131]
	v_mfma_f32_16x16x32_bf16 v[116:119], v[112:115], v[174:177], v[116:119]
	v_mfma_f32_16x16x32_bf16 v[96:99], v[88:91], v[182:185], v[96:99]
	v_mfma_f32_16x16x32_bf16 v[92:95], v[112:115], v[182:185], v[92:95]
	v_mfma_f32_16x16x32_bf16 v[76:79], v[88:91], v[190:193], v[76:79]
	v_mfma_f32_16x16x32_bf16 v[72:75], v[112:115], v[190:193], v[72:75]
	v_mfma_f32_16x16x32_bf16 v[166:169], v[100:103], v[170:173], v[166:169]
	v_mfma_f32_16x16x32_bf16 v[156:159], v[120:123], v[170:173], v[156:159]
	v_mfma_f32_16x16x32_bf16 v[128:131], v[100:103], v[178:181], v[128:131]
	v_mfma_f32_16x16x32_bf16 v[116:119], v[120:123], v[178:181], v[116:119]
	v_mfma_f32_16x16x32_bf16 v[96:99], v[100:103], v[186:189], v[96:99]
	v_mfma_f32_16x16x32_bf16 v[92:95], v[120:123], v[186:189], v[92:95]
	v_mfma_f32_16x16x32_bf16 v[76:79], v[100:103], v[194:197], v[76:79]
	v_mfma_f32_16x16x32_bf16 v[72:75], v[120:123], v[194:197], v[72:75]
	s_setprio 0
	s_setprio 1
	v_mfma_f32_16x16x32_bf16 v[136:139], v[124:127], v[152:155], v[136:139]
	v_mfma_f32_16x16x32_bf16 v[132:135], v[144:147], v[152:155], v[132:135]
	v_mfma_f32_16x16x32_bf16 v[108:111], v[124:127], v[174:177], v[108:111]
	v_mfma_f32_16x16x32_bf16 v[104:107], v[144:147], v[174:177], v[104:107]
	v_mfma_f32_16x16x32_bf16 v[84:87], v[124:127], v[182:185], v[84:87]
	v_mfma_f32_16x16x32_bf16 v[80:83], v[144:147], v[182:185], v[80:83]
	v_mfma_f32_16x16x32_bf16 v[68:71], v[124:127], v[190:193], v[68:71]
	v_mfma_f32_16x16x32_bf16 v[64:67], v[144:147], v[190:193], v[64:67]
	v_mfma_f32_16x16x32_bf16 v[136:139], v[140:143], v[170:173], v[136:139]
	v_mfma_f32_16x16x32_bf16 v[132:135], v[148:151], v[170:173], v[132:135]
	v_mfma_f32_16x16x32_bf16 v[108:111], v[140:143], v[178:181], v[108:111]
	v_mfma_f32_16x16x32_bf16 v[104:107], v[148:151], v[178:181], v[104:107]
	v_mfma_f32_16x16x32_bf16 v[84:87], v[140:143], v[186:189], v[84:87]
	v_mfma_f32_16x16x32_bf16 v[80:83], v[148:151], v[186:189], v[80:83]
	v_mfma_f32_16x16x32_bf16 v[68:71], v[140:143], v[194:197], v[68:71]
	v_mfma_f32_16x16x32_bf16 v[64:67], v[148:151], v[194:197], v[64:67]
	s_setprio 0
	s_barrier
	s_mov_b32 m0, s40
	v_lshl_add_u64 v[206:207], v[206:207], 0, s[86:87]
	s_add_u32 s16, s16, 0x80080
	ds_read_b128 v[152:155], v232 offset:49152
	ds_read_b128 v[170:173], v232 offset:50176
	ds_read_b128 v[174:177], v232 offset:51200
	ds_read_b128 v[178:181], v232 offset:52224
	ds_read_b128 v[182:185], v232 offset:53248
	ds_read_b128 v[186:189], v232 offset:54272
	ds_read_b128 v[190:193], v232 offset:55296
	ds_read_b128 v[194:197], v232 offset:56320
	global_load_lds_dwordx4 v[206:207], off
	v_lshl_add_u64 v[206:207], v[208:209], 0, s[86:87]
	s_mov_b32 m0, s41
	s_addc_u32 s17, s17, 0
	global_load_lds_dwordx4 v[206:207], off
	v_lshl_add_u64 v[206:207], s[16:17], 0, v[160:161]
	s_mov_b32 m0, s45
	s_nop 0
	global_load_lds_dwordx4 v[206:207], off
	v_lshl_add_u64 v[206:207], s[16:17], 0, v[200:201]
	s_mov_b32 m0, s46
	s_nop 0
	global_load_lds_dwordx4 v[206:207], off
	v_lshl_add_u64 v[206:207], v[210:211], 0, s[86:87]
	s_mov_b32 m0, s42
	s_nop 0
	global_load_lds_dwordx4 v[206:207], off
	v_lshl_add_u64 v[206:207], v[212:213], 0, s[86:87]
	s_mov_b32 m0, s43
	s_nop 0
	global_load_lds_dwordx4 v[206:207], off
	s_waitcnt vmcnt(8)
	s_waitcnt lgkmcnt(0)
	s_barrier
	s_setprio 1
	s_waitcnt lgkmcnt(0)
	v_mfma_f32_16x16x32_bf16 v[60:63], v[88:91], v[152:155], v[60:63]
	v_mfma_f32_16x16x32_bf16 v[56:59], v[112:115], v[152:155], v[56:59]
	v_mfma_f32_16x16x32_bf16 v[44:47], v[88:91], v[174:177], v[44:47]
	v_mfma_f32_16x16x32_bf16 v[40:43], v[112:115], v[174:177], v[40:43]
	v_mfma_f32_16x16x32_bf16 v[28:31], v[88:91], v[182:185], v[28:31]
	v_mfma_f32_16x16x32_bf16 v[24:27], v[112:115], v[182:185], v[24:27]
	v_mfma_f32_16x16x32_bf16 v[12:15], v[88:91], v[190:193], v[12:15]
	v_mfma_f32_16x16x32_bf16 v[8:11], v[112:115], v[190:193], v[8:11]
	v_mfma_f32_16x16x32_bf16 v[60:63], v[100:103], v[170:173], v[60:63]
	v_mfma_f32_16x16x32_bf16 v[56:59], v[120:123], v[170:173], v[56:59]
	v_mfma_f32_16x16x32_bf16 v[44:47], v[100:103], v[178:181], v[44:47]
	v_mfma_f32_16x16x32_bf16 v[40:43], v[120:123], v[178:181], v[40:43]
	v_mfma_f32_16x16x32_bf16 v[28:31], v[100:103], v[186:189], v[28:31]
	v_mfma_f32_16x16x32_bf16 v[24:27], v[120:123], v[186:189], v[24:27]
	v_mfma_f32_16x16x32_bf16 v[12:15], v[100:103], v[194:197], v[12:15]
	v_mfma_f32_16x16x32_bf16 v[8:11], v[120:123], v[194:197], v[8:11]
	s_setprio 0
	s_setprio 1
	v_mfma_f32_16x16x32_bf16 v[52:55], v[124:127], v[152:155], v[52:55]
	v_mfma_f32_16x16x32_bf16 v[48:51], v[144:147], v[152:155], v[48:51]
	v_mfma_f32_16x16x32_bf16 v[36:39], v[124:127], v[174:177], v[36:39]
	v_mfma_f32_16x16x32_bf16 v[32:35], v[144:147], v[174:177], v[32:35]
	v_mfma_f32_16x16x32_bf16 v[20:23], v[124:127], v[182:185], v[20:23]
	v_mfma_f32_16x16x32_bf16 v[16:19], v[144:147], v[182:185], v[16:19]
	v_mfma_f32_16x16x32_bf16 v[4:7], v[124:127], v[190:193], v[4:7]
	v_mfma_f32_16x16x32_bf16 v[0:3], v[144:147], v[190:193], v[0:3]
	v_mfma_f32_16x16x32_bf16 v[52:55], v[140:143], v[170:173], v[52:55]
	v_mfma_f32_16x16x32_bf16 v[48:51], v[148:151], v[170:173], v[48:51]
	v_mfma_f32_16x16x32_bf16 v[36:39], v[140:143], v[178:181], v[36:39]
	v_mfma_f32_16x16x32_bf16 v[32:35], v[148:151], v[178:181], v[32:35]
	v_mfma_f32_16x16x32_bf16 v[20:23], v[140:143], v[186:189], v[20:23]
	v_mfma_f32_16x16x32_bf16 v[16:19], v[148:151], v[186:189], v[16:19]
	v_mfma_f32_16x16x32_bf16 v[4:7], v[140:143], v[194:197], v[4:7]
	v_mfma_f32_16x16x32_bf16 v[0:3], v[148:151], v[194:197], v[0:3]
	s_setprio 0
	s_barrier
	s_add_i32 s54, s54, 2
	s_add_u32 s52, s52, 0x100
	s_addc_u32 s53, s53, 0
	s_add_u32 s14, s14, 0x100
	s_addc_u32 s15, s15, 0
	s_branch .LBB0_751

.LBB0_751:
	v_add_u32_e32 v120, s13, v230
	v_add_u32_e32 v148, s29, v230
	ds_read_b128 v[88:91], v120
	ds_read_b128 v[100:103], v120 offset:1024
	ds_read_b128 v[112:115], v120 offset:2048
	ds_read_b128 v[120:123], v120 offset:3072
	ds_read_b128 v[124:127], v148
	ds_read_b128 v[140:143], v148 offset:1024
	ds_read_b128 v[144:147], v148 offset:2048
	ds_read_b128 v[148:151], v148 offset:3072
	s_add_u32 s16, s14, 0xfff80080
	s_addc_u32 s17, s15, -1
	s_cmp_eq_u32 s54, 28
	s_cselect_b32 s19, s7, s17
	s_cselect_b32 s18, s50, s16
	s_cselect_b32 s17, s5, s53
	s_cselect_b32 s16, s51, s52
	v_lshl_add_u64 v[206:207], s[14:15], 0, v[204:205]
	s_add_i32 m0, s34, 0xc000
	ds_read_b128 v[152:155], v232
	ds_read_b128 v[170:173], v232 offset:1024
	ds_read_b128 v[174:177], v232 offset:2048
	ds_read_b128 v[178:181], v232 offset:3072
	ds_read_b128 v[182:185], v232 offset:4096
	ds_read_b128 v[186:189], v232 offset:5120
	ds_read_b128 v[190:193], v232 offset:6144
	ds_read_b128 v[194:197], v232 offset:7168
	global_load_lds_dwordx4 v[206:207], off
	v_lshl_add_u64 v[206:207], s[14:15], 0, v[202:203]
	s_add_i32 m0, s34, 0xe000
	s_nop 0
	global_load_lds_dwordx4 v[206:207], off
	s_waitcnt vmcnt(8)
	s_waitcnt lgkmcnt(0)
	s_barrier
	s_setprio 1
	s_waitcnt lgkmcnt(0)
	s_nop 0
	v_mfma_f32_16x16x32_bf16 v[166:169], v[88:91], v[152:155], v[166:169]
	v_mfma_f32_16x16x32_bf16 v[156:159], v[112:115], v[152:155], v[156:159]
	v_mfma_f32_16x16x32_bf16 v[128:131], v[88:91], v[174:177], v[128:131]
	v_mfma_f32_16x16x32_bf16 v[116:119], v[112:115], v[174:177], v[116:119]
	v_mfma_f32_16x16x32_bf16 v[96:99], v[88:91], v[182:185], v[96:99]
	v_mfma_f32_16x16x32_bf16 v[92:95], v[112:115], v[182:185], v[92:95]
	v_mfma_f32_16x16x32_bf16 v[76:79], v[88:91], v[190:193], v[76:79]
	v_mfma_f32_16x16x32_bf16 v[72:75], v[112:115], v[190:193], v[72:75]
	v_mfma_f32_16x16x32_bf16 v[166:169], v[100:103], v[170:173], v[166:169]
	v_mfma_f32_16x16x32_bf16 v[156:159], v[120:123], v[170:173], v[156:159]
	v_mfma_f32_16x16x32_bf16 v[128:131], v[100:103], v[178:181], v[128:131]
	v_mfma_f32_16x16x32_bf16 v[116:119], v[120:123], v[178:181], v[116:119]
	v_mfma_f32_16x16x32_bf16 v[96:99], v[100:103], v[186:189], v[96:99]
	v_mfma_f32_16x16x32_bf16 v[92:95], v[120:123], v[186:189], v[92:95]
	v_mfma_f32_16x16x32_bf16 v[76:79], v[100:103], v[194:197], v[76:79]
	v_mfma_f32_16x16x32_bf16 v[72:75], v[120:123], v[194:197], v[72:75]
	s_setprio 0
	s_setprio 1
	v_mfma_f32_16x16x32_bf16 v[136:139], v[124:127], v[152:155], v[136:139]
	v_mfma_f32_16x16x32_bf16 v[132:135], v[144:147], v[152:155], v[132:135]
	v_mfma_f32_16x16x32_bf16 v[108:111], v[124:127], v[174:177], v[108:111]
	v_mfma_f32_16x16x32_bf16 v[104:107], v[144:147], v[174:177], v[104:107]
	v_mfma_f32_16x16x32_bf16 v[84:87], v[124:127], v[182:185], v[84:87]
	v_mfma_f32_16x16x32_bf16 v[80:83], v[144:147], v[182:185], v[80:83]
	v_mfma_f32_16x16x32_bf16 v[68:71], v[124:127], v[190:193], v[68:71]
	v_mfma_f32_16x16x32_bf16 v[64:67], v[144:147], v[190:193], v[64:67]
	v_mfma_f32_16x16x32_bf16 v[136:139], v[140:143], v[170:173], v[136:139]
	v_mfma_f32_16x16x32_bf16 v[132:135], v[148:151], v[170:173], v[132:135]
	v_mfma_f32_16x16x32_bf16 v[108:111], v[140:143], v[178:181], v[108:111]
	v_mfma_f32_16x16x32_bf16 v[104:107], v[148:151], v[178:181], v[104:107]
	v_mfma_f32_16x16x32_bf16 v[84:87], v[140:143], v[186:189], v[84:87]
	v_mfma_f32_16x16x32_bf16 v[80:83], v[148:151], v[186:189], v[80:83]
	v_mfma_f32_16x16x32_bf16 v[68:71], v[140:143], v[194:197], v[68:71]
	v_mfma_f32_16x16x32_bf16 v[64:67], v[148:151], v[194:197], v[64:67]
	s_setprio 0
	s_barrier
	s_mov_b32 m0, s27
	v_lshl_add_u64 v[206:207], s[16:17], 0, v[160:161]
	s_add_u32 s56, s16, 0x80000
	ds_read_b128 v[152:155], v232 offset:16384
	ds_read_b128 v[170:173], v232 offset:17408
	ds_read_b128 v[174:177], v232 offset:18432
	ds_read_b128 v[178:181], v232 offset:19456
	ds_read_b128 v[182:185], v232 offset:20480
	ds_read_b128 v[186:189], v232 offset:21504
	ds_read_b128 v[190:193], v232 offset:22528
	ds_read_b128 v[194:197], v232 offset:23552
	global_load_lds_dwordx4 v[206:207], off
	v_lshl_add_u64 v[208:209], s[16:17], 0, v[200:201]
	s_mov_b32 m0, s28
	s_addc_u32 s57, s17, 0
	global_load_lds_dwordx4 v[208:209], off
	v_lshl_add_u64 v[210:211], s[56:57], 0, v[160:161]
	s_mov_b32 m0, s30
	v_lshl_add_u64 v[212:213], s[18:19], 0, v[198:199]
	global_load_lds_dwordx4 v[210:211], off
	v_lshl_add_u64 v[210:211], s[56:57], 0, v[200:201]
	s_mov_b32 m0, s31
	s_nop 0
	global_load_lds_dwordx4 v[210:211], off
	v_lshl_add_u64 v[210:211], s[18:19], 0, v[162:163]
	s_mov_b32 m0, s34
	s_nop 0
	global_load_lds_dwordx4 v[210:211], off
	s_mov_b32 m0, s35
	s_nop 0
	global_load_lds_dwordx4 v[212:213], off
	s_waitcnt vmcnt(8)
	s_waitcnt lgkmcnt(0)
	s_barrier
	s_setprio 1
	s_waitcnt lgkmcnt(0)
	s_nop 0
	v_mfma_f32_16x16x32_bf16 v[60:63], v[88:91], v[152:155], v[60:63]
	v_mfma_f32_16x16x32_bf16 v[56:59], v[112:115], v[152:155], v[56:59]
	v_mfma_f32_16x16x32_bf16 v[44:47], v[88:91], v[174:177], v[44:47]
	v_mfma_f32_16x16x32_bf16 v[40:43], v[112:115], v[174:177], v[40:43]
	v_mfma_f32_16x16x32_bf16 v[28:31], v[88:91], v[182:185], v[28:31]
	v_mfma_f32_16x16x32_bf16 v[24:27], v[112:115], v[182:185], v[24:27]
	v_mfma_f32_16x16x32_bf16 v[12:15], v[88:91], v[190:193], v[12:15]
	v_mfma_f32_16x16x32_bf16 v[8:11], v[112:115], v[190:193], v[8:11]
	v_mfma_f32_16x16x32_bf16 v[60:63], v[100:103], v[170:173], v[60:63]
	v_mfma_f32_16x16x32_bf16 v[56:59], v[120:123], v[170:173], v[56:59]
	v_mfma_f32_16x16x32_bf16 v[44:47], v[100:103], v[178:181], v[44:47]
	v_mfma_f32_16x16x32_bf16 v[40:43], v[120:123], v[178:181], v[40:43]
	v_mfma_f32_16x16x32_bf16 v[28:31], v[100:103], v[186:189], v[28:31]
	v_mfma_f32_16x16x32_bf16 v[24:27], v[120:123], v[186:189], v[24:27]
	v_mfma_f32_16x16x32_bf16 v[12:15], v[100:103], v[194:197], v[12:15]
	v_mfma_f32_16x16x32_bf16 v[8:11], v[120:123], v[194:197], v[8:11]
	s_setprio 0
	s_setprio 1
	v_mfma_f32_16x16x32_bf16 v[52:55], v[124:127], v[152:155], v[52:55]
	v_mfma_f32_16x16x32_bf16 v[48:51], v[144:147], v[152:155], v[48:51]
	v_mfma_f32_16x16x32_bf16 v[36:39], v[124:127], v[174:177], v[36:39]
	v_mfma_f32_16x16x32_bf16 v[32:35], v[144:147], v[174:177], v[32:35]
	v_mfma_f32_16x16x32_bf16 v[20:23], v[124:127], v[182:185], v[20:23]
	v_mfma_f32_16x16x32_bf16 v[16:19], v[144:147], v[182:185], v[16:19]
	v_mfma_f32_16x16x32_bf16 v[4:7], v[124:127], v[190:193], v[4:7]
	v_mfma_f32_16x16x32_bf16 v[0:3], v[144:147], v[190:193], v[0:3]
	v_mfma_f32_16x16x32_bf16 v[52:55], v[140:143], v[170:173], v[52:55]
	v_mfma_f32_16x16x32_bf16 v[48:51], v[148:151], v[170:173], v[48:51]
	v_mfma_f32_16x16x32_bf16 v[36:39], v[140:143], v[178:181], v[36:39]
	v_mfma_f32_16x16x32_bf16 v[32:35], v[148:151], v[178:181], v[32:35]
	v_mfma_f32_16x16x32_bf16 v[20:23], v[140:143], v[186:189], v[20:23]
	v_mfma_f32_16x16x32_bf16 v[16:19], v[148:151], v[186:189], v[16:19]
	v_mfma_f32_16x16x32_bf16 v[4:7], v[140:143], v[194:197], v[4:7]
	v_mfma_f32_16x16x32_bf16 v[0:3], v[148:151], v[194:197], v[0:3]
	s_setprio 0
	s_barrier
	v_add_u32_e32 v120, s39, v230
	v_add_u32_e32 v148, s44, v230
	ds_read_b128 v[88:91], v120
	ds_read_b128 v[100:103], v120 offset:1024
	ds_read_b128 v[112:115], v120 offset:2048
	ds_read_b128 v[120:123], v120 offset:3072
	ds_read_b128 v[124:127], v148
	ds_read_b128 v[140:143], v148 offset:1024
	ds_read_b128 v[144:147], v148 offset:2048
	ds_read_b128 v[148:151], v148 offset:3072
	s_add_u32 s18, s18, 0x80000
	s_addc_u32 s19, s19, 0
	s_mov_b32 m0, s36
	v_lshl_add_u64 v[214:215], s[18:19], 0, v[162:163]
	ds_read_b128 v[152:155], v232 offset:32768
	ds_read_b128 v[170:173], v232 offset:33792
	ds_read_b128 v[174:177], v232 offset:34816
	ds_read_b128 v[178:181], v232 offset:35840
	ds_read_b128 v[182:185], v232 offset:36864
	ds_read_b128 v[186:189], v232 offset:37888
	ds_read_b128 v[190:193], v232 offset:38912
	ds_read_b128 v[194:197], v232 offset:39936
	global_load_lds_dwordx4 v[214:215], off
	v_lshl_add_u64 v[214:215], s[18:19], 0, v[198:199]
	s_mov_b32 m0, s37
	s_nop 0
	global_load_lds_dwordx4 v[214:215], off
	s_waitcnt vmcnt(8)
	s_waitcnt lgkmcnt(0)
	s_barrier
	s_setprio 1
	s_waitcnt lgkmcnt(0)
	s_nop 0
	v_mfma_f32_16x16x32_bf16 v[166:169], v[88:91], v[152:155], v[166:169]
	v_mfma_f32_16x16x32_bf16 v[156:159], v[112:115], v[152:155], v[156:159]
	v_mfma_f32_16x16x32_bf16 v[128:131], v[88:91], v[174:177], v[128:131]
	v_mfma_f32_16x16x32_bf16 v[116:119], v[112:115], v[174:177], v[116:119]
	v_mfma_f32_16x16x32_bf16 v[96:99], v[88:91], v[182:185], v[96:99]
	v_mfma_f32_16x16x32_bf16 v[92:95], v[112:115], v[182:185], v[92:95]
	v_mfma_f32_16x16x32_bf16 v[76:79], v[88:91], v[190:193], v[76:79]
	v_mfma_f32_16x16x32_bf16 v[72:75], v[112:115], v[190:193], v[72:75]
	v_mfma_f32_16x16x32_bf16 v[166:169], v[100:103], v[170:173], v[166:169]
	v_mfma_f32_16x16x32_bf16 v[156:159], v[120:123], v[170:173], v[156:159]
	v_mfma_f32_16x16x32_bf16 v[128:131], v[100:103], v[178:181], v[128:131]
	v_mfma_f32_16x16x32_bf16 v[116:119], v[120:123], v[178:181], v[116:119]
	v_mfma_f32_16x16x32_bf16 v[96:99], v[100:103], v[186:189], v[96:99]
	v_mfma_f32_16x16x32_bf16 v[92:95], v[120:123], v[186:189], v[92:95]
	v_mfma_f32_16x16x32_bf16 v[76:79], v[100:103], v[194:197], v[76:79]
	v_mfma_f32_16x16x32_bf16 v[72:75], v[120:123], v[194:197], v[72:75]
	s_setprio 0
	s_setprio 1
	v_mfma_f32_16x16x32_bf16 v[136:139], v[124:127], v[152:155], v[136:139]
	v_mfma_f32_16x16x32_bf16 v[132:135], v[144:147], v[152:155], v[132:135]
	v_mfma_f32_16x16x32_bf16 v[108:111], v[124:127], v[174:177], v[108:111]
	v_mfma_f32_16x16x32_bf16 v[104:107], v[144:147], v[174:177], v[104:107]
	v_mfma_f32_16x16x32_bf16 v[84:87], v[124:127], v[182:185], v[84:87]
	v_mfma_f32_16x16x32_bf16 v[80:83], v[144:147], v[182:185], v[80:83]
	v_mfma_f32_16x16x32_bf16 v[68:71], v[124:127], v[190:193], v[68:71]
	v_mfma_f32_16x16x32_bf16 v[64:67], v[144:147], v[190:193], v[64:67]
	v_mfma_f32_16x16x32_bf16 v[136:139], v[140:143], v[170:173], v[136:139]
	v_mfma_f32_16x16x32_bf16 v[132:135], v[148:151], v[170:173], v[132:135]
	v_mfma_f32_16x16x32_bf16 v[108:111], v[140:143], v[178:181], v[108:111]
	v_mfma_f32_16x16x32_bf16 v[104:107], v[148:151], v[178:181], v[104:107]
	v_mfma_f32_16x16x32_bf16 v[84:87], v[140:143], v[186:189], v[84:87]
	v_mfma_f32_16x16x32_bf16 v[80:83], v[148:151], v[186:189], v[80:83]
	v_mfma_f32_16x16x32_bf16 v[68:71], v[140:143], v[194:197], v[68:71]
	v_mfma_f32_16x16x32_bf16 v[64:67], v[148:151], v[194:197], v[64:67]
	s_setprio 0
	s_barrier
	s_mov_b32 m0, s40
	v_lshl_add_u64 v[206:207], v[206:207], 0, s[86:87]
	s_add_u32 s16, s16, 0x80080
	ds_read_b128 v[152:155], v232 offset:49152
	ds_read_b128 v[170:173], v232 offset:50176
	ds_read_b128 v[174:177], v232 offset:51200
	ds_read_b128 v[178:181], v232 offset:52224
	ds_read_b128 v[182:185], v232 offset:53248
	ds_read_b128 v[186:189], v232 offset:54272
	ds_read_b128 v[190:193], v232 offset:55296
	ds_read_b128 v[194:197], v232 offset:56320
	global_load_lds_dwordx4 v[206:207], off
	v_lshl_add_u64 v[206:207], v[208:209], 0, s[86:87]
	s_mov_b32 m0, s41
	s_addc_u32 s17, s17, 0
	global_load_lds_dwordx4 v[206:207], off
	v_lshl_add_u64 v[206:207], s[16:17], 0, v[160:161]
	s_mov_b32 m0, s45
	s_nop 0
	global_load_lds_dwordx4 v[206:207], off
	v_lshl_add_u64 v[206:207], s[16:17], 0, v[200:201]
	s_mov_b32 m0, s46
	s_nop 0
	global_load_lds_dwordx4 v[206:207], off
	v_lshl_add_u64 v[206:207], v[210:211], 0, s[86:87]
	s_mov_b32 m0, s42
	s_nop 0
	global_load_lds_dwordx4 v[206:207], off
	v_lshl_add_u64 v[206:207], v[212:213], 0, s[86:87]
	s_mov_b32 m0, s43
	s_nop 0
	global_load_lds_dwordx4 v[206:207], off
	s_waitcnt vmcnt(8)
	s_waitcnt lgkmcnt(0)
	s_barrier
	s_setprio 1
	s_waitcnt lgkmcnt(0)
	v_mfma_f32_16x16x32_bf16 v[60:63], v[88:91], v[152:155], v[60:63]
	v_mfma_f32_16x16x32_bf16 v[56:59], v[112:115], v[152:155], v[56:59]
	v_mfma_f32_16x16x32_bf16 v[44:47], v[88:91], v[174:177], v[44:47]
	v_mfma_f32_16x16x32_bf16 v[40:43], v[112:115], v[174:177], v[40:43]
	v_mfma_f32_16x16x32_bf16 v[28:31], v[88:91], v[182:185], v[28:31]
	v_mfma_f32_16x16x32_bf16 v[24:27], v[112:115], v[182:185], v[24:27]
	v_mfma_f32_16x16x32_bf16 v[12:15], v[88:91], v[190:193], v[12:15]
	v_mfma_f32_16x16x32_bf16 v[8:11], v[112:115], v[190:193], v[8:11]
	v_mfma_f32_16x16x32_bf16 v[60:63], v[100:103], v[170:173], v[60:63]
	v_mfma_f32_16x16x32_bf16 v[56:59], v[120:123], v[170:173], v[56:59]
	v_mfma_f32_16x16x32_bf16 v[44:47], v[100:103], v[178:181], v[44:47]
	v_mfma_f32_16x16x32_bf16 v[40:43], v[120:123], v[178:181], v[40:43]
	v_mfma_f32_16x16x32_bf16 v[28:31], v[100:103], v[186:189], v[28:31]
	v_mfma_f32_16x16x32_bf16 v[24:27], v[120:123], v[186:189], v[24:27]
	v_mfma_f32_16x16x32_bf16 v[12:15], v[100:103], v[194:197], v[12:15]
	v_mfma_f32_16x16x32_bf16 v[8:11], v[120:123], v[194:197], v[8:11]
	s_setprio 0
	s_setprio 1
	v_mfma_f32_16x16x32_bf16 v[52:55], v[124:127], v[152:155], v[52:55]
	v_mfma_f32_16x16x32_bf16 v[48:51], v[144:147], v[152:155], v[48:51]
	v_mfma_f32_16x16x32_bf16 v[36:39], v[124:127], v[174:177], v[36:39]
	v_mfma_f32_16x16x32_bf16 v[32:35], v[144:147], v[174:177], v[32:35]
	v_mfma_f32_16x16x32_bf16 v[20:23], v[124:127], v[182:185], v[20:23]
	v_mfma_f32_16x16x32_bf16 v[16:19], v[144:147], v[182:185], v[16:19]
	v_mfma_f32_16x16x32_bf16 v[4:7], v[124:127], v[190:193], v[4:7]
	v_mfma_f32_16x16x32_bf16 v[0:3], v[144:147], v[190:193], v[0:3]
	v_mfma_f32_16x16x32_bf16 v[52:55], v[140:143], v[170:173], v[52:55]
	v_mfma_f32_16x16x32_bf16 v[48:51], v[148:151], v[170:173], v[48:51]
	v_mfma_f32_16x16x32_bf16 v[36:39], v[140:143], v[178:181], v[36:39]
	v_mfma_f32_16x16x32_bf16 v[32:35], v[148:151], v[178:181], v[32:35]
	v_mfma_f32_16x16x32_bf16 v[20:23], v[140:143], v[186:189], v[20:23]
	v_mfma_f32_16x16x32_bf16 v[16:19], v[148:151], v[186:189], v[16:19]
	v_mfma_f32_16x16x32_bf16 v[4:7], v[140:143], v[194:197], v[4:7]
	v_mfma_f32_16x16x32_bf16 v[0:3], v[148:151], v[194:197], v[0:3]
	s_setprio 0
	s_barrier
	s_add_i32 s54, s54, 2
	s_add_u32 s52, s52, 0x100
	s_addc_u32 s53, s53, 0
	s_add_u32 s14, s14, 0x100
	s_addc_u32 s15, s15, 0
	s_cmp_gt_u32 s54, 29
	s_cbranch_scc0 .LBB0_751
	v_lshl_or_b32 v90, s49, 8, v231
	v_lshl_add_u32 v88, s12, 8, v165
	v_ashrrev_i32_e32 v91, 31, v90
	v_lshlrev_b64 v[206:207], 1, v[90:91]
	v_ashrrev_i32_e32 v89, 31, v88
	v_lshl_add_u64 v[90:91], s[0:1], 0, v[206:207]
	v_lshlrev_b64 v[222:223], 12, v[88:89]
	v_lshl_add_u64 v[100:101], v[90:91], 0, v[222:223]
	global_load_dwordx4 v[194:197], v[100:101], off nt
	global_load_dwordx4 v[190:193], v[100:101], off offset:256 nt
	v_or_b32_e32 v100, 16, v88
	v_ashrrev_i32_e32 v101, 31, v100
	v_lshlrev_b64 v[220:221], 12, v[100:101]
	v_lshl_add_u64 v[100:101], v[90:91], 0, v[220:221]
	global_load_dwordx4 v[186:189], v[100:101], off nt
	global_load_dwordx4 v[182:185], v[100:101], off offset:256 nt
	v_or_b32_e32 v100, 32, v88
	v_ashrrev_i32_e32 v101, 31, v100
	v_lshlrev_b64 v[218:219], 12, v[100:101]
	v_lshl_add_u64 v[100:101], v[90:91], 0, v[218:219]
	global_load_dwordx4 v[178:181], v[100:101], off nt
	global_load_dwordx4 v[174:177], v[100:101], off offset:256 nt
	v_or_b32_e32 v88, 48, v88
	v_ashrrev_i32_e32 v89, 31, v88
	v_lshlrev_b64 v[216:217], 12, v[88:89]
	v_lshl_add_u64 v[88:89], v[90:91], 0, v[216:217]
	global_load_dwordx4 v[170:173], v[88:89], off nt
	global_load_dwordx4 v[152:155], v[88:89], off offset:256 nt
	v_lshl_add_u64 v[214:215], v[222:223], 0, s[58:59]
	v_lshl_add_u64 v[88:89], v[90:91], 0, v[214:215]
	global_load_dwordx4 v[148:151], v[88:89], off nt
	global_load_dwordx4 v[144:147], v[88:89], off offset:256 nt
	s_mov_b64 s[14:15], 0x90000
	v_lshl_add_u64 v[212:213], v[222:223], 0, s[14:15]
	v_lshl_add_u64 v[88:89], v[90:91], 0, v[212:213]
	global_load_dwordx4 v[140:143], v[88:89], off nt
	global_load_dwordx4 v[124:127], v[88:89], off offset:256 nt
	s_mov_b64 s[14:15], 0xa0000
	v_lshl_add_u64 v[210:211], v[222:223], 0, s[14:15]
	v_lshl_add_u64 v[88:89], v[90:91], 0, v[210:211]
	global_load_dwordx4 v[120:123], v[88:89], off nt
	global_load_dwordx4 v[112:115], v[88:89], off offset:256 nt
	s_mov_b64 s[14:15], 0xb0000
	v_lshl_add_u64 v[208:209], v[222:223], 0, s[14:15]
	v_lshl_add_u64 v[88:89], v[90:91], 0, v[208:209]
	global_load_dwordx4 v[100:103], v[88:89], off nt
	s_nop 0
	global_load_dwordx4 v[88:91], v[88:89], off offset:256 nt
	s_and_b64 vcc, exec, s[2:3]
	s_mov_b32 s49, s4
	s_mov_b32 s12, s6
	s_mov_b64 s[14:15], s[10:11]
	s_mov_b64 s[16:17], s[8:9]
	s_waitcnt vmcnt(0)
	v_cvt_f32_f16_e32 v224, v194
	v_cvt_f32_f16_sdwa v225, v194 dst_sel:DWORD dst_unused:UNUSED_PAD src0_sel:WORD_1
	v_pk_add_f32 v[166:167], v[166:167], v[224:225]
	s_nop 0
	v_cvt_pk_f16_f32 v194, v166, v167
	v_cvt_f32_f16_e32 v166, v196
	v_cvt_f32_f16_sdwa v167, v196 dst_sel:DWORD dst_unused:UNUSED_PAD src0_sel:WORD_1
	v_pk_add_f32 v[156:157], v[156:157], v[166:167]
	s_nop 0
	v_cvt_pk_f16_f32 v196, v156, v157
	v_cvt_f32_f16_e32 v156, v195
	v_cvt_f32_f16_sdwa v157, v195 dst_sel:DWORD dst_unused:UNUSED_PAD src0_sel:WORD_1
	v_pk_add_f32 v[156:157], v[168:169], v[156:157]
	s_nop 0
	v_cvt_pk_f16_f32 v195, v156, v157
	v_cvt_f32_f16_e32 v156, v197
	v_cvt_f32_f16_sdwa v157, v197 dst_sel:DWORD dst_unused:UNUSED_PAD src0_sel:WORD_1
	v_pk_add_f32 v[156:157], v[158:159], v[156:157]
	s_nop 0
	v_cvt_pk_f16_f32 v197, v156, v157
	v_lshl_add_u64 v[156:157], s[0:1], 0, v[222:223]
	v_lshl_add_u64 v[166:167], v[156:157], 0, v[206:207]
	v_cvt_f32_f16_e32 v156, v190
	v_cvt_f32_f16_sdwa v157, v190 dst_sel:DWORD dst_unused:UNUSED_PAD src0_sel:WORD_1
	global_store_dwordx4 v[166:167], v[194:197], off
	v_pk_add_f32 v[136:137], v[136:137], v[156:157]
	s_nop 0
	v_cvt_pk_f16_f32 v156, v136, v137
	v_cvt_f32_f16_e32 v136, v192
	v_cvt_f32_f16_sdwa v137, v192 dst_sel:DWORD dst_unused:UNUSED_PAD src0_sel:WORD_1
	v_pk_add_f32 v[132:133], v[132:133], v[136:137]
	s_nop 0
	v_cvt_pk_f16_f32 v158, v132, v133
	v_cvt_f32_f16_e32 v132, v191
	v_cvt_f32_f16_sdwa v133, v191 dst_sel:DWORD dst_unused:UNUSED_PAD src0_sel:WORD_1
	v_pk_add_f32 v[132:133], v[138:139], v[132:133]
	s_nop 0
	v_cvt_pk_f16_f32 v157, v132, v133
	v_cvt_f32_f16_e32 v132, v193
	v_cvt_f32_f16_sdwa v133, v193 dst_sel:DWORD dst_unused:UNUSED_PAD src0_sel:WORD_1
	v_pk_add_f32 v[132:133], v[134:135], v[132:133]
	s_nop 0
	v_cvt_pk_f16_f32 v159, v132, v133
	v_cvt_f32_f16_e32 v132, v186
	v_cvt_f32_f16_sdwa v133, v186 dst_sel:DWORD dst_unused:UNUSED_PAD src0_sel:WORD_1
	global_store_dwordx4 v[166:167], v[156:159], off offset:256
	v_pk_add_f32 v[128:129], v[128:129], v[132:133]
	s_nop 0
	v_cvt_pk_f16_f32 v132, v128, v129
	v_cvt_f32_f16_e32 v128, v188
	v_cvt_f32_f16_sdwa v129, v188 dst_sel:DWORD dst_unused:UNUSED_PAD src0_sel:WORD_1
	v_pk_add_f32 v[116:117], v[116:117], v[128:129]
	s_nop 0
	v_cvt_pk_f16_f32 v134, v116, v117
	v_cvt_f32_f16_e32 v116, v187
	v_cvt_f32_f16_sdwa v117, v187 dst_sel:DWORD dst_unused:UNUSED_PAD src0_sel:WORD_1
	v_pk_add_f32 v[116:117], v[130:131], v[116:117]
	s_nop 0
	v_cvt_pk_f16_f32 v133, v116, v117
	v_cvt_f32_f16_e32 v116, v189
	v_cvt_f32_f16_sdwa v117, v189 dst_sel:DWORD dst_unused:UNUSED_PAD src0_sel:WORD_1
	v_pk_add_f32 v[116:117], v[118:119], v[116:117]
	s_nop 0
	v_cvt_pk_f16_f32 v135, v116, v117
	v_lshl_add_u64 v[116:117], s[0:1], 0, v[220:221]
	v_lshl_add_u64 v[128:129], v[116:117], 0, v[206:207]
	v_cvt_f32_f16_e32 v116, v182
	v_cvt_f32_f16_sdwa v117, v182 dst_sel:DWORD dst_unused:UNUSED_PAD src0_sel:WORD_1
	global_store_dwordx4 v[128:129], v[132:135], off
	v_pk_add_f32 v[108:109], v[108:109], v[116:117]
	s_nop 0
	v_cvt_pk_f16_f32 v116, v108, v109
	v_cvt_f32_f16_e32 v108, v184
	v_cvt_f32_f16_sdwa v109, v184 dst_sel:DWORD dst_unused:UNUSED_PAD src0_sel:WORD_1
	v_pk_add_f32 v[104:105], v[104:105], v[108:109]
	s_nop 0
	v_cvt_pk_f16_f32 v118, v104, v105
	v_cvt_f32_f16_e32 v104, v183
	v_cvt_f32_f16_sdwa v105, v183 dst_sel:DWORD dst_unused:UNUSED_PAD src0_sel:WORD_1
	v_pk_add_f32 v[104:105], v[110:111], v[104:105]
	s_nop 0
	v_cvt_pk_f16_f32 v117, v104, v105
	v_cvt_f32_f16_e32 v104, v185
	v_cvt_f32_f16_sdwa v105, v185 dst_sel:DWORD dst_unused:UNUSED_PAD src0_sel:WORD_1
	v_pk_add_f32 v[104:105], v[106:107], v[104:105]
	s_nop 0
	v_cvt_pk_f16_f32 v119, v104, v105
	v_cvt_f32_f16_e32 v104, v178
	v_cvt_f32_f16_sdwa v105, v178 dst_sel:DWORD dst_unused:UNUSED_PAD src0_sel:WORD_1
	global_store_dwordx4 v[128:129], v[116:119], off offset:256
	v_pk_add_f32 v[96:97], v[96:97], v[104:105]
	s_nop 0
	v_cvt_pk_f16_f32 v104, v96, v97
	v_cvt_f32_f16_e32 v96, v180
	v_cvt_f32_f16_sdwa v97, v180 dst_sel:DWORD dst_unused:UNUSED_PAD src0_sel:WORD_1
	v_pk_add_f32 v[92:93], v[92:93], v[96:97]
	s_nop 0
	v_cvt_pk_f16_f32 v106, v92, v93
	v_cvt_f32_f16_e32 v92, v179
	v_cvt_f32_f16_sdwa v93, v179 dst_sel:DWORD dst_unused:UNUSED_PAD src0_sel:WORD_1
	v_pk_add_f32 v[92:93], v[98:99], v[92:93]
	s_nop 0
	v_cvt_pk_f16_f32 v105, v92, v93
	v_cvt_f32_f16_e32 v92, v181
	v_cvt_f32_f16_sdwa v93, v181 dst_sel:DWORD dst_unused:UNUSED_PAD src0_sel:WORD_1
	v_pk_add_f32 v[92:93], v[94:95], v[92:93]
	s_nop 0
	v_cvt_pk_f16_f32 v107, v92, v93
	v_lshl_add_u64 v[92:93], s[0:1], 0, v[218:219]
	v_lshl_add_u64 v[96:97], v[92:93], 0, v[206:207]
	v_cvt_f32_f16_e32 v92, v174
	v_cvt_f32_f16_sdwa v93, v174 dst_sel:DWORD dst_unused:UNUSED_PAD src0_sel:WORD_1
	global_store_dwordx4 v[96:97], v[104:107], off
	v_pk_add_f32 v[84:85], v[84:85], v[92:93]
	s_nop 0
	v_cvt_pk_f16_f32 v92, v84, v85
	v_cvt_f32_f16_e32 v84, v176
	v_cvt_f32_f16_sdwa v85, v176 dst_sel:DWORD dst_unused:UNUSED_PAD src0_sel:WORD_1
	v_pk_add_f32 v[80:81], v[80:81], v[84:85]
	s_nop 0
	v_cvt_pk_f16_f32 v94, v80, v81
	v_cvt_f32_f16_e32 v80, v175
	v_cvt_f32_f16_sdwa v81, v175 dst_sel:DWORD dst_unused:UNUSED_PAD src0_sel:WORD_1
	v_pk_add_f32 v[80:81], v[86:87], v[80:81]
	s_nop 0
	v_cvt_pk_f16_f32 v93, v80, v81
	v_cvt_f32_f16_e32 v80, v177
	v_cvt_f32_f16_sdwa v81, v177 dst_sel:DWORD dst_unused:UNUSED_PAD src0_sel:WORD_1
	v_pk_add_f32 v[80:81], v[82:83], v[80:81]
	s_nop 0
	v_cvt_pk_f16_f32 v95, v80, v81
	v_cvt_f32_f16_e32 v80, v170
	v_cvt_f32_f16_sdwa v81, v170 dst_sel:DWORD dst_unused:UNUSED_PAD src0_sel:WORD_1
	global_store_dwordx4 v[96:97], v[92:95], off offset:256
	v_pk_add_f32 v[76:77], v[76:77], v[80:81]
	s_nop 0
	v_cvt_pk_f16_f32 v80, v76, v77
	v_cvt_f32_f16_e32 v76, v172
	v_cvt_f32_f16_sdwa v77, v172 dst_sel:DWORD dst_unused:UNUSED_PAD src0_sel:WORD_1
	v_pk_add_f32 v[72:73], v[72:73], v[76:77]
	s_nop 0
	v_cvt_pk_f16_f32 v82, v72, v73
	v_cvt_f32_f16_e32 v72, v171
	v_cvt_f32_f16_sdwa v73, v171 dst_sel:DWORD dst_unused:UNUSED_PAD src0_sel:WORD_1
	v_pk_add_f32 v[72:73], v[78:79], v[72:73]
	s_nop 0
	v_cvt_pk_f16_f32 v81, v72, v73
	v_cvt_f32_f16_e32 v72, v173
	v_cvt_f32_f16_sdwa v73, v173 dst_sel:DWORD dst_unused:UNUSED_PAD src0_sel:WORD_1
	v_pk_add_f32 v[72:73], v[74:75], v[72:73]
	s_nop 0
	v_cvt_pk_f16_f32 v83, v72, v73
	v_lshl_add_u64 v[72:73], s[0:1], 0, v[216:217]
	v_lshl_add_u64 v[76:77], v[72:73], 0, v[206:207]
	v_cvt_f32_f16_e32 v72, v152
	v_cvt_f32_f16_sdwa v73, v152 dst_sel:DWORD dst_unused:UNUSED_PAD src0_sel:WORD_1
	global_store_dwordx4 v[76:77], v[80:83], off
	v_pk_add_f32 v[68:69], v[68:69], v[72:73]
	s_nop 0
	v_cvt_pk_f16_f32 v72, v68, v69
	v_cvt_f32_f16_e32 v68, v154
	v_cvt_f32_f16_sdwa v69, v154 dst_sel:DWORD dst_unused:UNUSED_PAD src0_sel:WORD_1
	v_pk_add_f32 v[64:65], v[64:65], v[68:69]
	s_nop 0
	v_cvt_pk_f16_f32 v74, v64, v65
	v_cvt_f32_f16_e32 v64, v153
	v_cvt_f32_f16_sdwa v65, v153 dst_sel:DWORD dst_unused:UNUSED_PAD src0_sel:WORD_1
	v_pk_add_f32 v[64:65], v[70:71], v[64:65]
	s_nop 0
	v_cvt_pk_f16_f32 v73, v64, v65
	v_cvt_f32_f16_e32 v64, v155
	v_cvt_f32_f16_sdwa v65, v155 dst_sel:DWORD dst_unused:UNUSED_PAD src0_sel:WORD_1
	v_pk_add_f32 v[64:65], v[66:67], v[64:65]
	s_nop 0
	v_cvt_pk_f16_f32 v75, v64, v65
	v_cvt_f32_f16_e32 v64, v148
	v_cvt_f32_f16_sdwa v65, v148 dst_sel:DWORD dst_unused:UNUSED_PAD src0_sel:WORD_1
	global_store_dwordx4 v[76:77], v[72:75], off offset:256
	v_pk_add_f32 v[60:61], v[60:61], v[64:65]
	s_nop 0
	v_cvt_pk_f16_f32 v64, v60, v61
	v_cvt_f32_f16_e32 v60, v150
	v_cvt_f32_f16_sdwa v61, v150 dst_sel:DWORD dst_unused:UNUSED_PAD src0_sel:WORD_1
	v_pk_add_f32 v[56:57], v[56:57], v[60:61]
	s_nop 0
	v_cvt_pk_f16_f32 v66, v56, v57
	v_cvt_f32_f16_e32 v56, v149
	v_cvt_f32_f16_sdwa v57, v149 dst_sel:DWORD dst_unused:UNUSED_PAD src0_sel:WORD_1
	v_pk_add_f32 v[56:57], v[62:63], v[56:57]
	s_nop 0
	v_cvt_pk_f16_f32 v65, v56, v57
	v_cvt_f32_f16_e32 v56, v151
	v_cvt_f32_f16_sdwa v57, v151 dst_sel:DWORD dst_unused:UNUSED_PAD src0_sel:WORD_1
	v_pk_add_f32 v[56:57], v[58:59], v[56:57]
	s_nop 0
	v_cvt_pk_f16_f32 v67, v56, v57
	v_lshl_add_u64 v[56:57], s[0:1], 0, v[214:215]
	v_lshl_add_u64 v[60:61], v[56:57], 0, v[206:207]
	v_cvt_f32_f16_e32 v56, v144
	v_cvt_f32_f16_sdwa v57, v144 dst_sel:DWORD dst_unused:UNUSED_PAD src0_sel:WORD_1
	global_store_dwordx4 v[60:61], v[64:67], off
	v_pk_add_f32 v[52:53], v[52:53], v[56:57]
	s_nop 0
	v_cvt_pk_f16_f32 v56, v52, v53
	v_cvt_f32_f16_e32 v52, v146
	v_cvt_f32_f16_sdwa v53, v146 dst_sel:DWORD dst_unused:UNUSED_PAD src0_sel:WORD_1
	v_pk_add_f32 v[48:49], v[48:49], v[52:53]
	s_nop 0
	v_cvt_pk_f16_f32 v58, v48, v49
	v_cvt_f32_f16_e32 v48, v145
	v_cvt_f32_f16_sdwa v49, v145 dst_sel:DWORD dst_unused:UNUSED_PAD src0_sel:WORD_1
	v_pk_add_f32 v[48:49], v[54:55], v[48:49]
	s_nop 0
	v_cvt_pk_f16_f32 v57, v48, v49
	v_cvt_f32_f16_e32 v48, v147
	v_cvt_f32_f16_sdwa v49, v147 dst_sel:DWORD dst_unused:UNUSED_PAD src0_sel:WORD_1
	v_pk_add_f32 v[48:49], v[50:51], v[48:49]
	s_nop 0
	v_cvt_pk_f16_f32 v59, v48, v49
	v_cvt_f32_f16_e32 v48, v140
	v_cvt_f32_f16_sdwa v49, v140 dst_sel:DWORD dst_unused:UNUSED_PAD src0_sel:WORD_1
	global_store_dwordx4 v[60:61], v[56:59], off offset:256
	v_pk_add_f32 v[44:45], v[44:45], v[48:49]
	s_nop 0
	v_cvt_pk_f16_f32 v48, v44, v45
	v_cvt_f32_f16_e32 v44, v142
	v_cvt_f32_f16_sdwa v45, v142 dst_sel:DWORD dst_unused:UNUSED_PAD src0_sel:WORD_1
	v_pk_add_f32 v[40:41], v[40:41], v[44:45]
	s_nop 0
	v_cvt_pk_f16_f32 v50, v40, v41
	v_cvt_f32_f16_e32 v40, v141
	v_cvt_f32_f16_sdwa v41, v141 dst_sel:DWORD dst_unused:UNUSED_PAD src0_sel:WORD_1
	v_pk_add_f32 v[40:41], v[46:47], v[40:41]
	s_nop 0
	v_cvt_pk_f16_f32 v49, v40, v41
	v_cvt_f32_f16_e32 v40, v143
	v_cvt_f32_f16_sdwa v41, v143 dst_sel:DWORD dst_unused:UNUSED_PAD src0_sel:WORD_1
	v_pk_add_f32 v[40:41], v[42:43], v[40:41]
	s_nop 0
	v_cvt_pk_f16_f32 v51, v40, v41
	v_lshl_add_u64 v[40:41], s[0:1], 0, v[212:213]
	v_lshl_add_u64 v[44:45], v[40:41], 0, v[206:207]
	v_cvt_f32_f16_e32 v40, v124
	v_cvt_f32_f16_sdwa v41, v124 dst_sel:DWORD dst_unused:UNUSED_PAD src0_sel:WORD_1
	global_store_dwordx4 v[44:45], v[48:51], off
	v_pk_add_f32 v[36:37], v[36:37], v[40:41]
	s_nop 0
	v_cvt_pk_f16_f32 v40, v36, v37
	v_cvt_f32_f16_e32 v36, v126
	v_cvt_f32_f16_sdwa v37, v126 dst_sel:DWORD dst_unused:UNUSED_PAD src0_sel:WORD_1
	v_pk_add_f32 v[32:33], v[32:33], v[36:37]
	s_nop 0
	v_cvt_pk_f16_f32 v42, v32, v33
	v_cvt_f32_f16_e32 v32, v125
	v_cvt_f32_f16_sdwa v33, v125 dst_sel:DWORD dst_unused:UNUSED_PAD src0_sel:WORD_1
	v_pk_add_f32 v[32:33], v[38:39], v[32:33]
	s_nop 0
	v_cvt_pk_f16_f32 v41, v32, v33
	v_cvt_f32_f16_e32 v32, v127
	v_cvt_f32_f16_sdwa v33, v127 dst_sel:DWORD dst_unused:UNUSED_PAD src0_sel:WORD_1
	v_pk_add_f32 v[32:33], v[34:35], v[32:33]
	s_nop 0
	v_cvt_pk_f16_f32 v43, v32, v33
	v_cvt_f32_f16_e32 v32, v120
	v_cvt_f32_f16_sdwa v33, v120 dst_sel:DWORD dst_unused:UNUSED_PAD src0_sel:WORD_1
	global_store_dwordx4 v[44:45], v[40:43], off offset:256
	v_pk_add_f32 v[28:29], v[28:29], v[32:33]
	s_nop 0
	v_cvt_pk_f16_f32 v32, v28, v29
	v_cvt_f32_f16_e32 v28, v122
	v_cvt_f32_f16_sdwa v29, v122 dst_sel:DWORD dst_unused:UNUSED_PAD src0_sel:WORD_1
	v_pk_add_f32 v[24:25], v[24:25], v[28:29]
	s_nop 0
	v_cvt_pk_f16_f32 v34, v24, v25
	v_cvt_f32_f16_e32 v24, v121
	v_cvt_f32_f16_sdwa v25, v121 dst_sel:DWORD dst_unused:UNUSED_PAD src0_sel:WORD_1
	v_pk_add_f32 v[24:25], v[30:31], v[24:25]
	s_nop 0
	v_cvt_pk_f16_f32 v33, v24, v25
	v_cvt_f32_f16_e32 v24, v123
	v_cvt_f32_f16_sdwa v25, v123 dst_sel:DWORD dst_unused:UNUSED_PAD src0_sel:WORD_1
	v_pk_add_f32 v[24:25], v[26:27], v[24:25]
	s_nop 0
	v_cvt_pk_f16_f32 v35, v24, v25
	v_lshl_add_u64 v[24:25], s[0:1], 0, v[210:211]
	v_lshl_add_u64 v[28:29], v[24:25], 0, v[206:207]
	v_cvt_f32_f16_e32 v24, v112
	v_cvt_f32_f16_sdwa v25, v112 dst_sel:DWORD dst_unused:UNUSED_PAD src0_sel:WORD_1
	global_store_dwordx4 v[28:29], v[32:35], off
	v_pk_add_f32 v[20:21], v[20:21], v[24:25]
	s_nop 0
	v_cvt_pk_f16_f32 v24, v20, v21
	v_cvt_f32_f16_e32 v20, v114
	v_cvt_f32_f16_sdwa v21, v114 dst_sel:DWORD dst_unused:UNUSED_PAD src0_sel:WORD_1
	v_pk_add_f32 v[16:17], v[16:17], v[20:21]
	s_nop 0
	v_cvt_pk_f16_f32 v26, v16, v17
	v_cvt_f32_f16_e32 v16, v113
	v_cvt_f32_f16_sdwa v17, v113 dst_sel:DWORD dst_unused:UNUSED_PAD src0_sel:WORD_1
	v_pk_add_f32 v[16:17], v[22:23], v[16:17]
	s_nop 0
	v_cvt_pk_f16_f32 v25, v16, v17
	v_cvt_f32_f16_e32 v16, v115
	v_cvt_f32_f16_sdwa v17, v115 dst_sel:DWORD dst_unused:UNUSED_PAD src0_sel:WORD_1
	v_pk_add_f32 v[16:17], v[18:19], v[16:17]
	s_nop 0
	v_cvt_pk_f16_f32 v27, v16, v17
	v_cvt_f32_f16_e32 v16, v100
	v_cvt_f32_f16_sdwa v17, v100 dst_sel:DWORD dst_unused:UNUSED_PAD src0_sel:WORD_1
	global_store_dwordx4 v[28:29], v[24:27], off offset:256
	v_pk_add_f32 v[12:13], v[12:13], v[16:17]
	s_nop 0
	v_cvt_pk_f16_f32 v16, v12, v13
	v_cvt_f32_f16_e32 v12, v102
	v_cvt_f32_f16_sdwa v13, v102 dst_sel:DWORD dst_unused:UNUSED_PAD src0_sel:WORD_1
	v_pk_add_f32 v[8:9], v[8:9], v[12:13]
	s_nop 0
	v_cvt_pk_f16_f32 v18, v8, v9
	v_cvt_f32_f16_e32 v8, v101
	v_cvt_f32_f16_sdwa v9, v101 dst_sel:DWORD dst_unused:UNUSED_PAD src0_sel:WORD_1
	v_pk_add_f32 v[8:9], v[14:15], v[8:9]
	s_nop 0
	v_cvt_pk_f16_f32 v17, v8, v9
	v_cvt_f32_f16_e32 v8, v103
	v_cvt_f32_f16_sdwa v9, v103 dst_sel:DWORD dst_unused:UNUSED_PAD src0_sel:WORD_1
	v_pk_add_f32 v[8:9], v[10:11], v[8:9]
	s_nop 0
	v_cvt_pk_f16_f32 v19, v8, v9
	v_lshl_add_u64 v[8:9], s[0:1], 0, v[208:209]
	v_lshl_add_u64 v[12:13], v[8:9], 0, v[206:207]
	v_cvt_f32_f16_e32 v8, v88
	v_cvt_f32_f16_sdwa v9, v88 dst_sel:DWORD dst_unused:UNUSED_PAD src0_sel:WORD_1
	global_store_dwordx4 v[12:13], v[16:19], off
	v_pk_add_f32 v[4:5], v[4:5], v[8:9]
	s_nop 0
	v_cvt_pk_f16_f32 v8, v4, v5
	v_cvt_f32_f16_e32 v4, v90
	v_cvt_f32_f16_sdwa v5, v90 dst_sel:DWORD dst_unused:UNUSED_PAD src0_sel:WORD_1
	v_pk_add_f32 v[0:1], v[0:1], v[4:5]
	s_nop 0
	v_cvt_pk_f16_f32 v10, v0, v1
	v_cvt_f32_f16_e32 v0, v89
	v_cvt_f32_f16_sdwa v1, v89 dst_sel:DWORD dst_unused:UNUSED_PAD src0_sel:WORD_1
	v_pk_add_f32 v[0:1], v[6:7], v[0:1]
	s_nop 0
	v_cvt_pk_f16_f32 v9, v0, v1
	v_cvt_f32_f16_e32 v0, v91
	v_cvt_f32_f16_sdwa v1, v91 dst_sel:DWORD dst_unused:UNUSED_PAD src0_sel:WORD_1
	v_pk_add_f32 v[0:1], v[2:3], v[0:1]
	s_nop 0
	v_cvt_pk_f16_f32 v11, v0, v1
	global_store_dwordx4 v[12:13], v[8:11], off offset:256
	s_cbranch_vccz .LBB0_744
	s_waitcnt vmcnt(0)
	s_cmpk_gt_u32 s21, 0xff
	s_cbranch_scc1 .LBB0_755
	s_barrier

.LBB0_855:
	s_ashr_i32 s11, s10, 31
	s_lshl_b64 s[12:13], s[10:11], 20
	s_add_u32 s12, s25, s12
	s_addc_u32 s13, s26, s13
	s_and_b64 s[14:15], s[2:3], exec
	s_cselect_b32 s11, s13, s21
	s_cselect_b32 s53, s12, s20
	s_ashr_i32 s9, s8, 31
	s_lshl_b64 s[14:15], s[8:9], 20
	s_add_u32 s14, s27, s14
	s_addc_u32 s15, s28, s15
	s_and_b64 s[22:23], s[2:3], exec
	s_cselect_b32 s9, s15, s19
	s_cselect_b32 s54, s14, s18
	s_add_u32 s55, s18, 0x100
	s_addc_u32 s56, s19, 0
	s_add_u32 s18, s20, 0x80080
	v_mov_b32_e32 v0, 0
	s_addc_u32 s19, s21, 0
	s_mov_b32 s57, -2
	s_cmp_eq_u32 s52, 1
	s_cbranch_scc1 .Lpeel_zero_P7
	v_add_u32_e32 v154, s30, v139
	v_add_u32_e32 v158, s35, v139
	ds_read_b128 v[142:145], v154
	ds_read_b128 v[146:149], v154 offset:1024
	ds_read_b128 v[150:153], v154 offset:2048
	ds_read_b128 v[154:157], v154 offset:3072
	ds_read_b128 v[166:169], v158
	ds_read_b128 v[170:173], v158 offset:1024
	ds_read_b128 v[174:177], v158 offset:2048
	ds_read_b128 v[178:181], v158 offset:3072
	s_add_u32 s20, s18, 0xfff80080
	s_addc_u32 s21, s19, -1
	s_cmp_eq_u32 s57, 28
	s_cselect_b32 s23, s11, s21
	s_cselect_b32 s22, s53, s20
	s_cselect_b32 s21, s9, s56
	s_cselect_b32 s20, s54, s55
	v_lshl_add_u64 v[158:159], s[18:19], 0, v[136:137]
	s_add_i32 m0, s38, 0xc000
	ds_read_b128 v[182:185], v141
	ds_read_b128 v[186:189], v141 offset:1024
	ds_read_b128 v[190:193], v141 offset:2048
	ds_read_b128 v[194:197], v141 offset:3072
	ds_read_b128 v[198:201], v141 offset:4096
	ds_read_b128 v[202:205], v141 offset:5120
	ds_read_b128 v[206:209], v141 offset:6144
	ds_read_b128 v[210:213], v141 offset:7168
	global_load_lds_dwordx4 v[158:159], off
	v_lshl_add_u64 v[158:159], s[18:19], 0, v[134:135]
	s_add_i32 m0, s38, 0xe000
	s_nop 0
	global_load_lds_dwordx4 v[158:159], off
	s_waitcnt vmcnt(16)
	s_waitcnt lgkmcnt(0)
	s_barrier
	s_setprio 1
	s_waitcnt lgkmcnt(0)
	s_nop 0
	v_mfma_f32_16x16x32_bf16 v[124:127], v[142:145], v[182:185], 0
	v_mfma_f32_16x16x32_bf16 v[116:119], v[150:153], v[182:185], 0
	v_mfma_f32_16x16x32_bf16 v[108:111], v[142:145], v[190:193], 0
	v_mfma_f32_16x16x32_bf16 v[100:103], v[150:153], v[190:193], 0
	v_mfma_f32_16x16x32_bf16 v[92:95], v[142:145], v[198:201], 0
	v_mfma_f32_16x16x32_bf16 v[84:87], v[150:153], v[198:201], 0
	v_mfma_f32_16x16x32_bf16 v[76:79], v[142:145], v[206:209], 0
	v_mfma_f32_16x16x32_bf16 v[68:71], v[150:153], v[206:209], 0
	v_mfma_f32_16x16x32_bf16 v[124:127], v[146:149], v[186:189], v[124:127]
	v_mfma_f32_16x16x32_bf16 v[116:119], v[154:157], v[186:189], v[116:119]
	v_mfma_f32_16x16x32_bf16 v[108:111], v[146:149], v[194:197], v[108:111]
	v_mfma_f32_16x16x32_bf16 v[100:103], v[154:157], v[194:197], v[100:103]
	v_mfma_f32_16x16x32_bf16 v[92:95], v[146:149], v[202:205], v[92:95]
	v_mfma_f32_16x16x32_bf16 v[84:87], v[154:157], v[202:205], v[84:87]
	v_mfma_f32_16x16x32_bf16 v[76:79], v[146:149], v[210:213], v[76:79]
	v_mfma_f32_16x16x32_bf16 v[68:71], v[154:157], v[210:213], v[68:71]
	s_setprio 0
	s_setprio 1
	v_mfma_f32_16x16x32_bf16 v[120:123], v[166:169], v[182:185], 0
	v_mfma_f32_16x16x32_bf16 v[112:115], v[174:177], v[182:185], 0
	v_mfma_f32_16x16x32_bf16 v[104:107], v[166:169], v[190:193], 0
	v_mfma_f32_16x16x32_bf16 v[96:99], v[174:177], v[190:193], 0
	v_mfma_f32_16x16x32_bf16 v[88:91], v[166:169], v[198:201], 0
	v_mfma_f32_16x16x32_bf16 v[80:83], v[174:177], v[198:201], 0
	v_mfma_f32_16x16x32_bf16 v[72:75], v[166:169], v[206:209], 0
	v_mfma_f32_16x16x32_bf16 v[64:67], v[174:177], v[206:209], 0
	v_mfma_f32_16x16x32_bf16 v[120:123], v[170:173], v[186:189], v[120:123]
	v_mfma_f32_16x16x32_bf16 v[112:115], v[178:181], v[186:189], v[112:115]
	v_mfma_f32_16x16x32_bf16 v[104:107], v[170:173], v[194:197], v[104:107]
	v_mfma_f32_16x16x32_bf16 v[96:99], v[178:181], v[194:197], v[96:99]
	v_mfma_f32_16x16x32_bf16 v[88:91], v[170:173], v[202:205], v[88:91]
	v_mfma_f32_16x16x32_bf16 v[80:83], v[178:181], v[202:205], v[80:83]
	v_mfma_f32_16x16x32_bf16 v[72:75], v[170:173], v[210:213], v[72:75]
	v_mfma_f32_16x16x32_bf16 v[64:67], v[178:181], v[210:213], v[64:67]
	s_setprio 0
	s_barrier
	s_mov_b32 m0, s31
	v_lshl_add_u64 v[158:159], s[20:21], 0, v[160:161]
	s_add_u32 s58, s20, 0x80000
	ds_read_b128 v[182:185], v141 offset:16384
	ds_read_b128 v[186:189], v141 offset:17408
	ds_read_b128 v[190:193], v141 offset:18432
	ds_read_b128 v[194:197], v141 offset:19456
	ds_read_b128 v[198:201], v141 offset:20480
	ds_read_b128 v[202:205], v141 offset:21504
	ds_read_b128 v[206:209], v141 offset:22528
	ds_read_b128 v[210:213], v141 offset:23552
	global_load_lds_dwordx4 v[158:159], off
	v_lshl_add_u64 v[162:163], s[20:21], 0, v[128:129]
	s_mov_b32 m0, s34
	s_addc_u32 s59, s21, 0
	global_load_lds_dwordx4 v[162:163], off
	v_lshl_add_u64 v[214:215], s[58:59], 0, v[160:161]
	s_mov_b32 m0, s36
	v_lshl_add_u64 v[216:217], s[22:23], 0, v[130:131]
	global_load_lds_dwordx4 v[214:215], off
	v_lshl_add_u64 v[214:215], s[58:59], 0, v[128:129]
	s_mov_b32 m0, s37
	s_nop 0
	global_load_lds_dwordx4 v[214:215], off
	v_lshl_add_u64 v[214:215], s[22:23], 0, v[132:133]
	s_mov_b32 m0, s38
	s_nop 0
	global_load_lds_dwordx4 v[214:215], off
	s_mov_b32 m0, s39
	s_nop 0
	global_load_lds_dwordx4 v[216:217], off
	s_waitcnt vmcnt(16)
	s_waitcnt lgkmcnt(0)
	s_barrier
	s_setprio 1
	s_waitcnt lgkmcnt(0)
	s_nop 0
	v_mfma_f32_16x16x32_bf16 v[60:63], v[142:145], v[182:185], 0
	v_mfma_f32_16x16x32_bf16 v[52:55], v[150:153], v[182:185], 0
	v_mfma_f32_16x16x32_bf16 v[44:47], v[142:145], v[190:193], 0
	v_mfma_f32_16x16x32_bf16 v[36:39], v[150:153], v[190:193], 0
	v_mfma_f32_16x16x32_bf16 v[28:31], v[142:145], v[198:201], 0
	v_mfma_f32_16x16x32_bf16 v[20:23], v[150:153], v[198:201], 0
	v_mfma_f32_16x16x32_bf16 v[12:15], v[142:145], v[206:209], 0
	v_mfma_f32_16x16x32_bf16 v[4:7], v[150:153], v[206:209], 0
	v_mfma_f32_16x16x32_bf16 v[60:63], v[146:149], v[186:189], v[60:63]
	v_mfma_f32_16x16x32_bf16 v[52:55], v[154:157], v[186:189], v[52:55]
	v_mfma_f32_16x16x32_bf16 v[44:47], v[146:149], v[194:197], v[44:47]
	v_mfma_f32_16x16x32_bf16 v[36:39], v[154:157], v[194:197], v[36:39]
	v_mfma_f32_16x16x32_bf16 v[28:31], v[146:149], v[202:205], v[28:31]
	v_mfma_f32_16x16x32_bf16 v[20:23], v[154:157], v[202:205], v[20:23]
	v_mfma_f32_16x16x32_bf16 v[12:15], v[146:149], v[210:213], v[12:15]
	v_mfma_f32_16x16x32_bf16 v[4:7], v[154:157], v[210:213], v[4:7]
	s_setprio 0
	s_setprio 1
	v_mfma_f32_16x16x32_bf16 v[56:59], v[166:169], v[182:185], 0
	v_mfma_f32_16x16x32_bf16 v[48:51], v[174:177], v[182:185], 0
	v_mfma_f32_16x16x32_bf16 v[40:43], v[166:169], v[190:193], 0
	v_mfma_f32_16x16x32_bf16 v[32:35], v[174:177], v[190:193], 0
	v_mfma_f32_16x16x32_bf16 v[24:27], v[166:169], v[198:201], 0
	v_mfma_f32_16x16x32_bf16 v[16:19], v[174:177], v[198:201], 0
	v_mfma_f32_16x16x32_bf16 v[8:11], v[166:169], v[206:209], 0
	v_mfma_f32_16x16x32_bf16 v[0:3], v[174:177], v[206:209], 0
	v_mfma_f32_16x16x32_bf16 v[56:59], v[170:173], v[186:189], v[56:59]
	v_mfma_f32_16x16x32_bf16 v[48:51], v[178:181], v[186:189], v[48:51]
	v_mfma_f32_16x16x32_bf16 v[40:43], v[170:173], v[194:197], v[40:43]
	v_mfma_f32_16x16x32_bf16 v[32:35], v[178:181], v[194:197], v[32:35]
	v_mfma_f32_16x16x32_bf16 v[24:27], v[170:173], v[202:205], v[24:27]
	v_mfma_f32_16x16x32_bf16 v[16:19], v[178:181], v[202:205], v[16:19]
	v_mfma_f32_16x16x32_bf16 v[8:11], v[170:173], v[210:213], v[8:11]
	v_mfma_f32_16x16x32_bf16 v[0:3], v[178:181], v[210:213], v[0:3]
	s_setprio 0
	s_barrier
	v_add_u32_e32 v154, s43, v139
	v_add_u32_e32 v165, s48, v139
	ds_read_b128 v[142:145], v154
	ds_read_b128 v[146:149], v154 offset:1024
	ds_read_b128 v[150:153], v154 offset:2048
	ds_read_b128 v[154:157], v154 offset:3072
	ds_read_b128 v[166:169], v165
	ds_read_b128 v[170:173], v165 offset:1024
	ds_read_b128 v[174:177], v165 offset:2048
	ds_read_b128 v[178:181], v165 offset:3072
	s_add_u32 s22, s22, 0x80000
	s_addc_u32 s23, s23, 0
	s_mov_b32 m0, s40
	v_lshl_add_u64 v[218:219], s[22:23], 0, v[132:133]
	ds_read_b128 v[182:185], v141 offset:32768
	ds_read_b128 v[186:189], v141 offset:33792
	ds_read_b128 v[190:193], v141 offset:34816
	ds_read_b128 v[194:197], v141 offset:35840
	ds_read_b128 v[198:201], v141 offset:36864
	ds_read_b128 v[202:205], v141 offset:37888
	ds_read_b128 v[206:209], v141 offset:38912
	ds_read_b128 v[210:213], v141 offset:39936
	global_load_lds_dwordx4 v[218:219], off
	v_lshl_add_u64 v[218:219], s[22:23], 0, v[130:131]
	s_mov_b32 m0, s41
	s_nop 0
	global_load_lds_dwordx4 v[218:219], off
	s_waitcnt vmcnt(8)
	s_waitcnt lgkmcnt(0)
	s_barrier
	s_setprio 1
	s_waitcnt lgkmcnt(0)
	s_nop 0
	v_mfma_f32_16x16x32_bf16 v[124:127], v[142:145], v[182:185], v[124:127]
	v_mfma_f32_16x16x32_bf16 v[116:119], v[150:153], v[182:185], v[116:119]
	v_mfma_f32_16x16x32_bf16 v[108:111], v[142:145], v[190:193], v[108:111]
	v_mfma_f32_16x16x32_bf16 v[100:103], v[150:153], v[190:193], v[100:103]
	v_mfma_f32_16x16x32_bf16 v[92:95], v[142:145], v[198:201], v[92:95]
	v_mfma_f32_16x16x32_bf16 v[84:87], v[150:153], v[198:201], v[84:87]
	v_mfma_f32_16x16x32_bf16 v[76:79], v[142:145], v[206:209], v[76:79]
	v_mfma_f32_16x16x32_bf16 v[68:71], v[150:153], v[206:209], v[68:71]
	v_mfma_f32_16x16x32_bf16 v[124:127], v[146:149], v[186:189], v[124:127]
	v_mfma_f32_16x16x32_bf16 v[116:119], v[154:157], v[186:189], v[116:119]
	v_mfma_f32_16x16x32_bf16 v[108:111], v[146:149], v[194:197], v[108:111]
	v_mfma_f32_16x16x32_bf16 v[100:103], v[154:157], v[194:197], v[100:103]
	v_mfma_f32_16x16x32_bf16 v[92:95], v[146:149], v[202:205], v[92:95]
	v_mfma_f32_16x16x32_bf16 v[84:87], v[154:157], v[202:205], v[84:87]
	v_mfma_f32_16x16x32_bf16 v[76:79], v[146:149], v[210:213], v[76:79]
	v_mfma_f32_16x16x32_bf16 v[68:71], v[154:157], v[210:213], v[68:71]
	s_setprio 0
	s_setprio 1
	v_mfma_f32_16x16x32_bf16 v[120:123], v[166:169], v[182:185], v[120:123]
	v_mfma_f32_16x16x32_bf16 v[112:115], v[174:177], v[182:185], v[112:115]
	v_mfma_f32_16x16x32_bf16 v[104:107], v[166:169], v[190:193], v[104:107]
	v_mfma_f32_16x16x32_bf16 v[96:99], v[174:177], v[190:193], v[96:99]
	v_mfma_f32_16x16x32_bf16 v[88:91], v[166:169], v[198:201], v[88:91]
	v_mfma_f32_16x16x32_bf16 v[80:83], v[174:177], v[198:201], v[80:83]
	v_mfma_f32_16x16x32_bf16 v[72:75], v[166:169], v[206:209], v[72:75]
	v_mfma_f32_16x16x32_bf16 v[64:67], v[174:177], v[206:209], v[64:67]
	v_mfma_f32_16x16x32_bf16 v[120:123], v[170:173], v[186:189], v[120:123]
	v_mfma_f32_16x16x32_bf16 v[112:115], v[178:181], v[186:189], v[112:115]
	v_mfma_f32_16x16x32_bf16 v[104:107], v[170:173], v[194:197], v[104:107]
	v_mfma_f32_16x16x32_bf16 v[96:99], v[178:181], v[194:197], v[96:99]
	v_mfma_f32_16x16x32_bf16 v[88:91], v[170:173], v[202:205], v[88:91]
	v_mfma_f32_16x16x32_bf16 v[80:83], v[178:181], v[202:205], v[80:83]
	v_mfma_f32_16x16x32_bf16 v[72:75], v[170:173], v[210:213], v[72:75]
	v_mfma_f32_16x16x32_bf16 v[64:67], v[178:181], v[210:213], v[64:67]
	s_setprio 0
	s_barrier
	s_mov_b32 m0, s44
	v_lshl_add_u64 v[158:159], v[158:159], 0, s[86:87]
	s_add_u32 s20, s20, 0x80080
	ds_read_b128 v[182:185], v141 offset:49152
	ds_read_b128 v[186:189], v141 offset:50176
	ds_read_b128 v[190:193], v141 offset:51200
	ds_read_b128 v[194:197], v141 offset:52224
	ds_read_b128 v[198:201], v141 offset:53248
	ds_read_b128 v[202:205], v141 offset:54272
	ds_read_b128 v[206:209], v141 offset:55296
	ds_read_b128 v[210:213], v141 offset:56320
	global_load_lds_dwordx4 v[158:159], off
	v_lshl_add_u64 v[158:159], v[162:163], 0, s[86:87]
	s_mov_b32 m0, s45
	s_addc_u32 s21, s21, 0
	global_load_lds_dwordx4 v[158:159], off
	v_lshl_add_u64 v[158:159], s[20:21], 0, v[160:161]
	s_mov_b32 m0, s49
	s_nop 0
	global_load_lds_dwordx4 v[158:159], off
	v_lshl_add_u64 v[158:159], s[20:21], 0, v[128:129]
	s_mov_b32 m0, s50
	s_nop 0
	global_load_lds_dwordx4 v[158:159], off
	v_lshl_add_u64 v[158:159], v[214:215], 0, s[86:87]
	s_mov_b32 m0, s46
	s_nop 0
	global_load_lds_dwordx4 v[158:159], off
	v_lshl_add_u64 v[158:159], v[216:217], 0, s[86:87]
	s_mov_b32 m0, s47
	s_nop 0
	global_load_lds_dwordx4 v[158:159], off
	s_waitcnt vmcnt(8)
	s_waitcnt lgkmcnt(0)
	s_barrier
	s_setprio 1
	s_waitcnt lgkmcnt(0)
	v_mfma_f32_16x16x32_bf16 v[60:63], v[142:145], v[182:185], v[60:63]
	v_mfma_f32_16x16x32_bf16 v[52:55], v[150:153], v[182:185], v[52:55]
	v_mfma_f32_16x16x32_bf16 v[44:47], v[142:145], v[190:193], v[44:47]
	v_mfma_f32_16x16x32_bf16 v[36:39], v[150:153], v[190:193], v[36:39]
	v_mfma_f32_16x16x32_bf16 v[28:31], v[142:145], v[198:201], v[28:31]
	v_mfma_f32_16x16x32_bf16 v[20:23], v[150:153], v[198:201], v[20:23]
	v_mfma_f32_16x16x32_bf16 v[12:15], v[142:145], v[206:209], v[12:15]
	v_mfma_f32_16x16x32_bf16 v[4:7], v[150:153], v[206:209], v[4:7]
	v_mfma_f32_16x16x32_bf16 v[60:63], v[146:149], v[186:189], v[60:63]
	v_mfma_f32_16x16x32_bf16 v[52:55], v[154:157], v[186:189], v[52:55]
	v_mfma_f32_16x16x32_bf16 v[44:47], v[146:149], v[194:197], v[44:47]
	v_mfma_f32_16x16x32_bf16 v[36:39], v[154:157], v[194:197], v[36:39]
	v_mfma_f32_16x16x32_bf16 v[28:31], v[146:149], v[202:205], v[28:31]
	v_mfma_f32_16x16x32_bf16 v[20:23], v[154:157], v[202:205], v[20:23]
	v_mfma_f32_16x16x32_bf16 v[12:15], v[146:149], v[210:213], v[12:15]
	v_mfma_f32_16x16x32_bf16 v[4:7], v[154:157], v[210:213], v[4:7]
	s_setprio 0
	s_setprio 1
	v_mfma_f32_16x16x32_bf16 v[56:59], v[166:169], v[182:185], v[56:59]
	v_mfma_f32_16x16x32_bf16 v[48:51], v[174:177], v[182:185], v[48:51]
	v_mfma_f32_16x16x32_bf16 v[40:43], v[166:169], v[190:193], v[40:43]
	v_mfma_f32_16x16x32_bf16 v[32:35], v[174:177], v[190:193], v[32:35]
	v_mfma_f32_16x16x32_bf16 v[24:27], v[166:169], v[198:201], v[24:27]
	v_mfma_f32_16x16x32_bf16 v[16:19], v[174:177], v[198:201], v[16:19]
	v_mfma_f32_16x16x32_bf16 v[8:11], v[166:169], v[206:209], v[8:11]
	v_mfma_f32_16x16x32_bf16 v[0:3], v[174:177], v[206:209], v[0:3]
	v_mfma_f32_16x16x32_bf16 v[56:59], v[170:173], v[186:189], v[56:59]
	v_mfma_f32_16x16x32_bf16 v[48:51], v[178:181], v[186:189], v[48:51]
	v_mfma_f32_16x16x32_bf16 v[40:43], v[170:173], v[194:197], v[40:43]
	v_mfma_f32_16x16x32_bf16 v[32:35], v[178:181], v[194:197], v[32:35]
	v_mfma_f32_16x16x32_bf16 v[24:27], v[170:173], v[202:205], v[24:27]
	v_mfma_f32_16x16x32_bf16 v[16:19], v[178:181], v[202:205], v[16:19]
	v_mfma_f32_16x16x32_bf16 v[8:11], v[170:173], v[210:213], v[8:11]
	v_mfma_f32_16x16x32_bf16 v[0:3], v[178:181], v[210:213], v[0:3]
	s_setprio 0
	s_barrier
	s_add_i32 s57, s57, 2
	s_add_u32 s55, s55, 0x100
	s_addc_u32 s56, s56, 0
	s_add_u32 s18, s18, 0x100
	s_addc_u32 s19, s19, 0
	s_branch .LBB0_856

.LBB0_856:
	v_add_u32_e32 v154, s30, v139
	v_add_u32_e32 v158, s35, v139
	ds_read_b128 v[142:145], v154
	ds_read_b128 v[146:149], v154 offset:1024
	ds_read_b128 v[150:153], v154 offset:2048
	ds_read_b128 v[154:157], v154 offset:3072
	ds_read_b128 v[166:169], v158
	ds_read_b128 v[170:173], v158 offset:1024
	ds_read_b128 v[174:177], v158 offset:2048
	ds_read_b128 v[178:181], v158 offset:3072
	s_add_u32 s20, s18, 0xfff80080
	s_addc_u32 s21, s19, -1
	s_cmp_eq_u32 s57, 28
	s_cselect_b32 s23, s11, s21
	s_cselect_b32 s22, s53, s20
	s_cselect_b32 s21, s9, s56
	s_cselect_b32 s20, s54, s55
	v_lshl_add_u64 v[158:159], s[18:19], 0, v[136:137]
	s_add_i32 m0, s38, 0xc000
	ds_read_b128 v[182:185], v141
	ds_read_b128 v[186:189], v141 offset:1024
	ds_read_b128 v[190:193], v141 offset:2048
	ds_read_b128 v[194:197], v141 offset:3072
	ds_read_b128 v[198:201], v141 offset:4096
	ds_read_b128 v[202:205], v141 offset:5120
	ds_read_b128 v[206:209], v141 offset:6144
	ds_read_b128 v[210:213], v141 offset:7168
	global_load_lds_dwordx4 v[158:159], off
	v_lshl_add_u64 v[158:159], s[18:19], 0, v[134:135]
	s_add_i32 m0, s38, 0xe000
	s_nop 0
	global_load_lds_dwordx4 v[158:159], off
	s_waitcnt vmcnt(8)
	s_waitcnt lgkmcnt(0)
	s_barrier
	s_setprio 1
	s_waitcnt lgkmcnt(0)
	s_nop 0
	v_mfma_f32_16x16x32_bf16 v[124:127], v[142:145], v[182:185], v[124:127]
	v_mfma_f32_16x16x32_bf16 v[116:119], v[150:153], v[182:185], v[116:119]
	v_mfma_f32_16x16x32_bf16 v[108:111], v[142:145], v[190:193], v[108:111]
	v_mfma_f32_16x16x32_bf16 v[100:103], v[150:153], v[190:193], v[100:103]
	v_mfma_f32_16x16x32_bf16 v[92:95], v[142:145], v[198:201], v[92:95]
	v_mfma_f32_16x16x32_bf16 v[84:87], v[150:153], v[198:201], v[84:87]
	v_mfma_f32_16x16x32_bf16 v[76:79], v[142:145], v[206:209], v[76:79]
	v_mfma_f32_16x16x32_bf16 v[68:71], v[150:153], v[206:209], v[68:71]
	v_mfma_f32_16x16x32_bf16 v[124:127], v[146:149], v[186:189], v[124:127]
	v_mfma_f32_16x16x32_bf16 v[116:119], v[154:157], v[186:189], v[116:119]
	v_mfma_f32_16x16x32_bf16 v[108:111], v[146:149], v[194:197], v[108:111]
	v_mfma_f32_16x16x32_bf16 v[100:103], v[154:157], v[194:197], v[100:103]
	v_mfma_f32_16x16x32_bf16 v[92:95], v[146:149], v[202:205], v[92:95]
	v_mfma_f32_16x16x32_bf16 v[84:87], v[154:157], v[202:205], v[84:87]
	v_mfma_f32_16x16x32_bf16 v[76:79], v[146:149], v[210:213], v[76:79]
	v_mfma_f32_16x16x32_bf16 v[68:71], v[154:157], v[210:213], v[68:71]
	s_setprio 0
	s_setprio 1
	v_mfma_f32_16x16x32_bf16 v[120:123], v[166:169], v[182:185], v[120:123]
	v_mfma_f32_16x16x32_bf16 v[112:115], v[174:177], v[182:185], v[112:115]
	v_mfma_f32_16x16x32_bf16 v[104:107], v[166:169], v[190:193], v[104:107]
	v_mfma_f32_16x16x32_bf16 v[96:99], v[174:177], v[190:193], v[96:99]
	v_mfma_f32_16x16x32_bf16 v[88:91], v[166:169], v[198:201], v[88:91]
	v_mfma_f32_16x16x32_bf16 v[80:83], v[174:177], v[198:201], v[80:83]
	v_mfma_f32_16x16x32_bf16 v[72:75], v[166:169], v[206:209], v[72:75]
	v_mfma_f32_16x16x32_bf16 v[64:67], v[174:177], v[206:209], v[64:67]
	v_mfma_f32_16x16x32_bf16 v[120:123], v[170:173], v[186:189], v[120:123]
	v_mfma_f32_16x16x32_bf16 v[112:115], v[178:181], v[186:189], v[112:115]
	v_mfma_f32_16x16x32_bf16 v[104:107], v[170:173], v[194:197], v[104:107]
	v_mfma_f32_16x16x32_bf16 v[96:99], v[178:181], v[194:197], v[96:99]
	v_mfma_f32_16x16x32_bf16 v[88:91], v[170:173], v[202:205], v[88:91]
	v_mfma_f32_16x16x32_bf16 v[80:83], v[178:181], v[202:205], v[80:83]
	v_mfma_f32_16x16x32_bf16 v[72:75], v[170:173], v[210:213], v[72:75]
	v_mfma_f32_16x16x32_bf16 v[64:67], v[178:181], v[210:213], v[64:67]
	s_setprio 0
	s_barrier
	s_mov_b32 m0, s31
	v_lshl_add_u64 v[158:159], s[20:21], 0, v[160:161]
	s_add_u32 s58, s20, 0x80000
	ds_read_b128 v[182:185], v141 offset:16384
	ds_read_b128 v[186:189], v141 offset:17408
	ds_read_b128 v[190:193], v141 offset:18432
	ds_read_b128 v[194:197], v141 offset:19456
	ds_read_b128 v[198:201], v141 offset:20480
	ds_read_b128 v[202:205], v141 offset:21504
	ds_read_b128 v[206:209], v141 offset:22528
	ds_read_b128 v[210:213], v141 offset:23552
	global_load_lds_dwordx4 v[158:159], off
	v_lshl_add_u64 v[162:163], s[20:21], 0, v[128:129]
	s_mov_b32 m0, s34
	s_addc_u32 s59, s21, 0
	global_load_lds_dwordx4 v[162:163], off
	v_lshl_add_u64 v[214:215], s[58:59], 0, v[160:161]
	s_mov_b32 m0, s36
	v_lshl_add_u64 v[216:217], s[22:23], 0, v[130:131]
	global_load_lds_dwordx4 v[214:215], off
	v_lshl_add_u64 v[214:215], s[58:59], 0, v[128:129]
	s_mov_b32 m0, s37
	s_nop 0
	global_load_lds_dwordx4 v[214:215], off
	v_lshl_add_u64 v[214:215], s[22:23], 0, v[132:133]
	s_mov_b32 m0, s38
	s_nop 0
	global_load_lds_dwordx4 v[214:215], off
	s_mov_b32 m0, s39
	s_nop 0
	global_load_lds_dwordx4 v[216:217], off
	s_waitcnt vmcnt(8)
	s_waitcnt lgkmcnt(0)
	s_barrier
	s_setprio 1
	s_waitcnt lgkmcnt(0)
	s_nop 0
	v_mfma_f32_16x16x32_bf16 v[60:63], v[142:145], v[182:185], v[60:63]
	v_mfma_f32_16x16x32_bf16 v[52:55], v[150:153], v[182:185], v[52:55]
	v_mfma_f32_16x16x32_bf16 v[44:47], v[142:145], v[190:193], v[44:47]
	v_mfma_f32_16x16x32_bf16 v[36:39], v[150:153], v[190:193], v[36:39]
	v_mfma_f32_16x16x32_bf16 v[28:31], v[142:145], v[198:201], v[28:31]
	v_mfma_f32_16x16x32_bf16 v[20:23], v[150:153], v[198:201], v[20:23]
	v_mfma_f32_16x16x32_bf16 v[12:15], v[142:145], v[206:209], v[12:15]
	v_mfma_f32_16x16x32_bf16 v[4:7], v[150:153], v[206:209], v[4:7]
	v_mfma_f32_16x16x32_bf16 v[60:63], v[146:149], v[186:189], v[60:63]
	v_mfma_f32_16x16x32_bf16 v[52:55], v[154:157], v[186:189], v[52:55]
	v_mfma_f32_16x16x32_bf16 v[44:47], v[146:149], v[194:197], v[44:47]
	v_mfma_f32_16x16x32_bf16 v[36:39], v[154:157], v[194:197], v[36:39]
	v_mfma_f32_16x16x32_bf16 v[28:31], v[146:149], v[202:205], v[28:31]
	v_mfma_f32_16x16x32_bf16 v[20:23], v[154:157], v[202:205], v[20:23]
	v_mfma_f32_16x16x32_bf16 v[12:15], v[146:149], v[210:213], v[12:15]
	v_mfma_f32_16x16x32_bf16 v[4:7], v[154:157], v[210:213], v[4:7]
	s_setprio 0
	s_setprio 1
	v_mfma_f32_16x16x32_bf16 v[56:59], v[166:169], v[182:185], v[56:59]
	v_mfma_f32_16x16x32_bf16 v[48:51], v[174:177], v[182:185], v[48:51]
	v_mfma_f32_16x16x32_bf16 v[40:43], v[166:169], v[190:193], v[40:43]
	v_mfma_f32_16x16x32_bf16 v[32:35], v[174:177], v[190:193], v[32:35]
	v_mfma_f32_16x16x32_bf16 v[24:27], v[166:169], v[198:201], v[24:27]
	v_mfma_f32_16x16x32_bf16 v[16:19], v[174:177], v[198:201], v[16:19]
	v_mfma_f32_16x16x32_bf16 v[8:11], v[166:169], v[206:209], v[8:11]
	v_mfma_f32_16x16x32_bf16 v[0:3], v[174:177], v[206:209], v[0:3]
	v_mfma_f32_16x16x32_bf16 v[56:59], v[170:173], v[186:189], v[56:59]
	v_mfma_f32_16x16x32_bf16 v[48:51], v[178:181], v[186:189], v[48:51]
	v_mfma_f32_16x16x32_bf16 v[40:43], v[170:173], v[194:197], v[40:43]
	v_mfma_f32_16x16x32_bf16 v[32:35], v[178:181], v[194:197], v[32:35]
	v_mfma_f32_16x16x32_bf16 v[24:27], v[170:173], v[202:205], v[24:27]
	v_mfma_f32_16x16x32_bf16 v[16:19], v[178:181], v[202:205], v[16:19]
	v_mfma_f32_16x16x32_bf16 v[8:11], v[170:173], v[210:213], v[8:11]
	v_mfma_f32_16x16x32_bf16 v[0:3], v[178:181], v[210:213], v[0:3]
	s_setprio 0
	s_barrier
	v_add_u32_e32 v154, s43, v139
	v_add_u32_e32 v165, s48, v139
	ds_read_b128 v[142:145], v154
	ds_read_b128 v[146:149], v154 offset:1024
	ds_read_b128 v[150:153], v154 offset:2048
	ds_read_b128 v[154:157], v154 offset:3072
	ds_read_b128 v[166:169], v165
	ds_read_b128 v[170:173], v165 offset:1024
	ds_read_b128 v[174:177], v165 offset:2048
	ds_read_b128 v[178:181], v165 offset:3072
	s_add_u32 s22, s22, 0x80000
	s_addc_u32 s23, s23, 0
	s_mov_b32 m0, s40
	v_lshl_add_u64 v[218:219], s[22:23], 0, v[132:133]
	ds_read_b128 v[182:185], v141 offset:32768
	ds_read_b128 v[186:189], v141 offset:33792
	ds_read_b128 v[190:193], v141 offset:34816
	ds_read_b128 v[194:197], v141 offset:35840
	ds_read_b128 v[198:201], v141 offset:36864
	ds_read_b128 v[202:205], v141 offset:37888
	ds_read_b128 v[206:209], v141 offset:38912
	ds_read_b128 v[210:213], v141 offset:39936
	global_load_lds_dwordx4 v[218:219], off
	v_lshl_add_u64 v[218:219], s[22:23], 0, v[130:131]
	s_mov_b32 m0, s41
	s_nop 0
	global_load_lds_dwordx4 v[218:219], off
	s_waitcnt vmcnt(8)
	s_waitcnt lgkmcnt(0)
	s_barrier
	s_setprio 1
	s_waitcnt lgkmcnt(0)
	s_nop 0
	v_mfma_f32_16x16x32_bf16 v[124:127], v[142:145], v[182:185], v[124:127]
	v_mfma_f32_16x16x32_bf16 v[116:119], v[150:153], v[182:185], v[116:119]
	v_mfma_f32_16x16x32_bf16 v[108:111], v[142:145], v[190:193], v[108:111]
	v_mfma_f32_16x16x32_bf16 v[100:103], v[150:153], v[190:193], v[100:103]
	v_mfma_f32_16x16x32_bf16 v[92:95], v[142:145], v[198:201], v[92:95]
	v_mfma_f32_16x16x32_bf16 v[84:87], v[150:153], v[198:201], v[84:87]
	v_mfma_f32_16x16x32_bf16 v[76:79], v[142:145], v[206:209], v[76:79]
	v_mfma_f32_16x16x32_bf16 v[68:71], v[150:153], v[206:209], v[68:71]
	v_mfma_f32_16x16x32_bf16 v[124:127], v[146:149], v[186:189], v[124:127]
	v_mfma_f32_16x16x32_bf16 v[116:119], v[154:157], v[186:189], v[116:119]
	v_mfma_f32_16x16x32_bf16 v[108:111], v[146:149], v[194:197], v[108:111]
	v_mfma_f32_16x16x32_bf16 v[100:103], v[154:157], v[194:197], v[100:103]
	v_mfma_f32_16x16x32_bf16 v[92:95], v[146:149], v[202:205], v[92:95]
	v_mfma_f32_16x16x32_bf16 v[84:87], v[154:157], v[202:205], v[84:87]
	v_mfma_f32_16x16x32_bf16 v[76:79], v[146:149], v[210:213], v[76:79]
	v_mfma_f32_16x16x32_bf16 v[68:71], v[154:157], v[210:213], v[68:71]
	s_setprio 0
	s_setprio 1
	v_mfma_f32_16x16x32_bf16 v[120:123], v[166:169], v[182:185], v[120:123]
	v_mfma_f32_16x16x32_bf16 v[112:115], v[174:177], v[182:185], v[112:115]
	v_mfma_f32_16x16x32_bf16 v[104:107], v[166:169], v[190:193], v[104:107]
	v_mfma_f32_16x16x32_bf16 v[96:99], v[174:177], v[190:193], v[96:99]
	v_mfma_f32_16x16x32_bf16 v[88:91], v[166:169], v[198:201], v[88:91]
	v_mfma_f32_16x16x32_bf16 v[80:83], v[174:177], v[198:201], v[80:83]
	v_mfma_f32_16x16x32_bf16 v[72:75], v[166:169], v[206:209], v[72:75]
	v_mfma_f32_16x16x32_bf16 v[64:67], v[174:177], v[206:209], v[64:67]
	v_mfma_f32_16x16x32_bf16 v[120:123], v[170:173], v[186:189], v[120:123]
	v_mfma_f32_16x16x32_bf16 v[112:115], v[178:181], v[186:189], v[112:115]
	v_mfma_f32_16x16x32_bf16 v[104:107], v[170:173], v[194:197], v[104:107]
	v_mfma_f32_16x16x32_bf16 v[96:99], v[178:181], v[194:197], v[96:99]
	v_mfma_f32_16x16x32_bf16 v[88:91], v[170:173], v[202:205], v[88:91]
	v_mfma_f32_16x16x32_bf16 v[80:83], v[178:181], v[202:205], v[80:83]
	v_mfma_f32_16x16x32_bf16 v[72:75], v[170:173], v[210:213], v[72:75]
	v_mfma_f32_16x16x32_bf16 v[64:67], v[178:181], v[210:213], v[64:67]
	s_setprio 0
	s_barrier
	s_mov_b32 m0, s44
	v_lshl_add_u64 v[158:159], v[158:159], 0, s[86:87]
	s_add_u32 s20, s20, 0x80080
	ds_read_b128 v[182:185], v141 offset:49152
	ds_read_b128 v[186:189], v141 offset:50176
	ds_read_b128 v[190:193], v141 offset:51200
	ds_read_b128 v[194:197], v141 offset:52224
	ds_read_b128 v[198:201], v141 offset:53248
	ds_read_b128 v[202:205], v141 offset:54272
	ds_read_b128 v[206:209], v141 offset:55296
	ds_read_b128 v[210:213], v141 offset:56320
	global_load_lds_dwordx4 v[158:159], off
	v_lshl_add_u64 v[158:159], v[162:163], 0, s[86:87]
	s_mov_b32 m0, s45
	s_addc_u32 s21, s21, 0
	global_load_lds_dwordx4 v[158:159], off
	v_lshl_add_u64 v[158:159], s[20:21], 0, v[160:161]
	s_mov_b32 m0, s49
	s_nop 0
	global_load_lds_dwordx4 v[158:159], off
	v_lshl_add_u64 v[158:159], s[20:21], 0, v[128:129]
	s_mov_b32 m0, s50
	s_nop 0
	global_load_lds_dwordx4 v[158:159], off
	v_lshl_add_u64 v[158:159], v[214:215], 0, s[86:87]
	s_mov_b32 m0, s46
	s_nop 0
	global_load_lds_dwordx4 v[158:159], off
	v_lshl_add_u64 v[158:159], v[216:217], 0, s[86:87]
	s_mov_b32 m0, s47
	s_nop 0
	global_load_lds_dwordx4 v[158:159], off
	s_waitcnt vmcnt(8)
	s_waitcnt lgkmcnt(0)
	s_barrier
	s_setprio 1
	s_waitcnt lgkmcnt(0)
	v_mfma_f32_16x16x32_bf16 v[60:63], v[142:145], v[182:185], v[60:63]
	v_mfma_f32_16x16x32_bf16 v[52:55], v[150:153], v[182:185], v[52:55]
	v_mfma_f32_16x16x32_bf16 v[44:47], v[142:145], v[190:193], v[44:47]
	v_mfma_f32_16x16x32_bf16 v[36:39], v[150:153], v[190:193], v[36:39]
	v_mfma_f32_16x16x32_bf16 v[28:31], v[142:145], v[198:201], v[28:31]
	v_mfma_f32_16x16x32_bf16 v[20:23], v[150:153], v[198:201], v[20:23]
	v_mfma_f32_16x16x32_bf16 v[12:15], v[142:145], v[206:209], v[12:15]
	v_mfma_f32_16x16x32_bf16 v[4:7], v[150:153], v[206:209], v[4:7]
	v_mfma_f32_16x16x32_bf16 v[60:63], v[146:149], v[186:189], v[60:63]
	v_mfma_f32_16x16x32_bf16 v[52:55], v[154:157], v[186:189], v[52:55]
	v_mfma_f32_16x16x32_bf16 v[44:47], v[146:149], v[194:197], v[44:47]
	v_mfma_f32_16x16x32_bf16 v[36:39], v[154:157], v[194:197], v[36:39]
	v_mfma_f32_16x16x32_bf16 v[28:31], v[146:149], v[202:205], v[28:31]
	v_mfma_f32_16x16x32_bf16 v[20:23], v[154:157], v[202:205], v[20:23]
	v_mfma_f32_16x16x32_bf16 v[12:15], v[146:149], v[210:213], v[12:15]
	v_mfma_f32_16x16x32_bf16 v[4:7], v[154:157], v[210:213], v[4:7]
	s_setprio 0
	s_setprio 1
	v_mfma_f32_16x16x32_bf16 v[56:59], v[166:169], v[182:185], v[56:59]
	v_mfma_f32_16x16x32_bf16 v[48:51], v[174:177], v[182:185], v[48:51]
	v_mfma_f32_16x16x32_bf16 v[40:43], v[166:169], v[190:193], v[40:43]
	v_mfma_f32_16x16x32_bf16 v[32:35], v[174:177], v[190:193], v[32:35]
	v_mfma_f32_16x16x32_bf16 v[24:27], v[166:169], v[198:201], v[24:27]
	v_mfma_f32_16x16x32_bf16 v[16:19], v[174:177], v[198:201], v[16:19]
	v_mfma_f32_16x16x32_bf16 v[8:11], v[166:169], v[206:209], v[8:11]
	v_mfma_f32_16x16x32_bf16 v[0:3], v[174:177], v[206:209], v[0:3]
	v_mfma_f32_16x16x32_bf16 v[56:59], v[170:173], v[186:189], v[56:59]
	v_mfma_f32_16x16x32_bf16 v[48:51], v[178:181], v[186:189], v[48:51]
	v_mfma_f32_16x16x32_bf16 v[40:43], v[170:173], v[194:197], v[40:43]
	v_mfma_f32_16x16x32_bf16 v[32:35], v[178:181], v[194:197], v[32:35]
	v_mfma_f32_16x16x32_bf16 v[24:27], v[170:173], v[202:205], v[24:27]
	v_mfma_f32_16x16x32_bf16 v[16:19], v[178:181], v[202:205], v[16:19]
	v_mfma_f32_16x16x32_bf16 v[8:11], v[170:173], v[210:213], v[8:11]
	v_mfma_f32_16x16x32_bf16 v[0:3], v[178:181], v[210:213], v[0:3]
	s_setprio 0
	s_barrier
	s_add_i32 s57, s57, 2
	s_add_u32 s55, s55, 0x100
	s_addc_u32 s56, s56, 0
	s_add_u32 s18, s18, 0x100
	s_addc_u32 s19, s19, 0
	s_cmp_gt_u32 s57, 29
	s_cbranch_scc0 .LBB0_856
	s_and_b64 vcc, exec, s[6:7]
	s_cbranch_vccz .LBB0_859
	s_barrier

.LBB0_926:
	s_add_u32 s50, s10, 0x100
	v_mov_b32_e32 v0, 0
	s_addc_u32 s51, s11, 0
	s_mov_b32 s52, -2
	s_cmp_eq_u32 s45, 1
	s_cbranch_scc1 .Lpeel_zero_P8
	v_add_u32_e32 v120, s23, v230
	v_add_u32_e32 v148, s26, v230
	ds_read_b128 v[88:91], v120
	ds_read_b128 v[100:103], v120 offset:1024
	ds_read_b128 v[112:115], v120 offset:2048
	ds_read_b128 v[120:123], v120 offset:3072
	ds_read_b128 v[124:127], v148
	ds_read_b128 v[140:143], v148 offset:1024
	ds_read_b128 v[144:147], v148 offset:2048
	ds_read_b128 v[148:151], v148 offset:3072
	s_add_u32 s10, s8, 0x100
	s_addc_u32 s11, s9, 0
	s_cmpk_eq_i32 s52, 0x54
	s_cselect_b32 s15, s5, s11
	s_cselect_b32 s14, s4, s10
	s_cselect_b32 s13, s7, s51
	s_cselect_b32 s12, s6, s50
	v_lshl_add_u64 v[206:207], s[8:9], 0, v[204:205]
	s_add_i32 m0, s29, 0xc000
	ds_read_b128 v[152:155], v232
	ds_read_b128 v[170:173], v232 offset:1024
	ds_read_b128 v[174:177], v232 offset:2048
	ds_read_b128 v[178:181], v232 offset:3072
	ds_read_b128 v[182:185], v232 offset:4096
	ds_read_b128 v[186:189], v232 offset:5120
	ds_read_b128 v[190:193], v232 offset:6144
	ds_read_b128 v[194:197], v232 offset:7168
	global_load_lds_dwordx4 v[206:207], off
	v_lshl_add_u64 v[206:207], s[8:9], 0, v[202:203]
	s_add_i32 m0, s29, 0xe000
	s_nop 0
	global_load_lds_dwordx4 v[206:207], off
	s_waitcnt vmcnt(40)
	s_waitcnt lgkmcnt(0)
	s_barrier
	s_setprio 1
	s_waitcnt lgkmcnt(0)
	v_mfma_f32_16x16x32_bf16 v[166:169], v[88:91], v[152:155], 0
	v_mfma_f32_16x16x32_bf16 v[156:159], v[112:115], v[152:155], 0
	v_mfma_f32_16x16x32_bf16 v[128:131], v[88:91], v[174:177], 0
	v_mfma_f32_16x16x32_bf16 v[116:119], v[112:115], v[174:177], 0
	v_mfma_f32_16x16x32_bf16 v[96:99], v[88:91], v[182:185], 0
	v_mfma_f32_16x16x32_bf16 v[92:95], v[112:115], v[182:185], 0
	v_mfma_f32_16x16x32_bf16 v[76:79], v[88:91], v[190:193], 0
	v_mfma_f32_16x16x32_bf16 v[72:75], v[112:115], v[190:193], 0
	v_mfma_f32_16x16x32_bf16 v[166:169], v[100:103], v[170:173], v[166:169]
	v_mfma_f32_16x16x32_bf16 v[156:159], v[120:123], v[170:173], v[156:159]
	v_mfma_f32_16x16x32_bf16 v[128:131], v[100:103], v[178:181], v[128:131]
	v_mfma_f32_16x16x32_bf16 v[116:119], v[120:123], v[178:181], v[116:119]
	v_mfma_f32_16x16x32_bf16 v[96:99], v[100:103], v[186:189], v[96:99]
	v_mfma_f32_16x16x32_bf16 v[92:95], v[120:123], v[186:189], v[92:95]
	v_mfma_f32_16x16x32_bf16 v[76:79], v[100:103], v[194:197], v[76:79]
	v_mfma_f32_16x16x32_bf16 v[72:75], v[120:123], v[194:197], v[72:75]
	s_setprio 0
	s_setprio 1
	v_mfma_f32_16x16x32_bf16 v[136:139], v[124:127], v[152:155], 0
	v_mfma_f32_16x16x32_bf16 v[132:135], v[144:147], v[152:155], 0
	v_mfma_f32_16x16x32_bf16 v[108:111], v[124:127], v[174:177], 0
	v_mfma_f32_16x16x32_bf16 v[104:107], v[144:147], v[174:177], 0
	v_mfma_f32_16x16x32_bf16 v[84:87], v[124:127], v[182:185], 0
	v_mfma_f32_16x16x32_bf16 v[80:83], v[144:147], v[182:185], 0
	v_mfma_f32_16x16x32_bf16 v[68:71], v[124:127], v[190:193], 0
	v_mfma_f32_16x16x32_bf16 v[64:67], v[144:147], v[190:193], 0
	v_mfma_f32_16x16x32_bf16 v[136:139], v[140:143], v[170:173], v[136:139]
	v_mfma_f32_16x16x32_bf16 v[132:135], v[148:151], v[170:173], v[132:135]
	v_mfma_f32_16x16x32_bf16 v[108:111], v[140:143], v[178:181], v[108:111]
	v_mfma_f32_16x16x32_bf16 v[104:107], v[148:151], v[178:181], v[104:107]
	v_mfma_f32_16x16x32_bf16 v[84:87], v[140:143], v[186:189], v[84:87]
	v_mfma_f32_16x16x32_bf16 v[80:83], v[148:151], v[186:189], v[80:83]
	v_mfma_f32_16x16x32_bf16 v[68:71], v[140:143], v[194:197], v[68:71]
	v_mfma_f32_16x16x32_bf16 v[64:67], v[148:151], v[194:197], v[64:67]
	s_setprio 0
	s_barrier
	s_mov_b32 m0, s24
	v_lshl_add_u64 v[206:207], s[12:13], 0, v[160:161]
	s_add_u32 s8, s12, 0x160000
	ds_read_b128 v[152:155], v232 offset:16384
	ds_read_b128 v[170:173], v232 offset:17408
	ds_read_b128 v[174:177], v232 offset:18432
	ds_read_b128 v[178:181], v232 offset:19456
	ds_read_b128 v[182:185], v232 offset:20480
	ds_read_b128 v[186:189], v232 offset:21504
	ds_read_b128 v[190:193], v232 offset:22528
	ds_read_b128 v[194:197], v232 offset:23552
	global_load_lds_dwordx4 v[206:207], off
	v_lshl_add_u64 v[208:209], s[12:13], 0, v[200:201]
	s_mov_b32 m0, s25
	s_addc_u32 s9, s13, 0
	global_load_lds_dwordx4 v[208:209], off
	v_lshl_add_u64 v[210:211], s[8:9], 0, v[160:161]
	s_mov_b32 m0, s27
	v_lshl_add_u64 v[212:213], s[14:15], 0, v[198:199]
	global_load_lds_dwordx4 v[210:211], off
	v_lshl_add_u64 v[210:211], s[8:9], 0, v[200:201]
	s_mov_b32 m0, s28
	s_nop 0
	global_load_lds_dwordx4 v[210:211], off
	v_lshl_add_u64 v[210:211], s[14:15], 0, v[162:163]
	s_mov_b32 m0, s29
	s_nop 0
	global_load_lds_dwordx4 v[210:211], off
	s_mov_b32 m0, s30
	s_nop 0
	global_load_lds_dwordx4 v[212:213], off
	s_waitcnt vmcnt(40)
	s_waitcnt lgkmcnt(0)
	s_barrier
	s_setprio 1
	s_waitcnt lgkmcnt(0)
	s_nop 0
	v_mfma_f32_16x16x32_bf16 v[60:63], v[88:91], v[152:155], 0
	v_mfma_f32_16x16x32_bf16 v[56:59], v[112:115], v[152:155], 0
	v_mfma_f32_16x16x32_bf16 v[44:47], v[88:91], v[174:177], 0
	v_mfma_f32_16x16x32_bf16 v[40:43], v[112:115], v[174:177], 0
	v_mfma_f32_16x16x32_bf16 v[28:31], v[88:91], v[182:185], 0
	v_mfma_f32_16x16x32_bf16 v[24:27], v[112:115], v[182:185], 0
	v_mfma_f32_16x16x32_bf16 v[12:15], v[88:91], v[190:193], 0
	v_mfma_f32_16x16x32_bf16 v[8:11], v[112:115], v[190:193], 0
	v_mfma_f32_16x16x32_bf16 v[60:63], v[100:103], v[170:173], v[60:63]
	v_mfma_f32_16x16x32_bf16 v[56:59], v[120:123], v[170:173], v[56:59]
	v_mfma_f32_16x16x32_bf16 v[44:47], v[100:103], v[178:181], v[44:47]
	v_mfma_f32_16x16x32_bf16 v[40:43], v[120:123], v[178:181], v[40:43]
	v_mfma_f32_16x16x32_bf16 v[28:31], v[100:103], v[186:189], v[28:31]
	v_mfma_f32_16x16x32_bf16 v[24:27], v[120:123], v[186:189], v[24:27]
	v_mfma_f32_16x16x32_bf16 v[12:15], v[100:103], v[194:197], v[12:15]
	v_mfma_f32_16x16x32_bf16 v[8:11], v[120:123], v[194:197], v[8:11]
	s_setprio 0
	s_setprio 1
	v_mfma_f32_16x16x32_bf16 v[52:55], v[124:127], v[152:155], 0
	v_mfma_f32_16x16x32_bf16 v[48:51], v[144:147], v[152:155], 0
	v_mfma_f32_16x16x32_bf16 v[36:39], v[124:127], v[174:177], 0
	v_mfma_f32_16x16x32_bf16 v[32:35], v[144:147], v[174:177], 0
	v_mfma_f32_16x16x32_bf16 v[20:23], v[124:127], v[182:185], 0
	v_mfma_f32_16x16x32_bf16 v[16:19], v[144:147], v[182:185], 0
	v_mfma_f32_16x16x32_bf16 v[4:7], v[124:127], v[190:193], 0
	v_mfma_f32_16x16x32_bf16 v[0:3], v[144:147], v[190:193], 0
	v_mfma_f32_16x16x32_bf16 v[52:55], v[140:143], v[170:173], v[52:55]
	v_mfma_f32_16x16x32_bf16 v[48:51], v[148:151], v[170:173], v[48:51]
	v_mfma_f32_16x16x32_bf16 v[36:39], v[140:143], v[178:181], v[36:39]
	v_mfma_f32_16x16x32_bf16 v[32:35], v[148:151], v[178:181], v[32:35]
	v_mfma_f32_16x16x32_bf16 v[20:23], v[140:143], v[186:189], v[20:23]
	v_mfma_f32_16x16x32_bf16 v[16:19], v[148:151], v[186:189], v[16:19]
	v_mfma_f32_16x16x32_bf16 v[4:7], v[140:143], v[194:197], v[4:7]
	v_mfma_f32_16x16x32_bf16 v[0:3], v[148:151], v[194:197], v[0:3]
	s_setprio 0
	s_barrier
	v_add_u32_e32 v120, s36, v230
	v_add_u32_e32 v148, s41, v230
	ds_read_b128 v[88:91], v120
	ds_read_b128 v[100:103], v120 offset:1024
	ds_read_b128 v[112:115], v120 offset:2048
	ds_read_b128 v[120:123], v120 offset:3072
	ds_read_b128 v[124:127], v148
	ds_read_b128 v[140:143], v148 offset:1024
	ds_read_b128 v[144:147], v148 offset:2048
	ds_read_b128 v[148:151], v148 offset:3072
	s_add_u32 s8, s14, 0x160000
	s_addc_u32 s9, s15, 0
	s_mov_b32 m0, s31
	v_lshl_add_u64 v[214:215], s[8:9], 0, v[162:163]
	ds_read_b128 v[152:155], v232 offset:32768
	ds_read_b128 v[170:173], v232 offset:33792
	ds_read_b128 v[174:177], v232 offset:34816
	ds_read_b128 v[178:181], v232 offset:35840
	ds_read_b128 v[182:185], v232 offset:36864
	ds_read_b128 v[186:189], v232 offset:37888
	ds_read_b128 v[190:193], v232 offset:38912
	ds_read_b128 v[194:197], v232 offset:39936
	global_load_lds_dwordx4 v[214:215], off
	v_lshl_add_u64 v[214:215], s[8:9], 0, v[198:199]
	s_mov_b32 m0, s34
	s_nop 0
	global_load_lds_dwordx4 v[214:215], off
	s_waitcnt vmcnt(8)
	s_waitcnt lgkmcnt(0)
	s_barrier
	s_setprio 1
	s_waitcnt lgkmcnt(0)
	s_nop 0
	v_mfma_f32_16x16x32_bf16 v[166:169], v[88:91], v[152:155], v[166:169]
	v_mfma_f32_16x16x32_bf16 v[156:159], v[112:115], v[152:155], v[156:159]
	v_mfma_f32_16x16x32_bf16 v[128:131], v[88:91], v[174:177], v[128:131]
	v_mfma_f32_16x16x32_bf16 v[116:119], v[112:115], v[174:177], v[116:119]
	v_mfma_f32_16x16x32_bf16 v[96:99], v[88:91], v[182:185], v[96:99]
	v_mfma_f32_16x16x32_bf16 v[92:95], v[112:115], v[182:185], v[92:95]
	v_mfma_f32_16x16x32_bf16 v[76:79], v[88:91], v[190:193], v[76:79]
	v_mfma_f32_16x16x32_bf16 v[72:75], v[112:115], v[190:193], v[72:75]
	v_mfma_f32_16x16x32_bf16 v[166:169], v[100:103], v[170:173], v[166:169]
	v_mfma_f32_16x16x32_bf16 v[156:159], v[120:123], v[170:173], v[156:159]
	v_mfma_f32_16x16x32_bf16 v[128:131], v[100:103], v[178:181], v[128:131]
	v_mfma_f32_16x16x32_bf16 v[116:119], v[120:123], v[178:181], v[116:119]
	v_mfma_f32_16x16x32_bf16 v[96:99], v[100:103], v[186:189], v[96:99]
	v_mfma_f32_16x16x32_bf16 v[92:95], v[120:123], v[186:189], v[92:95]
	v_mfma_f32_16x16x32_bf16 v[76:79], v[100:103], v[194:197], v[76:79]
	v_mfma_f32_16x16x32_bf16 v[72:75], v[120:123], v[194:197], v[72:75]
	s_setprio 0
	s_setprio 1
	v_mfma_f32_16x16x32_bf16 v[136:139], v[124:127], v[152:155], v[136:139]
	v_mfma_f32_16x16x32_bf16 v[132:135], v[144:147], v[152:155], v[132:135]
	v_mfma_f32_16x16x32_bf16 v[108:111], v[124:127], v[174:177], v[108:111]
	v_mfma_f32_16x16x32_bf16 v[104:107], v[144:147], v[174:177], v[104:107]
	v_mfma_f32_16x16x32_bf16 v[84:87], v[124:127], v[182:185], v[84:87]
	v_mfma_f32_16x16x32_bf16 v[80:83], v[144:147], v[182:185], v[80:83]
	v_mfma_f32_16x16x32_bf16 v[68:71], v[124:127], v[190:193], v[68:71]
	v_mfma_f32_16x16x32_bf16 v[64:67], v[144:147], v[190:193], v[64:67]
	v_mfma_f32_16x16x32_bf16 v[136:139], v[140:143], v[170:173], v[136:139]
	v_mfma_f32_16x16x32_bf16 v[132:135], v[148:151], v[170:173], v[132:135]
	v_mfma_f32_16x16x32_bf16 v[108:111], v[140:143], v[178:181], v[108:111]
	v_mfma_f32_16x16x32_bf16 v[104:107], v[148:151], v[178:181], v[104:107]
	v_mfma_f32_16x16x32_bf16 v[84:87], v[140:143], v[186:189], v[84:87]
	v_mfma_f32_16x16x32_bf16 v[80:83], v[148:151], v[186:189], v[80:83]
	v_mfma_f32_16x16x32_bf16 v[68:71], v[140:143], v[194:197], v[68:71]
	v_mfma_f32_16x16x32_bf16 v[64:67], v[148:151], v[194:197], v[64:67]
	s_setprio 0
	s_barrier
	s_mov_b32 m0, s37
	v_lshl_add_u64 v[206:207], v[206:207], 0, s[86:87]
	s_add_u32 s8, s12, 0x160080
	ds_read_b128 v[152:155], v232 offset:49152
	ds_read_b128 v[170:173], v232 offset:50176
	ds_read_b128 v[174:177], v232 offset:51200
	ds_read_b128 v[178:181], v232 offset:52224
	ds_read_b128 v[182:185], v232 offset:53248
	ds_read_b128 v[186:189], v232 offset:54272
	ds_read_b128 v[190:193], v232 offset:55296
	ds_read_b128 v[194:197], v232 offset:56320
	global_load_lds_dwordx4 v[206:207], off
	v_lshl_add_u64 v[206:207], v[208:209], 0, s[86:87]
	s_mov_b32 m0, s38
	s_addc_u32 s9, s13, 0
	global_load_lds_dwordx4 v[206:207], off
	v_lshl_add_u64 v[206:207], s[8:9], 0, v[160:161]
	s_mov_b32 m0, s42
	s_nop 0
	global_load_lds_dwordx4 v[206:207], off
	v_lshl_add_u64 v[206:207], s[8:9], 0, v[200:201]
	s_mov_b32 m0, s43
	s_nop 0
	global_load_lds_dwordx4 v[206:207], off
	v_lshl_add_u64 v[206:207], v[210:211], 0, s[86:87]
	s_mov_b32 m0, s39
	s_nop 0
	global_load_lds_dwordx4 v[206:207], off
	v_lshl_add_u64 v[206:207], v[212:213], 0, s[86:87]
	s_mov_b32 m0, s40
	s_nop 0
	global_load_lds_dwordx4 v[206:207], off
	s_waitcnt vmcnt(8)
	s_waitcnt lgkmcnt(0)
	s_barrier
	s_setprio 1
	s_waitcnt lgkmcnt(0)
	v_mfma_f32_16x16x32_bf16 v[60:63], v[88:91], v[152:155], v[60:63]
	v_mfma_f32_16x16x32_bf16 v[56:59], v[112:115], v[152:155], v[56:59]
	v_mfma_f32_16x16x32_bf16 v[44:47], v[88:91], v[174:177], v[44:47]
	v_mfma_f32_16x16x32_bf16 v[40:43], v[112:115], v[174:177], v[40:43]
	v_mfma_f32_16x16x32_bf16 v[28:31], v[88:91], v[182:185], v[28:31]
	v_mfma_f32_16x16x32_bf16 v[24:27], v[112:115], v[182:185], v[24:27]
	v_mfma_f32_16x16x32_bf16 v[12:15], v[88:91], v[190:193], v[12:15]
	v_mfma_f32_16x16x32_bf16 v[8:11], v[112:115], v[190:193], v[8:11]
	v_mfma_f32_16x16x32_bf16 v[60:63], v[100:103], v[170:173], v[60:63]
	v_mfma_f32_16x16x32_bf16 v[56:59], v[120:123], v[170:173], v[56:59]
	v_mfma_f32_16x16x32_bf16 v[44:47], v[100:103], v[178:181], v[44:47]
	v_mfma_f32_16x16x32_bf16 v[40:43], v[120:123], v[178:181], v[40:43]
	v_mfma_f32_16x16x32_bf16 v[28:31], v[100:103], v[186:189], v[28:31]
	v_mfma_f32_16x16x32_bf16 v[24:27], v[120:123], v[186:189], v[24:27]
	v_mfma_f32_16x16x32_bf16 v[12:15], v[100:103], v[194:197], v[12:15]
	v_mfma_f32_16x16x32_bf16 v[8:11], v[120:123], v[194:197], v[8:11]
	s_setprio 0
	s_setprio 1
	v_mfma_f32_16x16x32_bf16 v[52:55], v[124:127], v[152:155], v[52:55]
	v_mfma_f32_16x16x32_bf16 v[48:51], v[144:147], v[152:155], v[48:51]
	v_mfma_f32_16x16x32_bf16 v[36:39], v[124:127], v[174:177], v[36:39]
	v_mfma_f32_16x16x32_bf16 v[32:35], v[144:147], v[174:177], v[32:35]
	v_mfma_f32_16x16x32_bf16 v[20:23], v[124:127], v[182:185], v[20:23]
	v_mfma_f32_16x16x32_bf16 v[16:19], v[144:147], v[182:185], v[16:19]
	v_mfma_f32_16x16x32_bf16 v[4:7], v[124:127], v[190:193], v[4:7]
	v_mfma_f32_16x16x32_bf16 v[0:3], v[144:147], v[190:193], v[0:3]
	v_mfma_f32_16x16x32_bf16 v[52:55], v[140:143], v[170:173], v[52:55]
	v_mfma_f32_16x16x32_bf16 v[48:51], v[148:151], v[170:173], v[48:51]
	v_mfma_f32_16x16x32_bf16 v[36:39], v[140:143], v[178:181], v[36:39]
	v_mfma_f32_16x16x32_bf16 v[32:35], v[148:151], v[178:181], v[32:35]
	v_mfma_f32_16x16x32_bf16 v[20:23], v[140:143], v[186:189], v[20:23]
	v_mfma_f32_16x16x32_bf16 v[16:19], v[148:151], v[186:189], v[16:19]
	v_mfma_f32_16x16x32_bf16 v[4:7], v[140:143], v[194:197], v[4:7]
	v_mfma_f32_16x16x32_bf16 v[0:3], v[148:151], v[194:197], v[0:3]
	s_setprio 0
	s_barrier
	s_add_i32 s52, s52, 2
	s_add_u32 s50, s50, 0x100
	s_addc_u32 s51, s51, 0
	s_mov_b64 s[8:9], s[10:11]
	s_branch .LBB0_927

.LBB0_927:
	v_add_u32_e32 v120, s23, v230
	v_add_u32_e32 v148, s26, v230
	ds_read_b128 v[88:91], v120
	ds_read_b128 v[100:103], v120 offset:1024
	ds_read_b128 v[112:115], v120 offset:2048
	ds_read_b128 v[120:123], v120 offset:3072
	ds_read_b128 v[124:127], v148
	ds_read_b128 v[140:143], v148 offset:1024
	ds_read_b128 v[144:147], v148 offset:2048
	ds_read_b128 v[148:151], v148 offset:3072
	s_add_u32 s10, s8, 0x100
	s_addc_u32 s11, s9, 0
	s_cmpk_eq_i32 s52, 0x54
	s_cselect_b32 s15, s5, s11
	s_cselect_b32 s14, s4, s10
	s_cselect_b32 s13, s7, s51
	s_cselect_b32 s12, s6, s50
	v_lshl_add_u64 v[206:207], s[8:9], 0, v[204:205]
	s_add_i32 m0, s29, 0xc000
	ds_read_b128 v[152:155], v232
	ds_read_b128 v[170:173], v232 offset:1024
	ds_read_b128 v[174:177], v232 offset:2048
	ds_read_b128 v[178:181], v232 offset:3072
	ds_read_b128 v[182:185], v232 offset:4096
	ds_read_b128 v[186:189], v232 offset:5120
	ds_read_b128 v[190:193], v232 offset:6144
	ds_read_b128 v[194:197], v232 offset:7168
	global_load_lds_dwordx4 v[206:207], off
	v_lshl_add_u64 v[206:207], s[8:9], 0, v[202:203]
	s_add_i32 m0, s29, 0xe000
	s_nop 0
	global_load_lds_dwordx4 v[206:207], off
	s_waitcnt vmcnt(8)
	s_waitcnt lgkmcnt(0)
	s_barrier
	s_setprio 1
	s_waitcnt lgkmcnt(0)
	s_nop 0
	v_mfma_f32_16x16x32_bf16 v[166:169], v[88:91], v[152:155], v[166:169]
	v_mfma_f32_16x16x32_bf16 v[156:159], v[112:115], v[152:155], v[156:159]
	v_mfma_f32_16x16x32_bf16 v[128:131], v[88:91], v[174:177], v[128:131]
	v_mfma_f32_16x16x32_bf16 v[116:119], v[112:115], v[174:177], v[116:119]
	v_mfma_f32_16x16x32_bf16 v[96:99], v[88:91], v[182:185], v[96:99]
	v_mfma_f32_16x16x32_bf16 v[92:95], v[112:115], v[182:185], v[92:95]
	v_mfma_f32_16x16x32_bf16 v[76:79], v[88:91], v[190:193], v[76:79]
	v_mfma_f32_16x16x32_bf16 v[72:75], v[112:115], v[190:193], v[72:75]
	v_mfma_f32_16x16x32_bf16 v[166:169], v[100:103], v[170:173], v[166:169]
	v_mfma_f32_16x16x32_bf16 v[156:159], v[120:123], v[170:173], v[156:159]
	v_mfma_f32_16x16x32_bf16 v[128:131], v[100:103], v[178:181], v[128:131]
	v_mfma_f32_16x16x32_bf16 v[116:119], v[120:123], v[178:181], v[116:119]
	v_mfma_f32_16x16x32_bf16 v[96:99], v[100:103], v[186:189], v[96:99]
	v_mfma_f32_16x16x32_bf16 v[92:95], v[120:123], v[186:189], v[92:95]
	v_mfma_f32_16x16x32_bf16 v[76:79], v[100:103], v[194:197], v[76:79]
	v_mfma_f32_16x16x32_bf16 v[72:75], v[120:123], v[194:197], v[72:75]
	s_setprio 0
	s_setprio 1
	v_mfma_f32_16x16x32_bf16 v[136:139], v[124:127], v[152:155], v[136:139]
	v_mfma_f32_16x16x32_bf16 v[132:135], v[144:147], v[152:155], v[132:135]
	v_mfma_f32_16x16x32_bf16 v[108:111], v[124:127], v[174:177], v[108:111]
	v_mfma_f32_16x16x32_bf16 v[104:107], v[144:147], v[174:177], v[104:107]
	v_mfma_f32_16x16x32_bf16 v[84:87], v[124:127], v[182:185], v[84:87]
	v_mfma_f32_16x16x32_bf16 v[80:83], v[144:147], v[182:185], v[80:83]
	v_mfma_f32_16x16x32_bf16 v[68:71], v[124:127], v[190:193], v[68:71]
	v_mfma_f32_16x16x32_bf16 v[64:67], v[144:147], v[190:193], v[64:67]
	v_mfma_f32_16x16x32_bf16 v[136:139], v[140:143], v[170:173], v[136:139]
	v_mfma_f32_16x16x32_bf16 v[132:135], v[148:151], v[170:173], v[132:135]
	v_mfma_f32_16x16x32_bf16 v[108:111], v[140:143], v[178:181], v[108:111]
	v_mfma_f32_16x16x32_bf16 v[104:107], v[148:151], v[178:181], v[104:107]
	v_mfma_f32_16x16x32_bf16 v[84:87], v[140:143], v[186:189], v[84:87]
	v_mfma_f32_16x16x32_bf16 v[80:83], v[148:151], v[186:189], v[80:83]
	v_mfma_f32_16x16x32_bf16 v[68:71], v[140:143], v[194:197], v[68:71]
	v_mfma_f32_16x16x32_bf16 v[64:67], v[148:151], v[194:197], v[64:67]
	s_setprio 0
	s_barrier
	s_mov_b32 m0, s24
	v_lshl_add_u64 v[206:207], s[12:13], 0, v[160:161]
	s_add_u32 s8, s12, 0x160000
	ds_read_b128 v[152:155], v232 offset:16384
	ds_read_b128 v[170:173], v232 offset:17408
	ds_read_b128 v[174:177], v232 offset:18432
	ds_read_b128 v[178:181], v232 offset:19456
	ds_read_b128 v[182:185], v232 offset:20480
	ds_read_b128 v[186:189], v232 offset:21504
	ds_read_b128 v[190:193], v232 offset:22528
	ds_read_b128 v[194:197], v232 offset:23552
	global_load_lds_dwordx4 v[206:207], off
	v_lshl_add_u64 v[208:209], s[12:13], 0, v[200:201]
	s_mov_b32 m0, s25
	s_addc_u32 s9, s13, 0
	global_load_lds_dwordx4 v[208:209], off
	v_lshl_add_u64 v[210:211], s[8:9], 0, v[160:161]
	s_mov_b32 m0, s27
	v_lshl_add_u64 v[212:213], s[14:15], 0, v[198:199]
	global_load_lds_dwordx4 v[210:211], off
	v_lshl_add_u64 v[210:211], s[8:9], 0, v[200:201]
	s_mov_b32 m0, s28
	s_nop 0
	global_load_lds_dwordx4 v[210:211], off
	v_lshl_add_u64 v[210:211], s[14:15], 0, v[162:163]
	s_mov_b32 m0, s29
	s_nop 0
	global_load_lds_dwordx4 v[210:211], off
	s_mov_b32 m0, s30
	s_nop 0
	global_load_lds_dwordx4 v[212:213], off
	s_waitcnt vmcnt(8)
	s_waitcnt lgkmcnt(0)
	s_barrier
	s_setprio 1
	s_waitcnt lgkmcnt(0)
	s_nop 0
	v_mfma_f32_16x16x32_bf16 v[60:63], v[88:91], v[152:155], v[60:63]
	v_mfma_f32_16x16x32_bf16 v[56:59], v[112:115], v[152:155], v[56:59]
	v_mfma_f32_16x16x32_bf16 v[44:47], v[88:91], v[174:177], v[44:47]
	v_mfma_f32_16x16x32_bf16 v[40:43], v[112:115], v[174:177], v[40:43]
	v_mfma_f32_16x16x32_bf16 v[28:31], v[88:91], v[182:185], v[28:31]
	v_mfma_f32_16x16x32_bf16 v[24:27], v[112:115], v[182:185], v[24:27]
	v_mfma_f32_16x16x32_bf16 v[12:15], v[88:91], v[190:193], v[12:15]
	v_mfma_f32_16x16x32_bf16 v[8:11], v[112:115], v[190:193], v[8:11]
	v_mfma_f32_16x16x32_bf16 v[60:63], v[100:103], v[170:173], v[60:63]
	v_mfma_f32_16x16x32_bf16 v[56:59], v[120:123], v[170:173], v[56:59]
	v_mfma_f32_16x16x32_bf16 v[44:47], v[100:103], v[178:181], v[44:47]
	v_mfma_f32_16x16x32_bf16 v[40:43], v[120:123], v[178:181], v[40:43]
	v_mfma_f32_16x16x32_bf16 v[28:31], v[100:103], v[186:189], v[28:31]
	v_mfma_f32_16x16x32_bf16 v[24:27], v[120:123], v[186:189], v[24:27]
	v_mfma_f32_16x16x32_bf16 v[12:15], v[100:103], v[194:197], v[12:15]
	v_mfma_f32_16x16x32_bf16 v[8:11], v[120:123], v[194:197], v[8:11]
	s_setprio 0
	s_setprio 1
	v_mfma_f32_16x16x32_bf16 v[52:55], v[124:127], v[152:155], v[52:55]
	v_mfma_f32_16x16x32_bf16 v[48:51], v[144:147], v[152:155], v[48:51]
	v_mfma_f32_16x16x32_bf16 v[36:39], v[124:127], v[174:177], v[36:39]
	v_mfma_f32_16x16x32_bf16 v[32:35], v[144:147], v[174:177], v[32:35]
	v_mfma_f32_16x16x32_bf16 v[20:23], v[124:127], v[182:185], v[20:23]
	v_mfma_f32_16x16x32_bf16 v[16:19], v[144:147], v[182:185], v[16:19]
	v_mfma_f32_16x16x32_bf16 v[4:7], v[124:127], v[190:193], v[4:7]
	v_mfma_f32_16x16x32_bf16 v[0:3], v[144:147], v[190:193], v[0:3]
	v_mfma_f32_16x16x32_bf16 v[52:55], v[140:143], v[170:173], v[52:55]
	v_mfma_f32_16x16x32_bf16 v[48:51], v[148:151], v[170:173], v[48:51]
	v_mfma_f32_16x16x32_bf16 v[36:39], v[140:143], v[178:181], v[36:39]
	v_mfma_f32_16x16x32_bf16 v[32:35], v[148:151], v[178:181], v[32:35]
	v_mfma_f32_16x16x32_bf16 v[20:23], v[140:143], v[186:189], v[20:23]
	v_mfma_f32_16x16x32_bf16 v[16:19], v[148:151], v[186:189], v[16:19]
	v_mfma_f32_16x16x32_bf16 v[4:7], v[140:143], v[194:197], v[4:7]
	v_mfma_f32_16x16x32_bf16 v[0:3], v[148:151], v[194:197], v[0:3]
	s_setprio 0
	s_barrier
	v_add_u32_e32 v120, s36, v230
	v_add_u32_e32 v148, s41, v230
	ds_read_b128 v[88:91], v120
	ds_read_b128 v[100:103], v120 offset:1024
	ds_read_b128 v[112:115], v120 offset:2048
	ds_read_b128 v[120:123], v120 offset:3072
	ds_read_b128 v[124:127], v148
	ds_read_b128 v[140:143], v148 offset:1024
	ds_read_b128 v[144:147], v148 offset:2048
	ds_read_b128 v[148:151], v148 offset:3072
	s_add_u32 s8, s14, 0x160000
	s_addc_u32 s9, s15, 0
	s_mov_b32 m0, s31
	v_lshl_add_u64 v[214:215], s[8:9], 0, v[162:163]
	ds_read_b128 v[152:155], v232 offset:32768
	ds_read_b128 v[170:173], v232 offset:33792
	ds_read_b128 v[174:177], v232 offset:34816
	ds_read_b128 v[178:181], v232 offset:35840
	ds_read_b128 v[182:185], v232 offset:36864
	ds_read_b128 v[186:189], v232 offset:37888
	ds_read_b128 v[190:193], v232 offset:38912
	ds_read_b128 v[194:197], v232 offset:39936
	global_load_lds_dwordx4 v[214:215], off
	v_lshl_add_u64 v[214:215], s[8:9], 0, v[198:199]
	s_mov_b32 m0, s34
	s_nop 0
	global_load_lds_dwordx4 v[214:215], off
	s_waitcnt vmcnt(8)
	s_waitcnt lgkmcnt(0)
	s_barrier
	s_setprio 1
	s_waitcnt lgkmcnt(0)
	s_nop 0
	v_mfma_f32_16x16x32_bf16 v[166:169], v[88:91], v[152:155], v[166:169]
	v_mfma_f32_16x16x32_bf16 v[156:159], v[112:115], v[152:155], v[156:159]
	v_mfma_f32_16x16x32_bf16 v[128:131], v[88:91], v[174:177], v[128:131]
	v_mfma_f32_16x16x32_bf16 v[116:119], v[112:115], v[174:177], v[116:119]
	v_mfma_f32_16x16x32_bf16 v[96:99], v[88:91], v[182:185], v[96:99]
	v_mfma_f32_16x16x32_bf16 v[92:95], v[112:115], v[182:185], v[92:95]
	v_mfma_f32_16x16x32_bf16 v[76:79], v[88:91], v[190:193], v[76:79]
	v_mfma_f32_16x16x32_bf16 v[72:75], v[112:115], v[190:193], v[72:75]
	v_mfma_f32_16x16x32_bf16 v[166:169], v[100:103], v[170:173], v[166:169]
	v_mfma_f32_16x16x32_bf16 v[156:159], v[120:123], v[170:173], v[156:159]
	v_mfma_f32_16x16x32_bf16 v[128:131], v[100:103], v[178:181], v[128:131]
	v_mfma_f32_16x16x32_bf16 v[116:119], v[120:123], v[178:181], v[116:119]
	v_mfma_f32_16x16x32_bf16 v[96:99], v[100:103], v[186:189], v[96:99]
	v_mfma_f32_16x16x32_bf16 v[92:95], v[120:123], v[186:189], v[92:95]
	v_mfma_f32_16x16x32_bf16 v[76:79], v[100:103], v[194:197], v[76:79]
	v_mfma_f32_16x16x32_bf16 v[72:75], v[120:123], v[194:197], v[72:75]
	s_setprio 0
	s_setprio 1
	v_mfma_f32_16x16x32_bf16 v[136:139], v[124:127], v[152:155], v[136:139]
	v_mfma_f32_16x16x32_bf16 v[132:135], v[144:147], v[152:155], v[132:135]
	v_mfma_f32_16x16x32_bf16 v[108:111], v[124:127], v[174:177], v[108:111]
	v_mfma_f32_16x16x32_bf16 v[104:107], v[144:147], v[174:177], v[104:107]
	v_mfma_f32_16x16x32_bf16 v[84:87], v[124:127], v[182:185], v[84:87]
	v_mfma_f32_16x16x32_bf16 v[80:83], v[144:147], v[182:185], v[80:83]
	v_mfma_f32_16x16x32_bf16 v[68:71], v[124:127], v[190:193], v[68:71]
	v_mfma_f32_16x16x32_bf16 v[64:67], v[144:147], v[190:193], v[64:67]
	v_mfma_f32_16x16x32_bf16 v[136:139], v[140:143], v[170:173], v[136:139]
	v_mfma_f32_16x16x32_bf16 v[132:135], v[148:151], v[170:173], v[132:135]
	v_mfma_f32_16x16x32_bf16 v[108:111], v[140:143], v[178:181], v[108:111]
	v_mfma_f32_16x16x32_bf16 v[104:107], v[148:151], v[178:181], v[104:107]
	v_mfma_f32_16x16x32_bf16 v[84:87], v[140:143], v[186:189], v[84:87]
	v_mfma_f32_16x16x32_bf16 v[80:83], v[148:151], v[186:189], v[80:83]
	v_mfma_f32_16x16x32_bf16 v[68:71], v[140:143], v[194:197], v[68:71]
	v_mfma_f32_16x16x32_bf16 v[64:67], v[148:151], v[194:197], v[64:67]
	s_setprio 0
	s_barrier
	s_mov_b32 m0, s37
	v_lshl_add_u64 v[206:207], v[206:207], 0, s[86:87]
	s_add_u32 s8, s12, 0x160080
	ds_read_b128 v[152:155], v232 offset:49152
	ds_read_b128 v[170:173], v232 offset:50176
	ds_read_b128 v[174:177], v232 offset:51200
	ds_read_b128 v[178:181], v232 offset:52224
	ds_read_b128 v[182:185], v232 offset:53248
	ds_read_b128 v[186:189], v232 offset:54272
	ds_read_b128 v[190:193], v232 offset:55296
	ds_read_b128 v[194:197], v232 offset:56320
	global_load_lds_dwordx4 v[206:207], off
	v_lshl_add_u64 v[206:207], v[208:209], 0, s[86:87]
	s_mov_b32 m0, s38
	s_addc_u32 s9, s13, 0
	global_load_lds_dwordx4 v[206:207], off
	v_lshl_add_u64 v[206:207], s[8:9], 0, v[160:161]
	s_mov_b32 m0, s42
	s_nop 0
	global_load_lds_dwordx4 v[206:207], off
	v_lshl_add_u64 v[206:207], s[8:9], 0, v[200:201]
	s_mov_b32 m0, s43
	s_nop 0
	global_load_lds_dwordx4 v[206:207], off
	v_lshl_add_u64 v[206:207], v[210:211], 0, s[86:87]
	s_mov_b32 m0, s39
	s_nop 0
	global_load_lds_dwordx4 v[206:207], off
	v_lshl_add_u64 v[206:207], v[212:213], 0, s[86:87]
	s_mov_b32 m0, s40
	s_nop 0
	global_load_lds_dwordx4 v[206:207], off
	s_waitcnt vmcnt(8)
	s_waitcnt lgkmcnt(0)
	s_barrier
	s_setprio 1
	s_waitcnt lgkmcnt(0)
	v_mfma_f32_16x16x32_bf16 v[60:63], v[88:91], v[152:155], v[60:63]
	v_mfma_f32_16x16x32_bf16 v[56:59], v[112:115], v[152:155], v[56:59]
	v_mfma_f32_16x16x32_bf16 v[44:47], v[88:91], v[174:177], v[44:47]
	v_mfma_f32_16x16x32_bf16 v[40:43], v[112:115], v[174:177], v[40:43]
	v_mfma_f32_16x16x32_bf16 v[28:31], v[88:91], v[182:185], v[28:31]
	v_mfma_f32_16x16x32_bf16 v[24:27], v[112:115], v[182:185], v[24:27]
	v_mfma_f32_16x16x32_bf16 v[12:15], v[88:91], v[190:193], v[12:15]
	v_mfma_f32_16x16x32_bf16 v[8:11], v[112:115], v[190:193], v[8:11]
	v_mfma_f32_16x16x32_bf16 v[60:63], v[100:103], v[170:173], v[60:63]
	v_mfma_f32_16x16x32_bf16 v[56:59], v[120:123], v[170:173], v[56:59]
	v_mfma_f32_16x16x32_bf16 v[44:47], v[100:103], v[178:181], v[44:47]
	v_mfma_f32_16x16x32_bf16 v[40:43], v[120:123], v[178:181], v[40:43]
	v_mfma_f32_16x16x32_bf16 v[28:31], v[100:103], v[186:189], v[28:31]
	v_mfma_f32_16x16x32_bf16 v[24:27], v[120:123], v[186:189], v[24:27]
	v_mfma_f32_16x16x32_bf16 v[12:15], v[100:103], v[194:197], v[12:15]
	v_mfma_f32_16x16x32_bf16 v[8:11], v[120:123], v[194:197], v[8:11]
	s_setprio 0
	s_setprio 1
	v_mfma_f32_16x16x32_bf16 v[52:55], v[124:127], v[152:155], v[52:55]
	v_mfma_f32_16x16x32_bf16 v[48:51], v[144:147], v[152:155], v[48:51]
	v_mfma_f32_16x16x32_bf16 v[36:39], v[124:127], v[174:177], v[36:39]
	v_mfma_f32_16x16x32_bf16 v[32:35], v[144:147], v[174:177], v[32:35]
	v_mfma_f32_16x16x32_bf16 v[20:23], v[124:127], v[182:185], v[20:23]
	v_mfma_f32_16x16x32_bf16 v[16:19], v[144:147], v[182:185], v[16:19]
	v_mfma_f32_16x16x32_bf16 v[4:7], v[124:127], v[190:193], v[4:7]
	v_mfma_f32_16x16x32_bf16 v[0:3], v[144:147], v[190:193], v[0:3]
	v_mfma_f32_16x16x32_bf16 v[52:55], v[140:143], v[170:173], v[52:55]
	v_mfma_f32_16x16x32_bf16 v[48:51], v[148:151], v[170:173], v[48:51]
	v_mfma_f32_16x16x32_bf16 v[36:39], v[140:143], v[178:181], v[36:39]
	v_mfma_f32_16x16x32_bf16 v[32:35], v[148:151], v[178:181], v[32:35]
	v_mfma_f32_16x16x32_bf16 v[20:23], v[140:143], v[186:189], v[20:23]
	v_mfma_f32_16x16x32_bf16 v[16:19], v[148:151], v[186:189], v[16:19]
	v_mfma_f32_16x16x32_bf16 v[4:7], v[140:143], v[194:197], v[4:7]
	v_mfma_f32_16x16x32_bf16 v[0:3], v[148:151], v[194:197], v[0:3]
	s_setprio 0
	s_barrier
	s_add_i32 s52, s52, 2
	s_add_u32 s50, s50, 0x100
	s_addc_u32 s51, s51, 0
	s_cmpk_gt_u32 s52, 0x55
	s_mov_b64 s[8:9], s[10:11]
	s_cbranch_scc0 .LBB0_927
	v_lshl_or_b32 v90, s49, 8, v231
	v_lshl_add_u32 v88, s48, 8, v165
	v_ashrrev_i32_e32 v91, 31, v90
	v_lshlrev_b64 v[206:207], 1, v[90:91]
	v_ashrrev_i32_e32 v89, 31, v88
	v_lshl_add_u64 v[90:91], s[0:1], 0, v[206:207]
	v_lshlrev_b64 v[222:223], 12, v[88:89]
	v_lshl_add_u64 v[100:101], v[90:91], 0, v[222:223]
	global_load_dwordx4 v[194:197], v[100:101], off nt
	global_load_dwordx4 v[190:193], v[100:101], off offset:256 nt
	v_or_b32_e32 v100, 16, v88
	v_ashrrev_i32_e32 v101, 31, v100
	v_lshlrev_b64 v[220:221], 12, v[100:101]
	v_lshl_add_u64 v[100:101], v[90:91], 0, v[220:221]
	global_load_dwordx4 v[186:189], v[100:101], off nt
	global_load_dwordx4 v[182:185], v[100:101], off offset:256 nt
	v_or_b32_e32 v100, 32, v88
	v_ashrrev_i32_e32 v101, 31, v100
	v_lshlrev_b64 v[218:219], 12, v[100:101]
	v_lshl_add_u64 v[100:101], v[90:91], 0, v[218:219]
	global_load_dwordx4 v[178:181], v[100:101], off nt
	global_load_dwordx4 v[174:177], v[100:101], off offset:256 nt
	v_or_b32_e32 v88, 48, v88
	v_ashrrev_i32_e32 v89, 31, v88
	v_lshlrev_b64 v[216:217], 12, v[88:89]
	v_lshl_add_u64 v[88:89], v[90:91], 0, v[216:217]
	global_load_dwordx4 v[170:173], v[88:89], off nt
	global_load_dwordx4 v[152:155], v[88:89], off offset:256 nt
	v_lshl_add_u64 v[214:215], v[222:223], 0, s[54:55]
	v_lshl_add_u64 v[88:89], v[90:91], 0, v[214:215]
	global_load_dwordx4 v[148:151], v[88:89], off nt
	global_load_dwordx4 v[144:147], v[88:89], off offset:256 nt
	s_mov_b64 s[8:9], 0x90000
	v_lshl_add_u64 v[212:213], v[222:223], 0, s[8:9]
	v_lshl_add_u64 v[88:89], v[90:91], 0, v[212:213]
	global_load_dwordx4 v[140:143], v[88:89], off nt
	global_load_dwordx4 v[124:127], v[88:89], off offset:256 nt
	s_mov_b64 s[8:9], 0xa0000
	v_lshl_add_u64 v[210:211], v[222:223], 0, s[8:9]
	v_lshl_add_u64 v[88:89], v[90:91], 0, v[210:211]
	global_load_dwordx4 v[120:123], v[88:89], off nt
	global_load_dwordx4 v[112:115], v[88:89], off offset:256 nt
	s_mov_b64 s[8:9], 0xb0000
	v_lshl_add_u64 v[208:209], v[222:223], 0, s[8:9]
	v_lshl_add_u64 v[88:89], v[90:91], 0, v[208:209]
	global_load_dwordx4 v[100:103], v[88:89], off nt
	s_nop 0
	global_load_dwordx4 v[88:91], v[88:89], off offset:256 nt
	s_and_b64 vcc, exec, s[2:3]
	s_mov_b32 s49, s46
	s_mov_b32 s48, s47
	s_mov_b64 s[10:11], s[6:7]
	s_mov_b64 s[8:9], s[4:5]
	s_waitcnt vmcnt(0)
	v_cvt_f32_f16_e32 v224, v194
	v_cvt_f32_f16_sdwa v225, v194 dst_sel:DWORD dst_unused:UNUSED_PAD src0_sel:WORD_1
	v_pk_add_f32 v[166:167], v[166:167], v[224:225]
	s_nop 0
	v_cvt_pk_f16_f32 v194, v166, v167
	v_cvt_f32_f16_e32 v166, v196
	v_cvt_f32_f16_sdwa v167, v196 dst_sel:DWORD dst_unused:UNUSED_PAD src0_sel:WORD_1
	v_pk_add_f32 v[156:157], v[156:157], v[166:167]
	s_nop 0
	v_cvt_pk_f16_f32 v196, v156, v157
	v_cvt_f32_f16_e32 v156, v195
	v_cvt_f32_f16_sdwa v157, v195 dst_sel:DWORD dst_unused:UNUSED_PAD src0_sel:WORD_1
	v_pk_add_f32 v[156:157], v[168:169], v[156:157]
	s_nop 0
	v_cvt_pk_f16_f32 v195, v156, v157
	v_cvt_f32_f16_e32 v156, v197
	v_cvt_f32_f16_sdwa v157, v197 dst_sel:DWORD dst_unused:UNUSED_PAD src0_sel:WORD_1
	v_pk_add_f32 v[156:157], v[158:159], v[156:157]
	s_nop 0
	v_cvt_pk_f16_f32 v197, v156, v157
	v_lshl_add_u64 v[156:157], s[0:1], 0, v[222:223]
	v_lshl_add_u64 v[166:167], v[156:157], 0, v[206:207]
	v_cvt_f32_f16_e32 v156, v190
	v_cvt_f32_f16_sdwa v157, v190 dst_sel:DWORD dst_unused:UNUSED_PAD src0_sel:WORD_1
	global_store_dwordx4 v[166:167], v[194:197], off
	v_pk_add_f32 v[136:137], v[136:137], v[156:157]
	s_nop 0
	v_cvt_pk_f16_f32 v156, v136, v137
	v_cvt_f32_f16_e32 v136, v192
	v_cvt_f32_f16_sdwa v137, v192 dst_sel:DWORD dst_unused:UNUSED_PAD src0_sel:WORD_1
	v_pk_add_f32 v[132:133], v[132:133], v[136:137]
	s_nop 0
	v_cvt_pk_f16_f32 v158, v132, v133
	v_cvt_f32_f16_e32 v132, v191
	v_cvt_f32_f16_sdwa v133, v191 dst_sel:DWORD dst_unused:UNUSED_PAD src0_sel:WORD_1
	v_pk_add_f32 v[132:133], v[138:139], v[132:133]
	s_nop 0
	v_cvt_pk_f16_f32 v157, v132, v133
	v_cvt_f32_f16_e32 v132, v193
	v_cvt_f32_f16_sdwa v133, v193 dst_sel:DWORD dst_unused:UNUSED_PAD src0_sel:WORD_1
	v_pk_add_f32 v[132:133], v[134:135], v[132:133]
	s_nop 0
	v_cvt_pk_f16_f32 v159, v132, v133
	v_cvt_f32_f16_e32 v132, v186
	v_cvt_f32_f16_sdwa v133, v186 dst_sel:DWORD dst_unused:UNUSED_PAD src0_sel:WORD_1
	global_store_dwordx4 v[166:167], v[156:159], off offset:256
	v_pk_add_f32 v[128:129], v[128:129], v[132:133]
	s_nop 0
	v_cvt_pk_f16_f32 v132, v128, v129
	v_cvt_f32_f16_e32 v128, v188
	v_cvt_f32_f16_sdwa v129, v188 dst_sel:DWORD dst_unused:UNUSED_PAD src0_sel:WORD_1
	v_pk_add_f32 v[116:117], v[116:117], v[128:129]
	s_nop 0
	v_cvt_pk_f16_f32 v134, v116, v117
	v_cvt_f32_f16_e32 v116, v187
	v_cvt_f32_f16_sdwa v117, v187 dst_sel:DWORD dst_unused:UNUSED_PAD src0_sel:WORD_1
	v_pk_add_f32 v[116:117], v[130:131], v[116:117]
	s_nop 0
	v_cvt_pk_f16_f32 v133, v116, v117
	v_cvt_f32_f16_e32 v116, v189
	v_cvt_f32_f16_sdwa v117, v189 dst_sel:DWORD dst_unused:UNUSED_PAD src0_sel:WORD_1
	v_pk_add_f32 v[116:117], v[118:119], v[116:117]
	s_nop 0
	v_cvt_pk_f16_f32 v135, v116, v117
	v_lshl_add_u64 v[116:117], s[0:1], 0, v[220:221]
	v_lshl_add_u64 v[128:129], v[116:117], 0, v[206:207]
	v_cvt_f32_f16_e32 v116, v182
	v_cvt_f32_f16_sdwa v117, v182 dst_sel:DWORD dst_unused:UNUSED_PAD src0_sel:WORD_1
	global_store_dwordx4 v[128:129], v[132:135], off
	v_pk_add_f32 v[108:109], v[108:109], v[116:117]
	s_nop 0
	v_cvt_pk_f16_f32 v116, v108, v109
	v_cvt_f32_f16_e32 v108, v184
	v_cvt_f32_f16_sdwa v109, v184 dst_sel:DWORD dst_unused:UNUSED_PAD src0_sel:WORD_1
	v_pk_add_f32 v[104:105], v[104:105], v[108:109]
	s_nop 0
	v_cvt_pk_f16_f32 v118, v104, v105
	v_cvt_f32_f16_e32 v104, v183
	v_cvt_f32_f16_sdwa v105, v183 dst_sel:DWORD dst_unused:UNUSED_PAD src0_sel:WORD_1
	v_pk_add_f32 v[104:105], v[110:111], v[104:105]
	s_nop 0
	v_cvt_pk_f16_f32 v117, v104, v105
	v_cvt_f32_f16_e32 v104, v185
	v_cvt_f32_f16_sdwa v105, v185 dst_sel:DWORD dst_unused:UNUSED_PAD src0_sel:WORD_1
	v_pk_add_f32 v[104:105], v[106:107], v[104:105]
	s_nop 0
	v_cvt_pk_f16_f32 v119, v104, v105
	v_cvt_f32_f16_e32 v104, v178
	v_cvt_f32_f16_sdwa v105, v178 dst_sel:DWORD dst_unused:UNUSED_PAD src0_sel:WORD_1
	global_store_dwordx4 v[128:129], v[116:119], off offset:256
	v_pk_add_f32 v[96:97], v[96:97], v[104:105]
	s_nop 0
	v_cvt_pk_f16_f32 v104, v96, v97
	v_cvt_f32_f16_e32 v96, v180
	v_cvt_f32_f16_sdwa v97, v180 dst_sel:DWORD dst_unused:UNUSED_PAD src0_sel:WORD_1
	v_pk_add_f32 v[92:93], v[92:93], v[96:97]
	s_nop 0
	v_cvt_pk_f16_f32 v106, v92, v93
	v_cvt_f32_f16_e32 v92, v179
	v_cvt_f32_f16_sdwa v93, v179 dst_sel:DWORD dst_unused:UNUSED_PAD src0_sel:WORD_1
	v_pk_add_f32 v[92:93], v[98:99], v[92:93]
	s_nop 0
	v_cvt_pk_f16_f32 v105, v92, v93
	v_cvt_f32_f16_e32 v92, v181
	v_cvt_f32_f16_sdwa v93, v181 dst_sel:DWORD dst_unused:UNUSED_PAD src0_sel:WORD_1
	v_pk_add_f32 v[92:93], v[94:95], v[92:93]
	s_nop 0
	v_cvt_pk_f16_f32 v107, v92, v93
	v_lshl_add_u64 v[92:93], s[0:1], 0, v[218:219]
	v_lshl_add_u64 v[96:97], v[92:93], 0, v[206:207]
	v_cvt_f32_f16_e32 v92, v174
	v_cvt_f32_f16_sdwa v93, v174 dst_sel:DWORD dst_unused:UNUSED_PAD src0_sel:WORD_1
	global_store_dwordx4 v[96:97], v[104:107], off
	v_pk_add_f32 v[84:85], v[84:85], v[92:93]
	s_nop 0
	v_cvt_pk_f16_f32 v92, v84, v85
	v_cvt_f32_f16_e32 v84, v176
	v_cvt_f32_f16_sdwa v85, v176 dst_sel:DWORD dst_unused:UNUSED_PAD src0_sel:WORD_1
	v_pk_add_f32 v[80:81], v[80:81], v[84:85]
	s_nop 0
	v_cvt_pk_f16_f32 v94, v80, v81
	v_cvt_f32_f16_e32 v80, v175
	v_cvt_f32_f16_sdwa v81, v175 dst_sel:DWORD dst_unused:UNUSED_PAD src0_sel:WORD_1
	v_pk_add_f32 v[80:81], v[86:87], v[80:81]
	s_nop 0
	v_cvt_pk_f16_f32 v93, v80, v81
	v_cvt_f32_f16_e32 v80, v177
	v_cvt_f32_f16_sdwa v81, v177 dst_sel:DWORD dst_unused:UNUSED_PAD src0_sel:WORD_1
	v_pk_add_f32 v[80:81], v[82:83], v[80:81]
	s_nop 0
	v_cvt_pk_f16_f32 v95, v80, v81
	v_cvt_f32_f16_e32 v80, v170
	v_cvt_f32_f16_sdwa v81, v170 dst_sel:DWORD dst_unused:UNUSED_PAD src0_sel:WORD_1
	global_store_dwordx4 v[96:97], v[92:95], off offset:256
	v_pk_add_f32 v[76:77], v[76:77], v[80:81]
	s_nop 0
	v_cvt_pk_f16_f32 v80, v76, v77
	v_cvt_f32_f16_e32 v76, v172
	v_cvt_f32_f16_sdwa v77, v172 dst_sel:DWORD dst_unused:UNUSED_PAD src0_sel:WORD_1
	v_pk_add_f32 v[72:73], v[72:73], v[76:77]
	s_nop 0
	v_cvt_pk_f16_f32 v82, v72, v73
	v_cvt_f32_f16_e32 v72, v171
	v_cvt_f32_f16_sdwa v73, v171 dst_sel:DWORD dst_unused:UNUSED_PAD src0_sel:WORD_1
	v_pk_add_f32 v[72:73], v[78:79], v[72:73]
	s_nop 0
	v_cvt_pk_f16_f32 v81, v72, v73
	v_cvt_f32_f16_e32 v72, v173
	v_cvt_f32_f16_sdwa v73, v173 dst_sel:DWORD dst_unused:UNUSED_PAD src0_sel:WORD_1
	v_pk_add_f32 v[72:73], v[74:75], v[72:73]
	s_nop 0
	v_cvt_pk_f16_f32 v83, v72, v73
	v_lshl_add_u64 v[72:73], s[0:1], 0, v[216:217]
	v_lshl_add_u64 v[76:77], v[72:73], 0, v[206:207]
	v_cvt_f32_f16_e32 v72, v152
	v_cvt_f32_f16_sdwa v73, v152 dst_sel:DWORD dst_unused:UNUSED_PAD src0_sel:WORD_1
	global_store_dwordx4 v[76:77], v[80:83], off
	v_pk_add_f32 v[68:69], v[68:69], v[72:73]
	s_nop 0
	v_cvt_pk_f16_f32 v72, v68, v69
	v_cvt_f32_f16_e32 v68, v154
	v_cvt_f32_f16_sdwa v69, v154 dst_sel:DWORD dst_unused:UNUSED_PAD src0_sel:WORD_1
	v_pk_add_f32 v[64:65], v[64:65], v[68:69]
	s_nop 0
	v_cvt_pk_f16_f32 v74, v64, v65
	v_cvt_f32_f16_e32 v64, v153
	v_cvt_f32_f16_sdwa v65, v153 dst_sel:DWORD dst_unused:UNUSED_PAD src0_sel:WORD_1
	v_pk_add_f32 v[64:65], v[70:71], v[64:65]
	s_nop 0
	v_cvt_pk_f16_f32 v73, v64, v65
	v_cvt_f32_f16_e32 v64, v155
	v_cvt_f32_f16_sdwa v65, v155 dst_sel:DWORD dst_unused:UNUSED_PAD src0_sel:WORD_1
	v_pk_add_f32 v[64:65], v[66:67], v[64:65]
	s_nop 0
	v_cvt_pk_f16_f32 v75, v64, v65
	v_cvt_f32_f16_e32 v64, v148
	v_cvt_f32_f16_sdwa v65, v148 dst_sel:DWORD dst_unused:UNUSED_PAD src0_sel:WORD_1
	global_store_dwordx4 v[76:77], v[72:75], off offset:256
	v_pk_add_f32 v[60:61], v[60:61], v[64:65]
	s_nop 0
	v_cvt_pk_f16_f32 v64, v60, v61
	v_cvt_f32_f16_e32 v60, v150
	v_cvt_f32_f16_sdwa v61, v150 dst_sel:DWORD dst_unused:UNUSED_PAD src0_sel:WORD_1
	v_pk_add_f32 v[56:57], v[56:57], v[60:61]
	s_nop 0
	v_cvt_pk_f16_f32 v66, v56, v57
	v_cvt_f32_f16_e32 v56, v149
	v_cvt_f32_f16_sdwa v57, v149 dst_sel:DWORD dst_unused:UNUSED_PAD src0_sel:WORD_1
	v_pk_add_f32 v[56:57], v[62:63], v[56:57]
	s_nop 0
	v_cvt_pk_f16_f32 v65, v56, v57
	v_cvt_f32_f16_e32 v56, v151
	v_cvt_f32_f16_sdwa v57, v151 dst_sel:DWORD dst_unused:UNUSED_PAD src0_sel:WORD_1
	v_pk_add_f32 v[56:57], v[58:59], v[56:57]
	s_nop 0
	v_cvt_pk_f16_f32 v67, v56, v57
	v_lshl_add_u64 v[56:57], s[0:1], 0, v[214:215]
	v_lshl_add_u64 v[60:61], v[56:57], 0, v[206:207]
	v_cvt_f32_f16_e32 v56, v144
	v_cvt_f32_f16_sdwa v57, v144 dst_sel:DWORD dst_unused:UNUSED_PAD src0_sel:WORD_1
	global_store_dwordx4 v[60:61], v[64:67], off
	v_pk_add_f32 v[52:53], v[52:53], v[56:57]
	s_nop 0
	v_cvt_pk_f16_f32 v56, v52, v53
	v_cvt_f32_f16_e32 v52, v146
	v_cvt_f32_f16_sdwa v53, v146 dst_sel:DWORD dst_unused:UNUSED_PAD src0_sel:WORD_1
	v_pk_add_f32 v[48:49], v[48:49], v[52:53]
	s_nop 0
	v_cvt_pk_f16_f32 v58, v48, v49
	v_cvt_f32_f16_e32 v48, v145
	v_cvt_f32_f16_sdwa v49, v145 dst_sel:DWORD dst_unused:UNUSED_PAD src0_sel:WORD_1
	v_pk_add_f32 v[48:49], v[54:55], v[48:49]
	s_nop 0
	v_cvt_pk_f16_f32 v57, v48, v49
	v_cvt_f32_f16_e32 v48, v147
	v_cvt_f32_f16_sdwa v49, v147 dst_sel:DWORD dst_unused:UNUSED_PAD src0_sel:WORD_1
	v_pk_add_f32 v[48:49], v[50:51], v[48:49]
	s_nop 0
	v_cvt_pk_f16_f32 v59, v48, v49
	v_cvt_f32_f16_e32 v48, v140
	v_cvt_f32_f16_sdwa v49, v140 dst_sel:DWORD dst_unused:UNUSED_PAD src0_sel:WORD_1
	global_store_dwordx4 v[60:61], v[56:59], off offset:256
	v_pk_add_f32 v[44:45], v[44:45], v[48:49]
	s_nop 0
	v_cvt_pk_f16_f32 v48, v44, v45
	v_cvt_f32_f16_e32 v44, v142
	v_cvt_f32_f16_sdwa v45, v142 dst_sel:DWORD dst_unused:UNUSED_PAD src0_sel:WORD_1
	v_pk_add_f32 v[40:41], v[40:41], v[44:45]
	s_nop 0
	v_cvt_pk_f16_f32 v50, v40, v41
	v_cvt_f32_f16_e32 v40, v141
	v_cvt_f32_f16_sdwa v41, v141 dst_sel:DWORD dst_unused:UNUSED_PAD src0_sel:WORD_1
	v_pk_add_f32 v[40:41], v[46:47], v[40:41]
	s_nop 0
	v_cvt_pk_f16_f32 v49, v40, v41
	v_cvt_f32_f16_e32 v40, v143
	v_cvt_f32_f16_sdwa v41, v143 dst_sel:DWORD dst_unused:UNUSED_PAD src0_sel:WORD_1
	v_pk_add_f32 v[40:41], v[42:43], v[40:41]
	s_nop 0
	v_cvt_pk_f16_f32 v51, v40, v41
	v_lshl_add_u64 v[40:41], s[0:1], 0, v[212:213]
	v_lshl_add_u64 v[44:45], v[40:41], 0, v[206:207]
	v_cvt_f32_f16_e32 v40, v124
	v_cvt_f32_f16_sdwa v41, v124 dst_sel:DWORD dst_unused:UNUSED_PAD src0_sel:WORD_1
	global_store_dwordx4 v[44:45], v[48:51], off
	v_pk_add_f32 v[36:37], v[36:37], v[40:41]
	s_nop 0
	v_cvt_pk_f16_f32 v40, v36, v37
	v_cvt_f32_f16_e32 v36, v126
	v_cvt_f32_f16_sdwa v37, v126 dst_sel:DWORD dst_unused:UNUSED_PAD src0_sel:WORD_1
	v_pk_add_f32 v[32:33], v[32:33], v[36:37]
	s_nop 0
	v_cvt_pk_f16_f32 v42, v32, v33
	v_cvt_f32_f16_e32 v32, v125
	v_cvt_f32_f16_sdwa v33, v125 dst_sel:DWORD dst_unused:UNUSED_PAD src0_sel:WORD_1
	v_pk_add_f32 v[32:33], v[38:39], v[32:33]
	s_nop 0
	v_cvt_pk_f16_f32 v41, v32, v33
	v_cvt_f32_f16_e32 v32, v127
	v_cvt_f32_f16_sdwa v33, v127 dst_sel:DWORD dst_unused:UNUSED_PAD src0_sel:WORD_1
	v_pk_add_f32 v[32:33], v[34:35], v[32:33]
	s_nop 0
	v_cvt_pk_f16_f32 v43, v32, v33
	v_cvt_f32_f16_e32 v32, v120
	v_cvt_f32_f16_sdwa v33, v120 dst_sel:DWORD dst_unused:UNUSED_PAD src0_sel:WORD_1
	global_store_dwordx4 v[44:45], v[40:43], off offset:256
	v_pk_add_f32 v[28:29], v[28:29], v[32:33]
	s_nop 0
	v_cvt_pk_f16_f32 v32, v28, v29
	v_cvt_f32_f16_e32 v28, v122
	v_cvt_f32_f16_sdwa v29, v122 dst_sel:DWORD dst_unused:UNUSED_PAD src0_sel:WORD_1
	v_pk_add_f32 v[24:25], v[24:25], v[28:29]
	s_nop 0
	v_cvt_pk_f16_f32 v34, v24, v25
	v_cvt_f32_f16_e32 v24, v121
	v_cvt_f32_f16_sdwa v25, v121 dst_sel:DWORD dst_unused:UNUSED_PAD src0_sel:WORD_1
	v_pk_add_f32 v[24:25], v[30:31], v[24:25]
	s_nop 0
	v_cvt_pk_f16_f32 v33, v24, v25
	v_cvt_f32_f16_e32 v24, v123
	v_cvt_f32_f16_sdwa v25, v123 dst_sel:DWORD dst_unused:UNUSED_PAD src0_sel:WORD_1
	v_pk_add_f32 v[24:25], v[26:27], v[24:25]
	s_nop 0
	v_cvt_pk_f16_f32 v35, v24, v25
	v_lshl_add_u64 v[24:25], s[0:1], 0, v[210:211]
	v_lshl_add_u64 v[28:29], v[24:25], 0, v[206:207]
	v_cvt_f32_f16_e32 v24, v112
	v_cvt_f32_f16_sdwa v25, v112 dst_sel:DWORD dst_unused:UNUSED_PAD src0_sel:WORD_1
	global_store_dwordx4 v[28:29], v[32:35], off
	v_pk_add_f32 v[20:21], v[20:21], v[24:25]
	s_nop 0
	v_cvt_pk_f16_f32 v24, v20, v21
	v_cvt_f32_f16_e32 v20, v114
	v_cvt_f32_f16_sdwa v21, v114 dst_sel:DWORD dst_unused:UNUSED_PAD src0_sel:WORD_1
	v_pk_add_f32 v[16:17], v[16:17], v[20:21]
	s_nop 0
	v_cvt_pk_f16_f32 v26, v16, v17
	v_cvt_f32_f16_e32 v16, v113
	v_cvt_f32_f16_sdwa v17, v113 dst_sel:DWORD dst_unused:UNUSED_PAD src0_sel:WORD_1
	v_pk_add_f32 v[16:17], v[22:23], v[16:17]
	s_nop 0
	v_cvt_pk_f16_f32 v25, v16, v17
	v_cvt_f32_f16_e32 v16, v115
	v_cvt_f32_f16_sdwa v17, v115 dst_sel:DWORD dst_unused:UNUSED_PAD src0_sel:WORD_1
	v_pk_add_f32 v[16:17], v[18:19], v[16:17]
	s_nop 0
	v_cvt_pk_f16_f32 v27, v16, v17
	v_cvt_f32_f16_e32 v16, v100
	v_cvt_f32_f16_sdwa v17, v100 dst_sel:DWORD dst_unused:UNUSED_PAD src0_sel:WORD_1
	global_store_dwordx4 v[28:29], v[24:27], off offset:256
	v_pk_add_f32 v[12:13], v[12:13], v[16:17]
	s_nop 0
	v_cvt_pk_f16_f32 v16, v12, v13
	v_cvt_f32_f16_e32 v12, v102
	v_cvt_f32_f16_sdwa v13, v102 dst_sel:DWORD dst_unused:UNUSED_PAD src0_sel:WORD_1
	v_pk_add_f32 v[8:9], v[8:9], v[12:13]
	s_nop 0
	v_cvt_pk_f16_f32 v18, v8, v9
	v_cvt_f32_f16_e32 v8, v101
	v_cvt_f32_f16_sdwa v9, v101 dst_sel:DWORD dst_unused:UNUSED_PAD src0_sel:WORD_1
	v_pk_add_f32 v[8:9], v[14:15], v[8:9]
	s_nop 0
	v_cvt_pk_f16_f32 v17, v8, v9
	v_cvt_f32_f16_e32 v8, v103
	v_cvt_f32_f16_sdwa v9, v103 dst_sel:DWORD dst_unused:UNUSED_PAD src0_sel:WORD_1
	v_pk_add_f32 v[8:9], v[10:11], v[8:9]
	s_nop 0
	v_cvt_pk_f16_f32 v19, v8, v9
	v_lshl_add_u64 v[8:9], s[0:1], 0, v[208:209]
	v_lshl_add_u64 v[12:13], v[8:9], 0, v[206:207]
	v_cvt_f32_f16_e32 v8, v88
	v_cvt_f32_f16_sdwa v9, v88 dst_sel:DWORD dst_unused:UNUSED_PAD src0_sel:WORD_1
	global_store_dwordx4 v[12:13], v[16:19], off
	v_pk_add_f32 v[4:5], v[4:5], v[8:9]
	s_nop 0
	v_cvt_pk_f16_f32 v8, v4, v5
	v_cvt_f32_f16_e32 v4, v90
	v_cvt_f32_f16_sdwa v5, v90 dst_sel:DWORD dst_unused:UNUSED_PAD src0_sel:WORD_1
	v_pk_add_f32 v[0:1], v[0:1], v[4:5]
	s_nop 0
	v_cvt_pk_f16_f32 v10, v0, v1
	v_cvt_f32_f16_e32 v0, v89
	v_cvt_f32_f16_sdwa v1, v89 dst_sel:DWORD dst_unused:UNUSED_PAD src0_sel:WORD_1
	v_pk_add_f32 v[0:1], v[6:7], v[0:1]
	s_nop 0
	v_cvt_pk_f16_f32 v9, v0, v1
	v_cvt_f32_f16_e32 v0, v91
	v_cvt_f32_f16_sdwa v1, v91 dst_sel:DWORD dst_unused:UNUSED_PAD src0_sel:WORD_1
	v_pk_add_f32 v[0:1], v[2:3], v[0:1]
	s_nop 0
	v_cvt_pk_f16_f32 v11, v0, v1
	global_store_dwordx4 v[12:13], v[8:11], off offset:256
	s_cbranch_vccz .LBB0_916
	s_waitcnt vmcnt(0)
	s_cmpk_gt_u32 s17, 0xff
	s_cbranch_scc1 .LBB0_931
	s_barrier
